# v38 + loop back-edge scalar work (counter updates, compare) moved before the end-of-tile barrier
# baseline (speedup 1.0000x reference)
; #define G_DMA_A(kt, AO) do { G_DMA1(kt, AO, 0); G_DMA1(kt, AO, 1); G_DMA1(kt, AO, 2); G_DMA1(kt, AO, 3); if (MF == 9) G_DMA5(kt, AO); } while (0)
; #define G_ISSUE_B(kt) do { const unsigned _sb = (unsigned)(kt) * 4u * kstepB; \
;         _Pragma("unroll") for (int _i = 0; _i < 8; ++_i) sb[_i] = bload16(_i < 4 ? rsB0 : rsB1, vob, _sb + (_i & 3) * kstepB); } while (0)
; #define G_WRITE_B(BO) do { \
;         _Pragma("unroll") for (int _i = 0; _i < 8; ++_i) *(LAS u32x2*)(b_wr + (BO) + (_i & 3) * (16 * G_BSTRIDE) + (_i >> 2) * SLAB1) = pack4(__builtin_bit_cast(f32x4, sb[_i])); } while (0)
; #define G_ENDTILE(VM) do { asm volatile("s_waitcnt vmcnt(" #VM ")" ::: "memory"); \
;         asm volatile("s_waitcnt lgkmcnt(0)" ::: "memory"); __builtin_amdgcn_s_barrier(); asm volatile("" ::: "memory"); } while (0)
;     ...
;     __builtin_amdgcn_s_barrier();
;     G_DMA_A(0, G_A0); G_ISSUE_B(0); G_WRITE_B(G_B0);
;     __builtin_amdgcn_sched_barrier(0);
;     G_ISSUE_B(1);
;     __builtin_amdgcn_sched_barrier(0);
;     G_ENDTILE(8);
;     for (int ui = 0;; ++ui) {
; #pragma unroll
;         for (int m = 0; m < MF; ++m)
; #pragma unroll
;             for (int n = 0; n < 4; ++n) acc[m][n] = (f32x4){0.f, 0.f, 0.f, 0.f};
;         for (int t = 0; t < nt - 2; t += 2) {
;             G_TILE(G_A0, G_B0, true, G_B1, G_A1, t + 1, true, t + 2, (void)0);
.LBB0_69:
	s_andn2_b64 vcc, exec, s[30:31]
	v_mov_b32_e32 v159, 0
	s_cbranch_vccnz .LBB0_72
	s_mov_b32 s8, 0
	s_mov_b32 s9, 0x5a0000
	s_movk_i32 s24, 0x100
	s_mov_b32 m0, s68
	s_add_i32 s25, s24, 0xffffff80
	ds_read_b64_tr_b16 v[170:171], v166
	ds_read_b64_tr_b16 v[172:173], v167
	ds_read_b64_tr_b16 v[176:177], v167 offset:32
	ds_read_b128 v[178:181], v162
	ds_read_b64_tr_b16 v[174:175], v166 offset:32
	ds_read_b64_tr_b16 v[182:183], v166 offset:64
	ds_read_b64_tr_b16 v[186:187], v166 offset:96
	ds_read_b64_tr_b16 v[184:185], v167 offset:64
	ds_read_b64_tr_b16 v[188:189], v167 offset:96
	ds_read_b128 v[190:193], v162 offset:2048
	ds_read_b128 v[194:197], v162 offset:4096
	buffer_load_dwordx4 v163, s[20:23], s25 offen lds
	s_mov_b32 m0, s67
	s_waitcnt lgkmcnt(7)
	v_mfma_f32_16x16x32_bf16 v[156:159], v[170:173], v[178:181], 0
	buffer_load_dwordx4 v165, s[20:23], s25 offen lds
	s_waitcnt lgkmcnt(6)
	v_mfma_f32_16x16x32_bf16 v[152:155], v[174:177], v[178:181], 0
	s_waitcnt lgkmcnt(3)
	v_mfma_f32_16x16x32_bf16 v[148:151], v[182:185], v[178:181], 0
	s_waitcnt lgkmcnt(2)
	v_mfma_f32_16x16x32_bf16 v[144:147], v[186:189], v[178:181], 0
	s_waitcnt lgkmcnt(1)
	v_mfma_f32_16x16x32_bf16 v[140:143], v[170:173], v[190:193], 0
	s_mov_b32 m0, s66
	s_nop 0
	buffer_load_dwordx4 v164, s[20:23], s25 offen lds
	ds_read_b128 v[178:181], v162 offset:6144
	s_waitcnt vmcnt(10)
	v_cvt_pk_bf16_f32 v15, v14, v15
	v_cvt_pk_bf16_f32 v14, v12, v13
	v_mfma_f32_16x16x32_bf16 v[136:139], v[174:177], v[190:193], 0
	ds_write_b64 v161, v[14:15] offset:34816
	v_mfma_f32_16x16x32_bf16 v[132:135], v[182:185], v[190:193], 0
	s_mov_b32 m0, s65
	s_nop 0
	buffer_load_dwordx4 v168, s[20:23], s25 offen lds
	s_add_i32 s25, s9, 0xffd60000
	v_mfma_f32_16x16x32_bf16 v[128:131], v[186:189], v[190:193], 0
	s_waitcnt lgkmcnt(2)
	v_mfma_f32_16x16x32_bf16 v[124:127], v[170:173], v[194:197], 0
	ds_read_b128 v[190:193], v162 offset:8192
	v_mfma_f32_16x16x32_bf16 v[120:123], v[174:177], v[194:197], 0
	v_mfma_f32_16x16x32_bf16 v[116:119], v[182:185], v[194:197], 0
	v_mfma_f32_16x16x32_bf16 v[112:115], v[186:189], v[194:197], 0
	s_waitcnt lgkmcnt(2)
	v_mfma_f32_16x16x32_bf16 v[108:111], v[170:173], v[178:181], 0
	ds_read_b128 v[194:197], v162 offset:10240
	buffer_load_dwordx4 v[12:15], v160, s[12:15], s25 offen
	s_waitcnt vmcnt(11)
	v_cvt_pk_bf16_f32 v3, v2, v3
	v_cvt_pk_bf16_f32 v2, v0, v1
	v_mfma_f32_16x16x32_bf16 v[104:107], v[174:177], v[178:181], 0
	ds_write_b64 v161, v[2:3] offset:43520
	v_mfma_f32_16x16x32_bf16 v[100:103], v[182:185], v[178:181], 0
	v_mfma_f32_16x16x32_bf16 v[96:99], v[186:189], v[178:181], 0
	s_add_i32 s26, s9, 0xffdc0000
	s_waitcnt lgkmcnt(2)
	v_mfma_f32_16x16x32_bf16 v[92:95], v[170:173], v[190:193], 0
	ds_read_b128 v[178:181], v162 offset:12288
	v_mfma_f32_16x16x32_bf16 v[88:91], v[174:177], v[190:193], 0
	v_mfma_f32_16x16x32_bf16 v[84:87], v[182:185], v[190:193], 0
	v_mfma_f32_16x16x32_bf16 v[80:83], v[186:189], v[190:193], 0
	s_waitcnt lgkmcnt(2)
	v_mfma_f32_16x16x32_bf16 v[76:79], v[170:173], v[194:197], 0
	ds_read_b128 v[190:193], v162 offset:14336
	buffer_load_dwordx4 v[0:3], v160, s[12:15], s26 offen
	s_waitcnt vmcnt(11)
	v_cvt_pk_bf16_f32 v31, v30, v31
	v_cvt_pk_bf16_f32 v30, v28, v29
	v_mfma_f32_16x16x32_bf16 v[72:75], v[174:177], v[194:197], 0
	ds_write_b64 v161, v[30:31] offset:52224
	v_mfma_f32_16x16x32_bf16 v[68:71], v[182:185], v[194:197], 0
	v_mfma_f32_16x16x32_bf16 v[64:67], v[186:189], v[194:197], 0
	s_add_i32 s27, s9, 0xffe20000
	s_waitcnt lgkmcnt(2)
	v_mfma_f32_16x16x32_bf16 v[60:63], v[170:173], v[178:181], 0
	ds_read_b128 v[194:197], v162 offset:1024
	v_mfma_f32_16x16x32_bf16 v[56:59], v[174:177], v[178:181], 0
	v_mfma_f32_16x16x32_bf16 v[52:55], v[182:185], v[178:181], 0
	v_mfma_f32_16x16x32_bf16 v[48:51], v[186:189], v[178:181], 0
	s_waitcnt lgkmcnt(2)
	v_mfma_f32_16x16x32_bf16 v[44:47], v[170:173], v[190:193], 0
	ds_read_b128 v[170:173], v162 offset:3072
	buffer_load_dwordx4 v[28:31], v160, s[12:15], s27 offen
	s_waitcnt vmcnt(11)
	v_cvt_pk_bf16_f32 v27, v26, v27
	v_cvt_pk_bf16_f32 v26, v24, v25
	v_mfma_f32_16x16x32_bf16 v[40:43], v[174:177], v[190:193], 0
	ds_read_b64_tr_b16 v[244:245], v166 offset:17408
	ds_read_b64_tr_b16 v[248:249], v166 offset:17440
	ds_read_b64_tr_b16 v[198:199], v166 offset:17472
	ds_read_b64_tr_b16 v[202:203], v166 offset:17504
	ds_read_b64_tr_b16 v[246:247], v167 offset:17408
	ds_read_b64_tr_b16 v[250:251], v167 offset:17440
	ds_read_b64_tr_b16 v[200:201], v167 offset:17472
	ds_read_b64_tr_b16 v[204:205], v167 offset:17504
	ds_write_b64 v161, v[26:27] offset:60928
	v_mfma_f32_16x16x32_bf16 v[36:39], v[182:185], v[190:193], 0
	v_mfma_f32_16x16x32_bf16 v[32:35], v[186:189], v[190:193], 0
	s_add_i32 s42, s9, 0xffe80000
	s_waitcnt lgkmcnt(4)
	v_mfma_f32_16x16x32_bf16 v[156:159], v[244:247], v[194:197], v[156:159]
	ds_read_b128 v[182:185], v162 offset:5120
	s_waitcnt lgkmcnt(4)
	v_mfma_f32_16x16x32_bf16 v[152:155], v[248:251], v[194:197], v[152:155]
	s_waitcnt lgkmcnt(3)
	v_mfma_f32_16x16x32_bf16 v[148:151], v[198:201], v[194:197], v[148:151]
	s_waitcnt lgkmcnt(2)
	v_mfma_f32_16x16x32_bf16 v[144:147], v[202:205], v[194:197], v[144:147]
	v_mfma_f32_16x16x32_bf16 v[140:143], v[244:247], v[170:173], v[140:143]
	ds_read_b128 v[186:189], v162 offset:7168
	buffer_load_dwordx4 v[24:27], v160, s[12:15], s42 offen
	s_waitcnt vmcnt(11)
	v_cvt_pk_bf16_f32 v23, v22, v23
	v_cvt_pk_bf16_f32 v22, v20, v21
	v_mfma_f32_16x16x32_bf16 v[136:139], v[248:251], v[170:173], v[136:139]
	ds_write_b64 v161, v[22:23] offset:35072
	v_mfma_f32_16x16x32_bf16 v[132:135], v[198:201], v[170:173], v[132:135]
	v_mfma_f32_16x16x32_bf16 v[128:131], v[202:205], v[170:173], v[128:131]
	s_waitcnt lgkmcnt(2)
; #define G_DMA_A(kt, AO) do { G_DMA1(kt, AO, 0); G_DMA1(kt, AO, 1); G_DMA1(kt, AO, 2); G_DMA1(kt, AO, 3); if (MF == 9) G_DMA5(kt, AO); } while (0)
; #define G_ISSUE_B(kt) do { const unsigned _sb = (unsigned)(kt) * 4u * kstepB; \
;         _Pragma("unroll") for (int _i = 0; _i < 8; ++_i) sb[_i] = bload16(_i < 4 ? rsB0 : rsB1, vob, _sb + (_i & 3) * kstepB); } while (0)
; #define G_WRITE_B(BO) do { \
;         _Pragma("unroll") for (int _i = 0; _i < 8; ++_i) *(LAS u32x2*)(b_wr + (BO) + (_i & 3) * (16 * G_BSTRIDE) + (_i >> 2) * SLAB1) = pack4(__builtin_bit_cast(f32x4, sb[_i])); } while (0)
; #define G_ENDTILE(VM) do { asm volatile("s_waitcnt vmcnt(" #VM ")" ::: "memory"); \
;         asm volatile("s_waitcnt lgkmcnt(0)" ::: "memory"); __builtin_amdgcn_s_barrier(); asm volatile("" ::: "memory"); } while (0)
;     ...
;     __builtin_amdgcn_s_barrier();
;     G_DMA_A(0, G_A0); G_ISSUE_B(0); G_WRITE_B(G_B0);
;     __builtin_amdgcn_sched_barrier(0);
;     G_ISSUE_B(1);
;     __builtin_amdgcn_sched_barrier(0);
;     G_ENDTILE(8);
;     for (int ui = 0;; ++ui) {
; #pragma unroll
;         for (int m = 0; m < MF; ++m)
; #pragma unroll
;             for (int n = 0; n < 4; ++n) acc[m][n] = (f32x4){0.f, 0.f, 0.f, 0.f};
;         for (int t = 0; t < nt - 2; t += 2) {
;             G_TILE(G_A0, G_B0, true, G_B1, G_A1, t + 1, true, t + 2, (void)0);
;             G_ENDTILE(8);
;             G_TILE(G_A1, G_B1, true, G_B0, G_A0, t + 2, true, t + 3, (void)0);
	v_mfma_f32_16x16x32_bf16 v[124:127], v[244:247], v[182:185], v[124:127]
	ds_read_b128 v[170:173], v162 offset:9216
	v_mfma_f32_16x16x32_bf16 v[120:123], v[248:251], v[182:185], v[120:123]
	v_mfma_f32_16x16x32_bf16 v[116:119], v[198:201], v[182:185], v[116:119]
	v_mfma_f32_16x16x32_bf16 v[112:115], v[202:205], v[182:185], v[112:115]
	s_waitcnt lgkmcnt(2)
	v_mfma_f32_16x16x32_bf16 v[108:111], v[244:247], v[186:189], v[108:111]
	ds_read_b128 v[182:185], v162 offset:11264
	buffer_load_dwordx4 v[20:23], v160, s[16:19], s25 offen
	s_waitcnt vmcnt(11)
	v_cvt_pk_bf16_f32 v7, v6, v7
	v_cvt_pk_bf16_f32 v6, v4, v5
	v_mfma_f32_16x16x32_bf16 v[104:107], v[248:251], v[186:189], v[104:107]
	ds_write_b64 v161, v[6:7] offset:43776
	v_mfma_f32_16x16x32_bf16 v[100:103], v[198:201], v[186:189], v[100:103]
	v_mfma_f32_16x16x32_bf16 v[96:99], v[202:205], v[186:189], v[96:99]
	s_waitcnt lgkmcnt(2)
	v_mfma_f32_16x16x32_bf16 v[92:95], v[244:247], v[170:173], v[92:95]
	ds_read_b128 v[186:189], v162 offset:13312
	v_mfma_f32_16x16x32_bf16 v[88:91], v[248:251], v[170:173], v[88:91]
	v_mfma_f32_16x16x32_bf16 v[84:87], v[198:201], v[170:173], v[84:87]
	v_mfma_f32_16x16x32_bf16 v[80:83], v[202:205], v[170:173], v[80:83]
	s_waitcnt lgkmcnt(2)
	v_mfma_f32_16x16x32_bf16 v[76:79], v[244:247], v[182:185], v[76:79]
	ds_read_b128 v[252:255], v162 offset:15360
	buffer_load_dwordx4 v[4:7], v160, s[16:19], s26 offen
	s_waitcnt vmcnt(11)
	v_cvt_pk_bf16_f32 v11, v10, v11
	v_cvt_pk_bf16_f32 v10, v8, v9
	v_mfma_f32_16x16x32_bf16 v[72:75], v[248:251], v[182:185], v[72:75]
	ds_write_b64 v161, v[10:11] offset:52480
	v_mfma_f32_16x16x32_bf16 v[68:71], v[198:201], v[182:185], v[68:71]
	v_mfma_f32_16x16x32_bf16 v[64:67], v[202:205], v[182:185], v[64:67]
	s_waitcnt lgkmcnt(2)
	v_mfma_f32_16x16x32_bf16 v[60:63], v[244:247], v[186:189], v[60:63]
	buffer_load_dwordx4 v[8:11], v160, s[16:19], s27 offen
	s_waitcnt vmcnt(11)
	v_cvt_pk_bf16_f32 v19, v18, v19
	v_cvt_pk_bf16_f32 v18, v16, v17
	v_mfma_f32_16x16x32_bf16 v[56:59], v[248:251], v[186:189], v[56:59]
	ds_write_b64 v161, v[18:19] offset:61184
	v_mfma_f32_16x16x32_bf16 v[52:55], v[198:201], v[186:189], v[52:55]
	buffer_load_dwordx4 v[16:19], v160, s[16:19], s42 offen
	v_mfma_f32_16x16x32_bf16 v[48:51], v[202:205], v[186:189], v[48:51]
	s_waitcnt vmcnt(8)
	s_mov_b32 m0, s55
	s_waitcnt lgkmcnt(0)
	s_barrier
	ds_read_b64_tr_b16 v[170:171], v166 offset:34816
	ds_read_b64_tr_b16 v[172:173], v167 offset:34816
	ds_read_b64_tr_b16 v[176:177], v167 offset:34848
	ds_read_b128 v[178:181], v162 offset:32768
	ds_read_b64_tr_b16 v[174:175], v166 offset:34848
	ds_read_b64_tr_b16 v[182:183], v166 offset:34880
	ds_read_b64_tr_b16 v[186:187], v166 offset:34912
	ds_read_b64_tr_b16 v[184:185], v167 offset:34880
	ds_read_b64_tr_b16 v[188:189], v167 offset:34912
	ds_read_b128 v[190:193], v162 offset:34816
	ds_read_b128 v[194:197], v162 offset:36864
	buffer_load_dwordx4 v163, s[20:23], s24 offen lds
	s_mov_b32 m0, s56
	v_mfma_f32_16x16x32_bf16 v[44:47], v[244:247], v[252:255], v[44:47]
	v_mfma_f32_16x16x32_bf16 v[40:43], v[248:251], v[252:255], v[40:43]
	v_mfma_f32_16x16x32_bf16 v[36:39], v[198:201], v[252:255], v[36:39]
	v_mfma_f32_16x16x32_bf16 v[32:35], v[202:205], v[252:255], v[32:35]
	s_waitcnt lgkmcnt(7)
	v_mfma_f32_16x16x32_bf16 v[156:159], v[170:173], v[178:181], v[156:159]
	buffer_load_dwordx4 v165, s[20:23], s24 offen lds
	s_add_i32 s25, s9, 0xffee0000
	s_waitcnt lgkmcnt(6)
	v_mfma_f32_16x16x32_bf16 v[152:155], v[174:177], v[178:181], v[152:155]
	s_waitcnt lgkmcnt(3)
	v_mfma_f32_16x16x32_bf16 v[148:151], v[182:185], v[178:181], v[148:151]
	s_waitcnt lgkmcnt(2)
	v_mfma_f32_16x16x32_bf16 v[144:147], v[186:189], v[178:181], v[144:147]
	s_waitcnt lgkmcnt(1)
	v_mfma_f32_16x16x32_bf16 v[140:143], v[170:173], v[190:193], v[140:143]
	s_mov_b32 m0, s57
	s_nop 0
	buffer_load_dwordx4 v164, s[20:23], s24 offen lds
	ds_read_b128 v[178:181], v162 offset:38912
	s_waitcnt vmcnt(10)
	v_cvt_pk_bf16_f32 v15, v14, v15
	v_cvt_pk_bf16_f32 v14, v12, v13
	v_mfma_f32_16x16x32_bf16 v[136:139], v[174:177], v[190:193], v[136:139]
	ds_write_b64 v161, v[14:15]
	v_mfma_f32_16x16x32_bf16 v[132:135], v[182:185], v[190:193], v[132:135]
	s_mov_b32 m0, s59
	s_nop 0
	buffer_load_dwordx4 v168, s[20:23], s24 offen lds
	v_mfma_f32_16x16x32_bf16 v[128:131], v[186:189], v[190:193], v[128:131]
	s_waitcnt lgkmcnt(2)
	v_mfma_f32_16x16x32_bf16 v[124:127], v[170:173], v[194:197], v[124:127]
	ds_read_b128 v[190:193], v162 offset:40960
	v_mfma_f32_16x16x32_bf16 v[120:123], v[174:177], v[194:197], v[120:123]
	v_mfma_f32_16x16x32_bf16 v[116:119], v[182:185], v[194:197], v[116:119]
	v_mfma_f32_16x16x32_bf16 v[112:115], v[186:189], v[194:197], v[112:115]
	s_waitcnt lgkmcnt(2)
	v_mfma_f32_16x16x32_bf16 v[108:111], v[170:173], v[178:181], v[108:111]
	ds_read_b128 v[194:197], v162 offset:43008
	buffer_load_dwordx4 v[12:15], v160, s[12:15], s25 offen
	s_waitcnt vmcnt(11)
	v_cvt_pk_bf16_f32 v3, v2, v3
	v_cvt_pk_bf16_f32 v2, v0, v1
	v_mfma_f32_16x16x32_bf16 v[104:107], v[174:177], v[178:181], v[104:107]
	ds_write_b64 v161, v[2:3] offset:8704
	v_mfma_f32_16x16x32_bf16 v[100:103], v[182:185], v[178:181], v[100:103]
	v_mfma_f32_16x16x32_bf16 v[96:99], v[186:189], v[178:181], v[96:99]
	s_add_i32 s26, s9, 0xfff40000
	s_waitcnt lgkmcnt(2)
	v_mfma_f32_16x16x32_bf16 v[92:95], v[170:173], v[190:193], v[92:95]
	ds_read_b128 v[178:181], v162 offset:45056
	v_mfma_f32_16x16x32_bf16 v[88:91], v[174:177], v[190:193], v[88:91]
	v_mfma_f32_16x16x32_bf16 v[84:87], v[182:185], v[190:193], v[84:87]
	v_mfma_f32_16x16x32_bf16 v[80:83], v[186:189], v[190:193], v[80:83]
	s_waitcnt lgkmcnt(2)
; #define G_DMA_A(kt, AO) do { G_DMA1(kt, AO, 0); G_DMA1(kt, AO, 1); G_DMA1(kt, AO, 2); G_DMA1(kt, AO, 3); if (MF == 9) G_DMA5(kt, AO); } while (0)
; #define G_ISSUE_B(kt) do { const unsigned _sb = (unsigned)(kt) * 4u * kstepB; \
;         _Pragma("unroll") for (int _i = 0; _i < 8; ++_i) sb[_i] = bload16(_i < 4 ? rsB0 : rsB1, vob, _sb + (_i & 3) * kstepB); } while (0)
; #define G_WRITE_B(BO) do { \
;         _Pragma("unroll") for (int _i = 0; _i < 8; ++_i) *(LAS u32x2*)(b_wr + (BO) + (_i & 3) * (16 * G_BSTRIDE) + (_i >> 2) * SLAB1) = pack4(__builtin_bit_cast(f32x4, sb[_i])); } while (0)
; #define G_ENDTILE(VM) do { asm volatile("s_waitcnt vmcnt(" #VM ")" ::: "memory"); \
;         asm volatile("s_waitcnt lgkmcnt(0)" ::: "memory"); __builtin_amdgcn_s_barrier(); asm volatile("" ::: "memory"); } while (0)
;     ...
;     __builtin_amdgcn_s_barrier();
;     G_DMA_A(0, G_A0); G_ISSUE_B(0); G_WRITE_B(G_B0);
;     __builtin_amdgcn_sched_barrier(0);
;     G_ISSUE_B(1);
;     __builtin_amdgcn_sched_barrier(0);
;     G_ENDTILE(8);
;     for (int ui = 0;; ++ui) {
; #pragma unroll
;         for (int m = 0; m < MF; ++m)
; #pragma unroll
;             for (int n = 0; n < 4; ++n) acc[m][n] = (f32x4){0.f, 0.f, 0.f, 0.f};
;         for (int t = 0; t < nt - 2; t += 2) {
;             G_TILE(G_A0, G_B0, true, G_B1, G_A1, t + 1, true, t + 2, (void)0);
;             G_ENDTILE(8);
;             G_TILE(G_A1, G_B1, true, G_B0, G_A0, t + 2, true, t + 3, (void)0);
;             G_ENDTILE(8);
;         }
	v_mfma_f32_16x16x32_bf16 v[76:79], v[170:173], v[194:197], v[76:79]
	ds_read_b128 v[190:193], v162 offset:47104
	buffer_load_dwordx4 v[0:3], v160, s[12:15], s26 offen
	s_waitcnt vmcnt(11)
	v_cvt_pk_bf16_f32 v31, v30, v31
	v_cvt_pk_bf16_f32 v30, v28, v29
	v_mfma_f32_16x16x32_bf16 v[72:75], v[174:177], v[194:197], v[72:75]
	ds_write_b64 v161, v[30:31] offset:17408
	v_mfma_f32_16x16x32_bf16 v[68:71], v[182:185], v[194:197], v[68:71]
	v_mfma_f32_16x16x32_bf16 v[64:67], v[186:189], v[194:197], v[64:67]
	s_add_i32 s27, s9, 0xfffa0000
	s_waitcnt lgkmcnt(2)
	v_mfma_f32_16x16x32_bf16 v[60:63], v[170:173], v[178:181], v[60:63]
	ds_read_b128 v[194:197], v162 offset:33792
	v_mfma_f32_16x16x32_bf16 v[56:59], v[174:177], v[178:181], v[56:59]
	v_mfma_f32_16x16x32_bf16 v[52:55], v[182:185], v[178:181], v[52:55]
	v_mfma_f32_16x16x32_bf16 v[48:51], v[186:189], v[178:181], v[48:51]
	s_waitcnt lgkmcnt(2)
	v_mfma_f32_16x16x32_bf16 v[44:47], v[170:173], v[190:193], v[44:47]
	ds_read_b128 v[170:173], v162 offset:35840
	buffer_load_dwordx4 v[28:31], v160, s[12:15], s27 offen
	s_waitcnt vmcnt(11)
	v_cvt_pk_bf16_f32 v27, v26, v27
	v_cvt_pk_bf16_f32 v26, v24, v25
	v_mfma_f32_16x16x32_bf16 v[40:43], v[174:177], v[190:193], v[40:43]
	ds_read_b64_tr_b16 v[244:245], v166 offset:52224
	ds_read_b64_tr_b16 v[248:249], v166 offset:52256
	ds_read_b64_tr_b16 v[198:199], v166 offset:52288
	ds_read_b64_tr_b16 v[202:203], v166 offset:52320
	ds_read_b64_tr_b16 v[246:247], v167 offset:52224
	ds_read_b64_tr_b16 v[250:251], v167 offset:52256
	ds_read_b64_tr_b16 v[200:201], v167 offset:52288
	ds_read_b64_tr_b16 v[204:205], v167 offset:52320
	ds_write_b64 v161, v[26:27] offset:26112
	v_mfma_f32_16x16x32_bf16 v[36:39], v[182:185], v[190:193], v[36:39]
	v_mfma_f32_16x16x32_bf16 v[32:35], v[186:189], v[190:193], v[32:35]
	s_waitcnt lgkmcnt(4)
	v_mfma_f32_16x16x32_bf16 v[156:159], v[244:247], v[194:197], v[156:159]
	ds_read_b128 v[182:185], v162 offset:37888
	s_waitcnt lgkmcnt(4)
	v_mfma_f32_16x16x32_bf16 v[152:155], v[248:251], v[194:197], v[152:155]
	s_waitcnt lgkmcnt(3)
	v_mfma_f32_16x16x32_bf16 v[148:151], v[198:201], v[194:197], v[148:151]
	s_waitcnt lgkmcnt(2)
	v_mfma_f32_16x16x32_bf16 v[144:147], v[202:205], v[194:197], v[144:147]
	v_mfma_f32_16x16x32_bf16 v[140:143], v[244:247], v[170:173], v[140:143]
	ds_read_b128 v[186:189], v162 offset:39936
	buffer_load_dwordx4 v[24:27], v160, s[12:15], s9 offen
	s_waitcnt vmcnt(11)
	v_cvt_pk_bf16_f32 v23, v22, v23
	v_cvt_pk_bf16_f32 v22, v20, v21
	v_mfma_f32_16x16x32_bf16 v[136:139], v[248:251], v[170:173], v[136:139]
	ds_write_b64 v161, v[22:23] offset:256
	v_mfma_f32_16x16x32_bf16 v[132:135], v[198:201], v[170:173], v[132:135]
	v_mfma_f32_16x16x32_bf16 v[128:131], v[202:205], v[170:173], v[128:131]
	s_waitcnt lgkmcnt(2)
	v_mfma_f32_16x16x32_bf16 v[124:127], v[244:247], v[182:185], v[124:127]
	ds_read_b128 v[170:173], v162 offset:41984
	v_mfma_f32_16x16x32_bf16 v[120:123], v[248:251], v[182:185], v[120:123]
	v_mfma_f32_16x16x32_bf16 v[116:119], v[198:201], v[182:185], v[116:119]
	v_mfma_f32_16x16x32_bf16 v[112:115], v[202:205], v[182:185], v[112:115]
	s_waitcnt lgkmcnt(2)
	v_mfma_f32_16x16x32_bf16 v[108:111], v[244:247], v[186:189], v[108:111]
	ds_read_b128 v[182:185], v162 offset:44032
	buffer_load_dwordx4 v[20:23], v160, s[16:19], s25 offen
	s_waitcnt vmcnt(11)
	v_cvt_pk_bf16_f32 v7, v6, v7
	v_cvt_pk_bf16_f32 v6, v4, v5
	v_mfma_f32_16x16x32_bf16 v[104:107], v[248:251], v[186:189], v[104:107]
	ds_write_b64 v161, v[6:7] offset:8960
	v_mfma_f32_16x16x32_bf16 v[100:103], v[198:201], v[186:189], v[100:103]
	v_mfma_f32_16x16x32_bf16 v[96:99], v[202:205], v[186:189], v[96:99]
	s_waitcnt lgkmcnt(2)
	v_mfma_f32_16x16x32_bf16 v[92:95], v[244:247], v[170:173], v[92:95]
	ds_read_b128 v[186:189], v162 offset:46080
	v_mfma_f32_16x16x32_bf16 v[88:91], v[248:251], v[170:173], v[88:91]
	v_mfma_f32_16x16x32_bf16 v[84:87], v[198:201], v[170:173], v[84:87]
	v_mfma_f32_16x16x32_bf16 v[80:83], v[202:205], v[170:173], v[80:83]
	s_waitcnt lgkmcnt(2)
	v_mfma_f32_16x16x32_bf16 v[76:79], v[244:247], v[182:185], v[76:79]
	ds_read_b128 v[252:255], v162 offset:48128
	buffer_load_dwordx4 v[4:7], v160, s[16:19], s26 offen
	s_waitcnt vmcnt(11)
	v_cvt_pk_bf16_f32 v11, v10, v11
	v_cvt_pk_bf16_f32 v10, v8, v9
	v_mfma_f32_16x16x32_bf16 v[72:75], v[248:251], v[182:185], v[72:75]
	ds_write_b64 v161, v[10:11] offset:17664
	v_mfma_f32_16x16x32_bf16 v[68:71], v[198:201], v[182:185], v[68:71]
	v_mfma_f32_16x16x32_bf16 v[64:67], v[202:205], v[182:185], v[64:67]
	s_waitcnt lgkmcnt(2)
	v_mfma_f32_16x16x32_bf16 v[60:63], v[244:247], v[186:189], v[60:63]
	buffer_load_dwordx4 v[8:11], v160, s[16:19], s27 offen
	s_waitcnt vmcnt(11)
	v_cvt_pk_bf16_f32 v19, v18, v19
	v_cvt_pk_bf16_f32 v18, v16, v17
	v_mfma_f32_16x16x32_bf16 v[56:59], v[248:251], v[186:189], v[56:59]
	ds_write_b64 v161, v[18:19] offset:26368
	v_mfma_f32_16x16x32_bf16 v[52:55], v[198:201], v[186:189], v[52:55]
	buffer_load_dwordx4 v[16:19], v160, s[16:19], s9 offen
	v_mfma_f32_16x16x32_bf16 v[48:51], v[202:205], v[186:189], v[48:51]
	s_add_i32 s8, s8, 2
	s_add_i32 s9, s9, 0x300000
	s_addk_i32 s24, 0x100
	s_cmp_ge_i32 s8, s64
	s_waitcnt vmcnt(8)
	s_waitcnt lgkmcnt(0)
	s_barrier
	s_cbranch_scc1 .Lflush_P1
; #define G_DMA_A(kt, AO) do { G_DMA1(kt, AO, 0); G_DMA1(kt, AO, 1); G_DMA1(kt, AO, 2); G_DMA1(kt, AO, 3); if (MF == 9) G_DMA5(kt, AO); } while (0)
; #define G_ISSUE_B(kt) do { const unsigned _sb = (unsigned)(kt) * 4u * kstepB; \
;         _Pragma("unroll") for (int _i = 0; _i < 8; ++_i) sb[_i] = bload16(_i < 4 ? rsB0 : rsB1, vob, _sb + (_i & 3) * kstepB); } while (0)
; #define G_WRITE_B(BO) do { \
;         _Pragma("unroll") for (int _i = 0; _i < 8; ++_i) *(LAS u32x2*)(b_wr + (BO) + (_i & 3) * (16 * G_BSTRIDE) + (_i >> 2) * SLAB1) = pack4(__builtin_bit_cast(f32x4, sb[_i])); } while (0)
; #define G_ENDTILE(VM) do { asm volatile("s_waitcnt vmcnt(" #VM ")" ::: "memory"); \
;         asm volatile("s_waitcnt lgkmcnt(0)" ::: "memory"); __builtin_amdgcn_s_barrier(); asm volatile("" ::: "memory"); } while (0)
;     ...
;     __builtin_amdgcn_s_barrier();
;     G_DMA_A(0, G_A0); G_ISSUE_B(0); G_WRITE_B(G_B0);
;     __builtin_amdgcn_sched_barrier(0);
;     G_ISSUE_B(1);
;     __builtin_amdgcn_sched_barrier(0);
;     G_ENDTILE(8);
;     for (int ui = 0;; ++ui) {
; #pragma unroll
;         for (int m = 0; m < MF; ++m)
; #pragma unroll
;             for (int n = 0; n < 4; ++n) acc[m][n] = (f32x4){0.f, 0.f, 0.f, 0.f};
;         for (int t = 0; t < nt - 2; t += 2) {
;             G_TILE(G_A0, G_B0, true, G_B1, G_A1, t + 1, true, t + 2, (void)0);
.LBB0_71:
	s_mov_b32 m0, s68
	s_add_i32 s25, s24, 0xffffff80
	ds_read_b64_tr_b16 v[170:171], v166
	ds_read_b64_tr_b16 v[172:173], v167
	ds_read_b64_tr_b16 v[176:177], v167 offset:32
	ds_read_b128 v[178:181], v162
	ds_read_b64_tr_b16 v[174:175], v166 offset:32
	ds_read_b64_tr_b16 v[182:183], v166 offset:64
	ds_read_b64_tr_b16 v[186:187], v166 offset:96
	ds_read_b64_tr_b16 v[184:185], v167 offset:64
	ds_read_b64_tr_b16 v[188:189], v167 offset:96
	ds_read_b128 v[190:193], v162 offset:2048
	ds_read_b128 v[194:197], v162 offset:4096
	buffer_load_dwordx4 v163, s[20:23], s25 offen lds
	s_mov_b32 m0, s67
	v_mfma_f32_16x16x32_bf16 v[44:47], v[244:247], v[252:255], v[44:47]
	v_mfma_f32_16x16x32_bf16 v[40:43], v[248:251], v[252:255], v[40:43]
	v_mfma_f32_16x16x32_bf16 v[36:39], v[198:201], v[252:255], v[36:39]
	v_mfma_f32_16x16x32_bf16 v[32:35], v[202:205], v[252:255], v[32:35]
	s_waitcnt lgkmcnt(7)
	v_mfma_f32_16x16x32_bf16 v[156:159], v[170:173], v[178:181], v[156:159]
	buffer_load_dwordx4 v165, s[20:23], s25 offen lds
	s_waitcnt lgkmcnt(6)
	v_mfma_f32_16x16x32_bf16 v[152:155], v[174:177], v[178:181], v[152:155]
	s_waitcnt lgkmcnt(3)
	v_mfma_f32_16x16x32_bf16 v[148:151], v[182:185], v[178:181], v[148:151]
	s_waitcnt lgkmcnt(2)
	v_mfma_f32_16x16x32_bf16 v[144:147], v[186:189], v[178:181], v[144:147]
	s_waitcnt lgkmcnt(1)
	v_mfma_f32_16x16x32_bf16 v[140:143], v[170:173], v[190:193], v[140:143]
	s_mov_b32 m0, s66
	s_nop 0
	buffer_load_dwordx4 v164, s[20:23], s25 offen lds
	ds_read_b128 v[178:181], v162 offset:6144
	s_waitcnt vmcnt(10)
	v_cvt_pk_bf16_f32 v15, v14, v15
	v_cvt_pk_bf16_f32 v14, v12, v13
	v_mfma_f32_16x16x32_bf16 v[136:139], v[174:177], v[190:193], v[136:139]
	ds_write_b64 v161, v[14:15] offset:34816
	v_mfma_f32_16x16x32_bf16 v[132:135], v[182:185], v[190:193], v[132:135]
	s_mov_b32 m0, s65
	s_nop 0
	buffer_load_dwordx4 v168, s[20:23], s25 offen lds
	s_add_i32 s25, s9, 0xffd60000
	v_mfma_f32_16x16x32_bf16 v[128:131], v[186:189], v[190:193], v[128:131]
	s_waitcnt lgkmcnt(2)
	v_mfma_f32_16x16x32_bf16 v[124:127], v[170:173], v[194:197], v[124:127]
	ds_read_b128 v[190:193], v162 offset:8192
	v_mfma_f32_16x16x32_bf16 v[120:123], v[174:177], v[194:197], v[120:123]
	v_mfma_f32_16x16x32_bf16 v[116:119], v[182:185], v[194:197], v[116:119]
	v_mfma_f32_16x16x32_bf16 v[112:115], v[186:189], v[194:197], v[112:115]
	s_waitcnt lgkmcnt(2)
	v_mfma_f32_16x16x32_bf16 v[108:111], v[170:173], v[178:181], v[108:111]
	ds_read_b128 v[194:197], v162 offset:10240
	buffer_load_dwordx4 v[12:15], v160, s[12:15], s25 offen
	s_waitcnt vmcnt(11)
	v_cvt_pk_bf16_f32 v3, v2, v3
	v_cvt_pk_bf16_f32 v2, v0, v1
	v_mfma_f32_16x16x32_bf16 v[104:107], v[174:177], v[178:181], v[104:107]
	ds_write_b64 v161, v[2:3] offset:43520
	v_mfma_f32_16x16x32_bf16 v[100:103], v[182:185], v[178:181], v[100:103]
	v_mfma_f32_16x16x32_bf16 v[96:99], v[186:189], v[178:181], v[96:99]
	s_add_i32 s26, s9, 0xffdc0000
	s_waitcnt lgkmcnt(2)
	v_mfma_f32_16x16x32_bf16 v[92:95], v[170:173], v[190:193], v[92:95]
	ds_read_b128 v[178:181], v162 offset:12288
	v_mfma_f32_16x16x32_bf16 v[88:91], v[174:177], v[190:193], v[88:91]
	v_mfma_f32_16x16x32_bf16 v[84:87], v[182:185], v[190:193], v[84:87]
	v_mfma_f32_16x16x32_bf16 v[80:83], v[186:189], v[190:193], v[80:83]
	s_waitcnt lgkmcnt(2)
	v_mfma_f32_16x16x32_bf16 v[76:79], v[170:173], v[194:197], v[76:79]
	ds_read_b128 v[190:193], v162 offset:14336
	buffer_load_dwordx4 v[0:3], v160, s[12:15], s26 offen
	s_waitcnt vmcnt(11)
	v_cvt_pk_bf16_f32 v31, v30, v31
	v_cvt_pk_bf16_f32 v30, v28, v29
	v_mfma_f32_16x16x32_bf16 v[72:75], v[174:177], v[194:197], v[72:75]
	ds_write_b64 v161, v[30:31] offset:52224
	v_mfma_f32_16x16x32_bf16 v[68:71], v[182:185], v[194:197], v[68:71]
	v_mfma_f32_16x16x32_bf16 v[64:67], v[186:189], v[194:197], v[64:67]
	s_add_i32 s27, s9, 0xffe20000
	s_waitcnt lgkmcnt(2)
	v_mfma_f32_16x16x32_bf16 v[60:63], v[170:173], v[178:181], v[60:63]
	ds_read_b128 v[194:197], v162 offset:1024
	v_mfma_f32_16x16x32_bf16 v[56:59], v[174:177], v[178:181], v[56:59]
	v_mfma_f32_16x16x32_bf16 v[52:55], v[182:185], v[178:181], v[52:55]
	v_mfma_f32_16x16x32_bf16 v[48:51], v[186:189], v[178:181], v[48:51]
	s_waitcnt lgkmcnt(2)
	v_mfma_f32_16x16x32_bf16 v[44:47], v[170:173], v[190:193], v[44:47]
	ds_read_b128 v[170:173], v162 offset:3072
	buffer_load_dwordx4 v[28:31], v160, s[12:15], s27 offen
	s_waitcnt vmcnt(11)
	v_cvt_pk_bf16_f32 v27, v26, v27
	v_cvt_pk_bf16_f32 v26, v24, v25
	v_mfma_f32_16x16x32_bf16 v[40:43], v[174:177], v[190:193], v[40:43]
	ds_read_b64_tr_b16 v[244:245], v166 offset:17408
	ds_read_b64_tr_b16 v[248:249], v166 offset:17440
	ds_read_b64_tr_b16 v[198:199], v166 offset:17472
	ds_read_b64_tr_b16 v[202:203], v166 offset:17504
	ds_read_b64_tr_b16 v[246:247], v167 offset:17408
	ds_read_b64_tr_b16 v[250:251], v167 offset:17440
	ds_read_b64_tr_b16 v[200:201], v167 offset:17472
	ds_read_b64_tr_b16 v[204:205], v167 offset:17504
	ds_write_b64 v161, v[26:27] offset:60928
	v_mfma_f32_16x16x32_bf16 v[36:39], v[182:185], v[190:193], v[36:39]
	v_mfma_f32_16x16x32_bf16 v[32:35], v[186:189], v[190:193], v[32:35]
	s_add_i32 s42, s9, 0xffe80000
	s_waitcnt lgkmcnt(4)
	v_mfma_f32_16x16x32_bf16 v[156:159], v[244:247], v[194:197], v[156:159]
	ds_read_b128 v[182:185], v162 offset:5120
	s_waitcnt lgkmcnt(4)
	v_mfma_f32_16x16x32_bf16 v[152:155], v[248:251], v[194:197], v[152:155]
	s_waitcnt lgkmcnt(3)
	v_mfma_f32_16x16x32_bf16 v[148:151], v[198:201], v[194:197], v[148:151]
	s_waitcnt lgkmcnt(2)
	v_mfma_f32_16x16x32_bf16 v[144:147], v[202:205], v[194:197], v[144:147]
	v_mfma_f32_16x16x32_bf16 v[140:143], v[244:247], v[170:173], v[140:143]
	ds_read_b128 v[186:189], v162 offset:7168
	buffer_load_dwordx4 v[24:27], v160, s[12:15], s42 offen
	s_waitcnt vmcnt(11)
; #define G_DMA_A(kt, AO) do { G_DMA1(kt, AO, 0); G_DMA1(kt, AO, 1); G_DMA1(kt, AO, 2); G_DMA1(kt, AO, 3); if (MF == 9) G_DMA5(kt, AO); } while (0)
; #define G_ISSUE_B(kt) do { const unsigned _sb = (unsigned)(kt) * 4u * kstepB; \
;         _Pragma("unroll") for (int _i = 0; _i < 8; ++_i) sb[_i] = bload16(_i < 4 ? rsB0 : rsB1, vob, _sb + (_i & 3) * kstepB); } while (0)
; #define G_WRITE_B(BO) do { \
;         _Pragma("unroll") for (int _i = 0; _i < 8; ++_i) *(LAS u32x2*)(b_wr + (BO) + (_i & 3) * (16 * G_BSTRIDE) + (_i >> 2) * SLAB1) = pack4(__builtin_bit_cast(f32x4, sb[_i])); } while (0)
; #define G_ENDTILE(VM) do { asm volatile("s_waitcnt vmcnt(" #VM ")" ::: "memory"); \
;         asm volatile("s_waitcnt lgkmcnt(0)" ::: "memory"); __builtin_amdgcn_s_barrier(); asm volatile("" ::: "memory"); } while (0)
;     ...
;     __builtin_amdgcn_s_barrier();
;     G_DMA_A(0, G_A0); G_ISSUE_B(0); G_WRITE_B(G_B0);
;     __builtin_amdgcn_sched_barrier(0);
;     G_ISSUE_B(1);
;     __builtin_amdgcn_sched_barrier(0);
;     G_ENDTILE(8);
;     for (int ui = 0;; ++ui) {
; #pragma unroll
;         for (int m = 0; m < MF; ++m)
; #pragma unroll
;             for (int n = 0; n < 4; ++n) acc[m][n] = (f32x4){0.f, 0.f, 0.f, 0.f};
;         for (int t = 0; t < nt - 2; t += 2) {
;             G_TILE(G_A0, G_B0, true, G_B1, G_A1, t + 1, true, t + 2, (void)0);
;             G_ENDTILE(8);
;             G_TILE(G_A1, G_B1, true, G_B0, G_A0, t + 2, true, t + 3, (void)0);
	v_cvt_pk_bf16_f32 v23, v22, v23
	v_cvt_pk_bf16_f32 v22, v20, v21
	v_mfma_f32_16x16x32_bf16 v[136:139], v[248:251], v[170:173], v[136:139]
	ds_write_b64 v161, v[22:23] offset:35072
	v_mfma_f32_16x16x32_bf16 v[132:135], v[198:201], v[170:173], v[132:135]
	v_mfma_f32_16x16x32_bf16 v[128:131], v[202:205], v[170:173], v[128:131]
	s_waitcnt lgkmcnt(2)
	v_mfma_f32_16x16x32_bf16 v[124:127], v[244:247], v[182:185], v[124:127]
	ds_read_b128 v[170:173], v162 offset:9216
	v_mfma_f32_16x16x32_bf16 v[120:123], v[248:251], v[182:185], v[120:123]
	v_mfma_f32_16x16x32_bf16 v[116:119], v[198:201], v[182:185], v[116:119]
	v_mfma_f32_16x16x32_bf16 v[112:115], v[202:205], v[182:185], v[112:115]
	s_waitcnt lgkmcnt(2)
	v_mfma_f32_16x16x32_bf16 v[108:111], v[244:247], v[186:189], v[108:111]
	ds_read_b128 v[182:185], v162 offset:11264
	buffer_load_dwordx4 v[20:23], v160, s[16:19], s25 offen
	s_waitcnt vmcnt(11)
	v_cvt_pk_bf16_f32 v7, v6, v7
	v_cvt_pk_bf16_f32 v6, v4, v5
	v_mfma_f32_16x16x32_bf16 v[104:107], v[248:251], v[186:189], v[104:107]
	ds_write_b64 v161, v[6:7] offset:43776
	v_mfma_f32_16x16x32_bf16 v[100:103], v[198:201], v[186:189], v[100:103]
	v_mfma_f32_16x16x32_bf16 v[96:99], v[202:205], v[186:189], v[96:99]
	s_waitcnt lgkmcnt(2)
	v_mfma_f32_16x16x32_bf16 v[92:95], v[244:247], v[170:173], v[92:95]
	ds_read_b128 v[186:189], v162 offset:13312
	v_mfma_f32_16x16x32_bf16 v[88:91], v[248:251], v[170:173], v[88:91]
	v_mfma_f32_16x16x32_bf16 v[84:87], v[198:201], v[170:173], v[84:87]
	v_mfma_f32_16x16x32_bf16 v[80:83], v[202:205], v[170:173], v[80:83]
	s_waitcnt lgkmcnt(2)
	v_mfma_f32_16x16x32_bf16 v[76:79], v[244:247], v[182:185], v[76:79]
	ds_read_b128 v[252:255], v162 offset:15360
	buffer_load_dwordx4 v[4:7], v160, s[16:19], s26 offen
	s_waitcnt vmcnt(11)
	v_cvt_pk_bf16_f32 v11, v10, v11
	v_cvt_pk_bf16_f32 v10, v8, v9
	v_mfma_f32_16x16x32_bf16 v[72:75], v[248:251], v[182:185], v[72:75]
	ds_write_b64 v161, v[10:11] offset:52480
	v_mfma_f32_16x16x32_bf16 v[68:71], v[198:201], v[182:185], v[68:71]
	v_mfma_f32_16x16x32_bf16 v[64:67], v[202:205], v[182:185], v[64:67]
	s_waitcnt lgkmcnt(2)
	v_mfma_f32_16x16x32_bf16 v[60:63], v[244:247], v[186:189], v[60:63]
	buffer_load_dwordx4 v[8:11], v160, s[16:19], s27 offen
	s_waitcnt vmcnt(11)
	v_cvt_pk_bf16_f32 v19, v18, v19
	v_cvt_pk_bf16_f32 v18, v16, v17
	v_mfma_f32_16x16x32_bf16 v[56:59], v[248:251], v[186:189], v[56:59]
	ds_write_b64 v161, v[18:19] offset:61184
	v_mfma_f32_16x16x32_bf16 v[52:55], v[198:201], v[186:189], v[52:55]
	buffer_load_dwordx4 v[16:19], v160, s[16:19], s42 offen
	v_mfma_f32_16x16x32_bf16 v[48:51], v[202:205], v[186:189], v[48:51]
	s_waitcnt vmcnt(8)
	s_mov_b32 m0, s55
	s_waitcnt lgkmcnt(0)
	s_barrier
	ds_read_b64_tr_b16 v[170:171], v166 offset:34816
	ds_read_b64_tr_b16 v[172:173], v167 offset:34816
	ds_read_b64_tr_b16 v[176:177], v167 offset:34848
	ds_read_b128 v[178:181], v162 offset:32768
	ds_read_b64_tr_b16 v[174:175], v166 offset:34848
	ds_read_b64_tr_b16 v[182:183], v166 offset:34880
	ds_read_b64_tr_b16 v[186:187], v166 offset:34912
	ds_read_b64_tr_b16 v[184:185], v167 offset:34880
	ds_read_b64_tr_b16 v[188:189], v167 offset:34912
	ds_read_b128 v[190:193], v162 offset:34816
	ds_read_b128 v[194:197], v162 offset:36864
	buffer_load_dwordx4 v163, s[20:23], s24 offen lds
	s_mov_b32 m0, s56
	v_mfma_f32_16x16x32_bf16 v[44:47], v[244:247], v[252:255], v[44:47]
	v_mfma_f32_16x16x32_bf16 v[40:43], v[248:251], v[252:255], v[40:43]
	v_mfma_f32_16x16x32_bf16 v[36:39], v[198:201], v[252:255], v[36:39]
	v_mfma_f32_16x16x32_bf16 v[32:35], v[202:205], v[252:255], v[32:35]
	s_waitcnt lgkmcnt(7)
	v_mfma_f32_16x16x32_bf16 v[156:159], v[170:173], v[178:181], v[156:159]
	buffer_load_dwordx4 v165, s[20:23], s24 offen lds
	s_add_i32 s25, s9, 0xffee0000
	s_waitcnt lgkmcnt(6)
	v_mfma_f32_16x16x32_bf16 v[152:155], v[174:177], v[178:181], v[152:155]
	s_waitcnt lgkmcnt(3)
	v_mfma_f32_16x16x32_bf16 v[148:151], v[182:185], v[178:181], v[148:151]
	s_waitcnt lgkmcnt(2)
	v_mfma_f32_16x16x32_bf16 v[144:147], v[186:189], v[178:181], v[144:147]
	s_waitcnt lgkmcnt(1)
	v_mfma_f32_16x16x32_bf16 v[140:143], v[170:173], v[190:193], v[140:143]
	s_mov_b32 m0, s57
	s_nop 0
	buffer_load_dwordx4 v164, s[20:23], s24 offen lds
	ds_read_b128 v[178:181], v162 offset:38912
	s_waitcnt vmcnt(10)
	v_cvt_pk_bf16_f32 v15, v14, v15
	v_cvt_pk_bf16_f32 v14, v12, v13
	v_mfma_f32_16x16x32_bf16 v[136:139], v[174:177], v[190:193], v[136:139]
	ds_write_b64 v161, v[14:15]
	v_mfma_f32_16x16x32_bf16 v[132:135], v[182:185], v[190:193], v[132:135]
	s_mov_b32 m0, s59
	s_nop 0
	buffer_load_dwordx4 v168, s[20:23], s24 offen lds
	v_mfma_f32_16x16x32_bf16 v[128:131], v[186:189], v[190:193], v[128:131]
	s_waitcnt lgkmcnt(2)
	v_mfma_f32_16x16x32_bf16 v[124:127], v[170:173], v[194:197], v[124:127]
	ds_read_b128 v[190:193], v162 offset:40960
	v_mfma_f32_16x16x32_bf16 v[120:123], v[174:177], v[194:197], v[120:123]
	v_mfma_f32_16x16x32_bf16 v[116:119], v[182:185], v[194:197], v[116:119]
	v_mfma_f32_16x16x32_bf16 v[112:115], v[186:189], v[194:197], v[112:115]
	s_waitcnt lgkmcnt(2)
	v_mfma_f32_16x16x32_bf16 v[108:111], v[170:173], v[178:181], v[108:111]
	ds_read_b128 v[194:197], v162 offset:43008
	buffer_load_dwordx4 v[12:15], v160, s[12:15], s25 offen
	s_waitcnt vmcnt(11)
	v_cvt_pk_bf16_f32 v3, v2, v3
	v_cvt_pk_bf16_f32 v2, v0, v1
	v_mfma_f32_16x16x32_bf16 v[104:107], v[174:177], v[178:181], v[104:107]
	ds_write_b64 v161, v[2:3] offset:8704
	v_mfma_f32_16x16x32_bf16 v[100:103], v[182:185], v[178:181], v[100:103]
	v_mfma_f32_16x16x32_bf16 v[96:99], v[186:189], v[178:181], v[96:99]
	s_add_i32 s26, s9, 0xfff40000
	s_waitcnt lgkmcnt(2)
; #define G_DMA_A(kt, AO) do { G_DMA1(kt, AO, 0); G_DMA1(kt, AO, 1); G_DMA1(kt, AO, 2); G_DMA1(kt, AO, 3); if (MF == 9) G_DMA5(kt, AO); } while (0)
; #define G_ISSUE_B(kt) do { const unsigned _sb = (unsigned)(kt) * 4u * kstepB; \
;         _Pragma("unroll") for (int _i = 0; _i < 8; ++_i) sb[_i] = bload16(_i < 4 ? rsB0 : rsB1, vob, _sb + (_i & 3) * kstepB); } while (0)
; #define G_WRITE_B(BO) do { \
;         _Pragma("unroll") for (int _i = 0; _i < 8; ++_i) *(LAS u32x2*)(b_wr + (BO) + (_i & 3) * (16 * G_BSTRIDE) + (_i >> 2) * SLAB1) = pack4(__builtin_bit_cast(f32x4, sb[_i])); } while (0)
; #define G_ENDTILE(VM) do { asm volatile("s_waitcnt vmcnt(" #VM ")" ::: "memory"); \
;         asm volatile("s_waitcnt lgkmcnt(0)" ::: "memory"); __builtin_amdgcn_s_barrier(); asm volatile("" ::: "memory"); } while (0)
;     ...
;     __builtin_amdgcn_s_barrier();
;     G_DMA_A(0, G_A0); G_ISSUE_B(0); G_WRITE_B(G_B0);
;     __builtin_amdgcn_sched_barrier(0);
;     G_ISSUE_B(1);
;     __builtin_amdgcn_sched_barrier(0);
;     G_ENDTILE(8);
;     for (int ui = 0;; ++ui) {
; #pragma unroll
;         for (int m = 0; m < MF; ++m)
; #pragma unroll
;             for (int n = 0; n < 4; ++n) acc[m][n] = (f32x4){0.f, 0.f, 0.f, 0.f};
;         for (int t = 0; t < nt - 2; t += 2) {
;             G_TILE(G_A0, G_B0, true, G_B1, G_A1, t + 1, true, t + 2, (void)0);
;             G_ENDTILE(8);
;             G_TILE(G_A1, G_B1, true, G_B0, G_A0, t + 2, true, t + 3, (void)0);
;             G_ENDTILE(8);
;         }
	v_mfma_f32_16x16x32_bf16 v[92:95], v[170:173], v[190:193], v[92:95]
	ds_read_b128 v[178:181], v162 offset:45056
	v_mfma_f32_16x16x32_bf16 v[88:91], v[174:177], v[190:193], v[88:91]
	v_mfma_f32_16x16x32_bf16 v[84:87], v[182:185], v[190:193], v[84:87]
	v_mfma_f32_16x16x32_bf16 v[80:83], v[186:189], v[190:193], v[80:83]
	s_waitcnt lgkmcnt(2)
	v_mfma_f32_16x16x32_bf16 v[76:79], v[170:173], v[194:197], v[76:79]
	ds_read_b128 v[190:193], v162 offset:47104
	buffer_load_dwordx4 v[0:3], v160, s[12:15], s26 offen
	s_waitcnt vmcnt(11)
	v_cvt_pk_bf16_f32 v31, v30, v31
	v_cvt_pk_bf16_f32 v30, v28, v29
	v_mfma_f32_16x16x32_bf16 v[72:75], v[174:177], v[194:197], v[72:75]
	ds_write_b64 v161, v[30:31] offset:17408
	v_mfma_f32_16x16x32_bf16 v[68:71], v[182:185], v[194:197], v[68:71]
	v_mfma_f32_16x16x32_bf16 v[64:67], v[186:189], v[194:197], v[64:67]
	s_add_i32 s27, s9, 0xfffa0000
	s_waitcnt lgkmcnt(2)
	v_mfma_f32_16x16x32_bf16 v[60:63], v[170:173], v[178:181], v[60:63]
	ds_read_b128 v[194:197], v162 offset:33792
	v_mfma_f32_16x16x32_bf16 v[56:59], v[174:177], v[178:181], v[56:59]
	v_mfma_f32_16x16x32_bf16 v[52:55], v[182:185], v[178:181], v[52:55]
	v_mfma_f32_16x16x32_bf16 v[48:51], v[186:189], v[178:181], v[48:51]
	s_waitcnt lgkmcnt(2)
	v_mfma_f32_16x16x32_bf16 v[44:47], v[170:173], v[190:193], v[44:47]
	ds_read_b128 v[170:173], v162 offset:35840
	buffer_load_dwordx4 v[28:31], v160, s[12:15], s27 offen
	s_waitcnt vmcnt(11)
	v_cvt_pk_bf16_f32 v27, v26, v27
	v_cvt_pk_bf16_f32 v26, v24, v25
	v_mfma_f32_16x16x32_bf16 v[40:43], v[174:177], v[190:193], v[40:43]
	ds_read_b64_tr_b16 v[244:245], v166 offset:52224
	ds_read_b64_tr_b16 v[248:249], v166 offset:52256
	ds_read_b64_tr_b16 v[198:199], v166 offset:52288
	ds_read_b64_tr_b16 v[202:203], v166 offset:52320
	ds_read_b64_tr_b16 v[246:247], v167 offset:52224
	ds_read_b64_tr_b16 v[250:251], v167 offset:52256
	ds_read_b64_tr_b16 v[200:201], v167 offset:52288
	ds_read_b64_tr_b16 v[204:205], v167 offset:52320
	ds_write_b64 v161, v[26:27] offset:26112
	v_mfma_f32_16x16x32_bf16 v[36:39], v[182:185], v[190:193], v[36:39]
	v_mfma_f32_16x16x32_bf16 v[32:35], v[186:189], v[190:193], v[32:35]
	s_waitcnt lgkmcnt(4)
	v_mfma_f32_16x16x32_bf16 v[156:159], v[244:247], v[194:197], v[156:159]
	ds_read_b128 v[182:185], v162 offset:37888
	s_waitcnt lgkmcnt(4)
	v_mfma_f32_16x16x32_bf16 v[152:155], v[248:251], v[194:197], v[152:155]
	s_waitcnt lgkmcnt(3)
	v_mfma_f32_16x16x32_bf16 v[148:151], v[198:201], v[194:197], v[148:151]
	s_waitcnt lgkmcnt(2)
	v_mfma_f32_16x16x32_bf16 v[144:147], v[202:205], v[194:197], v[144:147]
	v_mfma_f32_16x16x32_bf16 v[140:143], v[244:247], v[170:173], v[140:143]
	ds_read_b128 v[186:189], v162 offset:39936
	buffer_load_dwordx4 v[24:27], v160, s[12:15], s9 offen
	s_waitcnt vmcnt(11)
	v_cvt_pk_bf16_f32 v23, v22, v23
	v_cvt_pk_bf16_f32 v22, v20, v21
	v_mfma_f32_16x16x32_bf16 v[136:139], v[248:251], v[170:173], v[136:139]
	ds_write_b64 v161, v[22:23] offset:256
	v_mfma_f32_16x16x32_bf16 v[132:135], v[198:201], v[170:173], v[132:135]
	v_mfma_f32_16x16x32_bf16 v[128:131], v[202:205], v[170:173], v[128:131]
	s_waitcnt lgkmcnt(2)
	v_mfma_f32_16x16x32_bf16 v[124:127], v[244:247], v[182:185], v[124:127]
	ds_read_b128 v[170:173], v162 offset:41984
	v_mfma_f32_16x16x32_bf16 v[120:123], v[248:251], v[182:185], v[120:123]
	v_mfma_f32_16x16x32_bf16 v[116:119], v[198:201], v[182:185], v[116:119]
	v_mfma_f32_16x16x32_bf16 v[112:115], v[202:205], v[182:185], v[112:115]
	s_waitcnt lgkmcnt(2)
	v_mfma_f32_16x16x32_bf16 v[108:111], v[244:247], v[186:189], v[108:111]
	ds_read_b128 v[182:185], v162 offset:44032
	buffer_load_dwordx4 v[20:23], v160, s[16:19], s25 offen
	s_waitcnt vmcnt(11)
	v_cvt_pk_bf16_f32 v7, v6, v7
	v_cvt_pk_bf16_f32 v6, v4, v5
	v_mfma_f32_16x16x32_bf16 v[104:107], v[248:251], v[186:189], v[104:107]
	ds_write_b64 v161, v[6:7] offset:8960
	v_mfma_f32_16x16x32_bf16 v[100:103], v[198:201], v[186:189], v[100:103]
	v_mfma_f32_16x16x32_bf16 v[96:99], v[202:205], v[186:189], v[96:99]
	s_waitcnt lgkmcnt(2)
	v_mfma_f32_16x16x32_bf16 v[92:95], v[244:247], v[170:173], v[92:95]
	ds_read_b128 v[186:189], v162 offset:46080
	v_mfma_f32_16x16x32_bf16 v[88:91], v[248:251], v[170:173], v[88:91]
	v_mfma_f32_16x16x32_bf16 v[84:87], v[198:201], v[170:173], v[84:87]
	v_mfma_f32_16x16x32_bf16 v[80:83], v[202:205], v[170:173], v[80:83]
	s_waitcnt lgkmcnt(2)
	v_mfma_f32_16x16x32_bf16 v[76:79], v[244:247], v[182:185], v[76:79]
	ds_read_b128 v[252:255], v162 offset:48128
	buffer_load_dwordx4 v[4:7], v160, s[16:19], s26 offen
	s_waitcnt vmcnt(11)
	v_cvt_pk_bf16_f32 v11, v10, v11
	v_cvt_pk_bf16_f32 v10, v8, v9
	v_mfma_f32_16x16x32_bf16 v[72:75], v[248:251], v[182:185], v[72:75]
	ds_write_b64 v161, v[10:11] offset:17664
	v_mfma_f32_16x16x32_bf16 v[68:71], v[198:201], v[182:185], v[68:71]
	v_mfma_f32_16x16x32_bf16 v[64:67], v[202:205], v[182:185], v[64:67]
	s_waitcnt lgkmcnt(2)
	v_mfma_f32_16x16x32_bf16 v[60:63], v[244:247], v[186:189], v[60:63]
	buffer_load_dwordx4 v[8:11], v160, s[16:19], s27 offen
	s_waitcnt vmcnt(11)
	v_cvt_pk_bf16_f32 v19, v18, v19
	v_cvt_pk_bf16_f32 v18, v16, v17
	v_mfma_f32_16x16x32_bf16 v[56:59], v[248:251], v[186:189], v[56:59]
	ds_write_b64 v161, v[18:19] offset:26368
	v_mfma_f32_16x16x32_bf16 v[52:55], v[198:201], v[186:189], v[52:55]
	buffer_load_dwordx4 v[16:19], v160, s[16:19], s9 offen
	v_mfma_f32_16x16x32_bf16 v[48:51], v[202:205], v[186:189], v[48:51]
	s_add_i32 s8, s8, 2
	s_add_i32 s9, s9, 0x300000
	s_addk_i32 s24, 0x100
	s_cmp_ge_i32 s8, s64
	s_waitcnt vmcnt(8)
	s_waitcnt lgkmcnt(0)
	s_barrier
	s_cbranch_scc0 .LBB0_71

; #define G_DMA_A(kt, AO) do { G_DMA1(kt, AO, 0); G_DMA1(kt, AO, 1); G_DMA1(kt, AO, 2); G_DMA1(kt, AO, 3); if (MF == 9) G_DMA5(kt, AO); } while (0)
; #define G_ISSUE_B(kt) do { const unsigned _sb = (unsigned)(kt) * 4u * kstepB; \
;         _Pragma("unroll") for (int _i = 0; _i < 8; ++_i) sb[_i] = bload16(_i < 4 ? rsB0 : rsB1, vob, _sb + (_i & 3) * kstepB); } while (0)
; #define G_WRITE_B(BO) do { \
;         _Pragma("unroll") for (int _i = 0; _i < 8; ++_i) *(LAS u32x2*)(b_wr + (BO) + (_i & 3) * (16 * G_BSTRIDE) + (_i >> 2) * SLAB1) = pack4(__builtin_bit_cast(f32x4, sb[_i])); } while (0)
; #define G_ENDTILE(VM) do { asm volatile("s_waitcnt vmcnt(" #VM ")" ::: "memory"); \
;         asm volatile("s_waitcnt lgkmcnt(0)" ::: "memory"); __builtin_amdgcn_s_barrier(); asm volatile("" ::: "memory"); } while (0)
;     ...
;     __builtin_amdgcn_s_barrier();
;     G_DMA_A(0, G_A0); G_ISSUE_B(0); G_WRITE_B(G_B0);
;     __builtin_amdgcn_sched_barrier(0);
;     G_ISSUE_B(1);
;     __builtin_amdgcn_sched_barrier(0);
;     G_ENDTILE(8);
;     for (int ui = 0;; ++ui) {
; #pragma unroll
;         for (int m = 0; m < MF; ++m)
; #pragma unroll
;             for (int n = 0; n < 4; ++n) acc[m][n] = (f32x4){0.f, 0.f, 0.f, 0.f};
;         for (int t = 0; t < nt - 2; t += 2) {
;             G_TILE(G_A0, G_B0, true, G_B1, G_A1, t + 1, true, t + 2, (void)0);
.LBB0_376:
	s_andn2_b64 vcc, exec, s[30:31]
	v_mov_b32_e32 v159, 0
	s_cbranch_vccnz .LBB0_379
	s_mov_b32 s8, 0
	s_mov_b32 s9, 0x1e0000
	s_movk_i32 s24, 0x100
	s_mov_b32 m0, s72
	s_add_i32 s25, s24, 0xffffff80
	ds_read_b64_tr_b16 v[170:171], v165
	ds_read_b64_tr_b16 v[172:173], v166
	ds_read_b64_tr_b16 v[176:177], v166 offset:32
	ds_read_b128 v[178:181], v162
	ds_read_b64_tr_b16 v[174:175], v165 offset:32
	ds_read_b64_tr_b16 v[182:183], v165 offset:64
	ds_read_b64_tr_b16 v[186:187], v165 offset:96
	ds_read_b64_tr_b16 v[184:185], v166 offset:64
	ds_read_b64_tr_b16 v[188:189], v166 offset:96
	ds_read_b128 v[190:193], v162 offset:2048
	ds_read_b128 v[198:201], v162 offset:4096
	buffer_load_dwordx4 v163, s[20:23], s25 offen lds
	s_mov_b32 m0, s71
	s_waitcnt lgkmcnt(7)
	v_mfma_f32_16x16x32_bf16 v[156:159], v[170:173], v[178:181], 0
	buffer_load_dwordx4 v164, s[20:23], s25 offen lds
	s_waitcnt lgkmcnt(6)
	v_mfma_f32_16x16x32_bf16 v[152:155], v[174:177], v[178:181], 0
	s_waitcnt lgkmcnt(3)
	v_mfma_f32_16x16x32_bf16 v[148:151], v[182:185], v[178:181], 0
	s_waitcnt lgkmcnt(2)
	v_mfma_f32_16x16x32_bf16 v[144:147], v[186:189], v[178:181], 0
	s_waitcnt lgkmcnt(1)
	v_mfma_f32_16x16x32_bf16 v[140:143], v[170:173], v[190:193], 0
	s_mov_b32 m0, s70
	s_nop 0
	buffer_load_dwordx4 v167, s[20:23], s25 offen lds
	ds_read_b128 v[178:181], v162 offset:6144
	s_waitcnt vmcnt(10)
	v_cvt_pk_bf16_f32 v15, v14, v15
	v_cvt_pk_bf16_f32 v14, v12, v13
	v_mfma_f32_16x16x32_bf16 v[136:139], v[174:177], v[190:193], 0
	ds_write_b64 v161, v[14:15] offset:34816
	v_mfma_f32_16x16x32_bf16 v[132:135], v[182:185], v[190:193], 0
	s_mov_b32 m0, s68
	s_nop 0
	buffer_load_dwordx4 v168, s[20:23], s25 offen lds
	s_add_i32 s25, s9, 0xfff20000
	v_mfma_f32_16x16x32_bf16 v[128:131], v[186:189], v[190:193], 0
	s_waitcnt lgkmcnt(2)
	v_mfma_f32_16x16x32_bf16 v[124:127], v[170:173], v[198:201], 0
	ds_read_b128 v[190:193], v162 offset:8192
	v_mfma_f32_16x16x32_bf16 v[120:123], v[174:177], v[198:201], 0
	v_mfma_f32_16x16x32_bf16 v[116:119], v[182:185], v[198:201], 0
	v_mfma_f32_16x16x32_bf16 v[112:115], v[186:189], v[198:201], 0
	s_waitcnt lgkmcnt(2)
	v_mfma_f32_16x16x32_bf16 v[108:111], v[170:173], v[178:181], 0
	ds_read_b128 v[198:201], v162 offset:10240
	buffer_load_dwordx4 v[12:15], v160, s[12:15], s25 offen
	s_waitcnt vmcnt(10)
	v_cvt_pk_bf16_f32 v31, v30, v31
	v_cvt_pk_bf16_f32 v30, v28, v29
	v_mfma_f32_16x16x32_bf16 v[104:107], v[174:177], v[178:181], 0
	ds_write_b64 v161, v[30:31] offset:43520
	v_mfma_f32_16x16x32_bf16 v[100:103], v[182:185], v[178:181], 0
	v_mfma_f32_16x16x32_bf16 v[96:99], v[186:189], v[178:181], 0
	s_add_i32 s26, s9, 0xfff40000
	s_waitcnt lgkmcnt(2)
	v_mfma_f32_16x16x32_bf16 v[92:95], v[170:173], v[190:193], 0
	ds_read_b128 v[178:181], v162 offset:12288
	v_mfma_f32_16x16x32_bf16 v[88:91], v[174:177], v[190:193], 0
	v_mfma_f32_16x16x32_bf16 v[84:87], v[182:185], v[190:193], 0
	v_mfma_f32_16x16x32_bf16 v[80:83], v[186:189], v[190:193], 0
	s_waitcnt lgkmcnt(2)
	v_mfma_f32_16x16x32_bf16 v[76:79], v[170:173], v[198:201], 0
	ds_read_b128 v[190:193], v162 offset:14336
	v_cvt_pk_bf16_f32 v7, v6, v7
	v_cvt_pk_bf16_f32 v6, v4, v5
	v_mfma_f32_16x16x32_bf16 v[72:75], v[174:177], v[198:201], 0
	ds_write_b64 v161, v[6:7] offset:52224
	v_mfma_f32_16x16x32_bf16 v[68:71], v[182:185], v[198:201], 0
	v_mfma_f32_16x16x32_bf16 v[64:67], v[186:189], v[198:201], 0
	s_add_i32 s27, s9, 0xfff60000
	buffer_load_dwordx4 v[28:31], v160, s[12:15], s26 offen
	s_waitcnt lgkmcnt(2)
	v_mfma_f32_16x16x32_bf16 v[60:63], v[170:173], v[178:181], 0
	ds_read_b128 v[198:201], v162 offset:1024
	v_mfma_f32_16x16x32_bf16 v[56:59], v[174:177], v[178:181], 0
	v_mfma_f32_16x16x32_bf16 v[52:55], v[182:185], v[178:181], 0
	v_mfma_f32_16x16x32_bf16 v[48:51], v[186:189], v[178:181], 0
	s_waitcnt lgkmcnt(2)
	v_mfma_f32_16x16x32_bf16 v[44:47], v[170:173], v[190:193], 0
	ds_read_b128 v[170:173], v162 offset:3072
	buffer_load_dwordx4 v[4:7], v160, s[12:15], s27 offen
	s_waitcnt vmcnt(11)
	v_cvt_pk_bf16_f32 v27, v26, v27
	v_cvt_pk_bf16_f32 v26, v24, v25
	v_mfma_f32_16x16x32_bf16 v[40:43], v[174:177], v[190:193], 0
	ds_read_b64_tr_b16 v[244:245], v165 offset:17408
	ds_read_b64_tr_b16 v[248:249], v165 offset:17440
	ds_read_b64_tr_b16 v[202:203], v165 offset:17472
	ds_read_b64_tr_b16 v[206:207], v165 offset:17504
	ds_read_b64_tr_b16 v[246:247], v166 offset:17408
	ds_read_b64_tr_b16 v[250:251], v166 offset:17440
	ds_read_b64_tr_b16 v[204:205], v166 offset:17472
	ds_read_b64_tr_b16 v[208:209], v166 offset:17504
	ds_write_b64 v161, v[26:27] offset:60928
	v_mfma_f32_16x16x32_bf16 v[36:39], v[182:185], v[190:193], 0
	v_mfma_f32_16x16x32_bf16 v[32:35], v[186:189], v[190:193], 0
	s_add_i32 s45, s9, 0xfff80000
	s_waitcnt lgkmcnt(4)
	v_mfma_f32_16x16x32_bf16 v[156:159], v[244:247], v[198:201], v[156:159]
	ds_read_b128 v[182:185], v162 offset:5120
	s_waitcnt lgkmcnt(4)
	v_mfma_f32_16x16x32_bf16 v[152:155], v[248:251], v[198:201], v[152:155]
	s_waitcnt lgkmcnt(3)
	v_mfma_f32_16x16x32_bf16 v[148:151], v[202:205], v[198:201], v[148:151]
	s_waitcnt lgkmcnt(2)
	v_mfma_f32_16x16x32_bf16 v[144:147], v[206:209], v[198:201], v[144:147]
	v_mfma_f32_16x16x32_bf16 v[140:143], v[244:247], v[170:173], v[140:143]
	ds_read_b128 v[186:189], v162 offset:7168
	buffer_load_dwordx4 v[24:27], v160, s[12:15], s45 offen
	s_waitcnt vmcnt(11)
	v_cvt_pk_bf16_f32 v23, v22, v23
	v_cvt_pk_bf16_f32 v22, v20, v21
	v_mfma_f32_16x16x32_bf16 v[136:139], v[248:251], v[170:173], v[136:139]
	ds_write_b64 v161, v[22:23] offset:35072
	v_mfma_f32_16x16x32_bf16 v[132:135], v[202:205], v[170:173], v[132:135]
	v_mfma_f32_16x16x32_bf16 v[128:131], v[206:209], v[170:173], v[128:131]
	s_waitcnt lgkmcnt(2)
; #define G_DMA_A(kt, AO) do { G_DMA1(kt, AO, 0); G_DMA1(kt, AO, 1); G_DMA1(kt, AO, 2); G_DMA1(kt, AO, 3); if (MF == 9) G_DMA5(kt, AO); } while (0)
; #define G_ISSUE_B(kt) do { const unsigned _sb = (unsigned)(kt) * 4u * kstepB; \
;         _Pragma("unroll") for (int _i = 0; _i < 8; ++_i) sb[_i] = bload16(_i < 4 ? rsB0 : rsB1, vob, _sb + (_i & 3) * kstepB); } while (0)
; #define G_WRITE_B(BO) do { \
;         _Pragma("unroll") for (int _i = 0; _i < 8; ++_i) *(LAS u32x2*)(b_wr + (BO) + (_i & 3) * (16 * G_BSTRIDE) + (_i >> 2) * SLAB1) = pack4(__builtin_bit_cast(f32x4, sb[_i])); } while (0)
; #define G_ENDTILE(VM) do { asm volatile("s_waitcnt vmcnt(" #VM ")" ::: "memory"); \
;         asm volatile("s_waitcnt lgkmcnt(0)" ::: "memory"); __builtin_amdgcn_s_barrier(); asm volatile("" ::: "memory"); } while (0)
;     ...
;     __builtin_amdgcn_s_barrier();
;     G_DMA_A(0, G_A0); G_ISSUE_B(0); G_WRITE_B(G_B0);
;     __builtin_amdgcn_sched_barrier(0);
;     G_ISSUE_B(1);
;     __builtin_amdgcn_sched_barrier(0);
;     G_ENDTILE(8);
;     for (int ui = 0;; ++ui) {
; #pragma unroll
;         for (int m = 0; m < MF; ++m)
; #pragma unroll
;             for (int n = 0; n < 4; ++n) acc[m][n] = (f32x4){0.f, 0.f, 0.f, 0.f};
;         for (int t = 0; t < nt - 2; t += 2) {
;             G_TILE(G_A0, G_B0, true, G_B1, G_A1, t + 1, true, t + 2, (void)0);
;             G_ENDTILE(8);
;             G_TILE(G_A1, G_B1, true, G_B0, G_A0, t + 2, true, t + 3, (void)0);
	v_mfma_f32_16x16x32_bf16 v[124:127], v[244:247], v[182:185], v[124:127]
	ds_read_b128 v[170:173], v162 offset:9216
	v_mfma_f32_16x16x32_bf16 v[120:123], v[248:251], v[182:185], v[120:123]
	v_mfma_f32_16x16x32_bf16 v[116:119], v[202:205], v[182:185], v[116:119]
	v_mfma_f32_16x16x32_bf16 v[112:115], v[206:209], v[182:185], v[112:115]
	s_waitcnt lgkmcnt(2)
	v_mfma_f32_16x16x32_bf16 v[108:111], v[244:247], v[186:189], v[108:111]
	ds_read_b128 v[182:185], v162 offset:11264
	buffer_load_dwordx4 v[20:23], v160, s[16:19], s25 offen
	s_waitcnt vmcnt(10)
	v_cvt_pk_bf16_f32 v11, v10, v11
	v_cvt_pk_bf16_f32 v10, v8, v9
	v_mfma_f32_16x16x32_bf16 v[104:107], v[248:251], v[186:189], v[104:107]
	ds_write_b64 v161, v[10:11] offset:43776
	v_mfma_f32_16x16x32_bf16 v[100:103], v[202:205], v[186:189], v[100:103]
	v_mfma_f32_16x16x32_bf16 v[96:99], v[206:209], v[186:189], v[96:99]
	s_waitcnt lgkmcnt(2)
	v_mfma_f32_16x16x32_bf16 v[92:95], v[244:247], v[170:173], v[92:95]
	ds_read_b128 v[186:189], v162 offset:13312
	v_mfma_f32_16x16x32_bf16 v[88:91], v[248:251], v[170:173], v[88:91]
	v_mfma_f32_16x16x32_bf16 v[84:87], v[202:205], v[170:173], v[84:87]
	v_mfma_f32_16x16x32_bf16 v[80:83], v[206:209], v[170:173], v[80:83]
	s_waitcnt lgkmcnt(2)
	v_mfma_f32_16x16x32_bf16 v[76:79], v[244:247], v[182:185], v[76:79]
	ds_read_b128 v[252:255], v162 offset:15360
	v_cvt_pk_bf16_f32 v3, v2, v3
	v_cvt_pk_bf16_f32 v2, v0, v1
	v_mfma_f32_16x16x32_bf16 v[72:75], v[248:251], v[182:185], v[72:75]
	ds_write_b64 v161, v[2:3] offset:52480
	v_mfma_f32_16x16x32_bf16 v[68:71], v[202:205], v[182:185], v[68:71]
	v_mfma_f32_16x16x32_bf16 v[64:67], v[206:209], v[182:185], v[64:67]
	buffer_load_dwordx4 v[8:11], v160, s[16:19], s26 offen
	s_waitcnt lgkmcnt(2)
	v_mfma_f32_16x16x32_bf16 v[60:63], v[244:247], v[186:189], v[60:63]
	buffer_load_dwordx4 v[0:3], v160, s[16:19], s27 offen
	s_waitcnt vmcnt(11)
	v_cvt_pk_bf16_f32 v19, v18, v19
	v_cvt_pk_bf16_f32 v18, v16, v17
	v_mfma_f32_16x16x32_bf16 v[56:59], v[248:251], v[186:189], v[56:59]
	ds_write_b64 v161, v[18:19] offset:61184
	v_mfma_f32_16x16x32_bf16 v[52:55], v[202:205], v[186:189], v[52:55]
	buffer_load_dwordx4 v[16:19], v160, s[16:19], s45 offen
	v_mfma_f32_16x16x32_bf16 v[48:51], v[206:209], v[186:189], v[48:51]
	s_waitcnt vmcnt(8)
	s_mov_b32 m0, s59
	s_waitcnt lgkmcnt(0)
	s_barrier
	ds_read_b64_tr_b16 v[170:171], v165 offset:34816
	ds_read_b64_tr_b16 v[172:173], v166 offset:34816
	ds_read_b64_tr_b16 v[176:177], v166 offset:34848
	ds_read_b128 v[178:181], v162 offset:32768
	ds_read_b64_tr_b16 v[174:175], v165 offset:34848
	ds_read_b64_tr_b16 v[182:183], v165 offset:34880
	ds_read_b64_tr_b16 v[186:187], v165 offset:34912
	ds_read_b64_tr_b16 v[184:185], v166 offset:34880
	ds_read_b64_tr_b16 v[188:189], v166 offset:34912
	ds_read_b128 v[190:193], v162 offset:34816
	ds_read_b128 v[198:201], v162 offset:36864
	buffer_load_dwordx4 v163, s[20:23], s24 offen lds
	s_mov_b32 m0, s60
	v_mfma_f32_16x16x32_bf16 v[44:47], v[244:247], v[252:255], v[44:47]
	v_mfma_f32_16x16x32_bf16 v[40:43], v[248:251], v[252:255], v[40:43]
	v_mfma_f32_16x16x32_bf16 v[36:39], v[202:205], v[252:255], v[36:39]
	v_mfma_f32_16x16x32_bf16 v[32:35], v[206:209], v[252:255], v[32:35]
	s_waitcnt lgkmcnt(7)
	v_mfma_f32_16x16x32_bf16 v[156:159], v[170:173], v[178:181], v[156:159]
	buffer_load_dwordx4 v164, s[20:23], s24 offen lds
	s_add_i32 s25, s9, 0xfffa0000
	s_waitcnt lgkmcnt(6)
	v_mfma_f32_16x16x32_bf16 v[152:155], v[174:177], v[178:181], v[152:155]
	s_waitcnt lgkmcnt(3)
	v_mfma_f32_16x16x32_bf16 v[148:151], v[182:185], v[178:181], v[148:151]
	s_waitcnt lgkmcnt(2)
	v_mfma_f32_16x16x32_bf16 v[144:147], v[186:189], v[178:181], v[144:147]
	s_waitcnt lgkmcnt(1)
	v_mfma_f32_16x16x32_bf16 v[140:143], v[170:173], v[190:193], v[140:143]
	s_mov_b32 m0, s61
	s_nop 0
	buffer_load_dwordx4 v167, s[20:23], s24 offen lds
	ds_read_b128 v[178:181], v162 offset:38912
	s_waitcnt vmcnt(10)
	v_cvt_pk_bf16_f32 v15, v14, v15
	v_cvt_pk_bf16_f32 v14, v12, v13
	v_mfma_f32_16x16x32_bf16 v[136:139], v[174:177], v[190:193], v[136:139]
	ds_write_b64 v161, v[14:15]
	v_mfma_f32_16x16x32_bf16 v[132:135], v[182:185], v[190:193], v[132:135]
	s_mov_b32 m0, s62
	s_nop 0
	buffer_load_dwordx4 v168, s[20:23], s24 offen lds
	v_mfma_f32_16x16x32_bf16 v[128:131], v[186:189], v[190:193], v[128:131]
	s_waitcnt lgkmcnt(2)
	v_mfma_f32_16x16x32_bf16 v[124:127], v[170:173], v[198:201], v[124:127]
	ds_read_b128 v[190:193], v162 offset:40960
	v_mfma_f32_16x16x32_bf16 v[120:123], v[174:177], v[198:201], v[120:123]
	v_mfma_f32_16x16x32_bf16 v[116:119], v[182:185], v[198:201], v[116:119]
	v_mfma_f32_16x16x32_bf16 v[112:115], v[186:189], v[198:201], v[112:115]
	s_waitcnt lgkmcnt(2)
	v_mfma_f32_16x16x32_bf16 v[108:111], v[170:173], v[178:181], v[108:111]
	ds_read_b128 v[198:201], v162 offset:43008
	buffer_load_dwordx4 v[12:15], v160, s[12:15], s25 offen
	s_waitcnt vmcnt(11)
	v_cvt_pk_bf16_f32 v31, v30, v31
	v_cvt_pk_bf16_f32 v30, v28, v29
	v_mfma_f32_16x16x32_bf16 v[104:107], v[174:177], v[178:181], v[104:107]
	ds_write_b64 v161, v[30:31] offset:8704
	v_mfma_f32_16x16x32_bf16 v[100:103], v[182:185], v[178:181], v[100:103]
	v_mfma_f32_16x16x32_bf16 v[96:99], v[186:189], v[178:181], v[96:99]
	s_add_i32 s26, s9, 0xfffc0000
	s_waitcnt lgkmcnt(2)
	v_mfma_f32_16x16x32_bf16 v[92:95], v[170:173], v[190:193], v[92:95]
	ds_read_b128 v[178:181], v162 offset:45056
	v_mfma_f32_16x16x32_bf16 v[88:91], v[174:177], v[190:193], v[88:91]
	v_mfma_f32_16x16x32_bf16 v[84:87], v[182:185], v[190:193], v[84:87]
	v_mfma_f32_16x16x32_bf16 v[80:83], v[186:189], v[190:193], v[80:83]
	s_waitcnt lgkmcnt(2)
; #define G_DMA_A(kt, AO) do { G_DMA1(kt, AO, 0); G_DMA1(kt, AO, 1); G_DMA1(kt, AO, 2); G_DMA1(kt, AO, 3); if (MF == 9) G_DMA5(kt, AO); } while (0)
; #define G_ISSUE_B(kt) do { const unsigned _sb = (unsigned)(kt) * 4u * kstepB; \
;         _Pragma("unroll") for (int _i = 0; _i < 8; ++_i) sb[_i] = bload16(_i < 4 ? rsB0 : rsB1, vob, _sb + (_i & 3) * kstepB); } while (0)
; #define G_WRITE_B(BO) do { \
;         _Pragma("unroll") for (int _i = 0; _i < 8; ++_i) *(LAS u32x2*)(b_wr + (BO) + (_i & 3) * (16 * G_BSTRIDE) + (_i >> 2) * SLAB1) = pack4(__builtin_bit_cast(f32x4, sb[_i])); } while (0)
; #define G_ENDTILE(VM) do { asm volatile("s_waitcnt vmcnt(" #VM ")" ::: "memory"); \
;         asm volatile("s_waitcnt lgkmcnt(0)" ::: "memory"); __builtin_amdgcn_s_barrier(); asm volatile("" ::: "memory"); } while (0)
;     ...
;     __builtin_amdgcn_s_barrier();
;     G_DMA_A(0, G_A0); G_ISSUE_B(0); G_WRITE_B(G_B0);
;     __builtin_amdgcn_sched_barrier(0);
;     G_ISSUE_B(1);
;     __builtin_amdgcn_sched_barrier(0);
;     G_ENDTILE(8);
;     for (int ui = 0;; ++ui) {
; #pragma unroll
;         for (int m = 0; m < MF; ++m)
; #pragma unroll
;             for (int n = 0; n < 4; ++n) acc[m][n] = (f32x4){0.f, 0.f, 0.f, 0.f};
;         for (int t = 0; t < nt - 2; t += 2) {
;             G_TILE(G_A0, G_B0, true, G_B1, G_A1, t + 1, true, t + 2, (void)0);
;             G_ENDTILE(8);
;             G_TILE(G_A1, G_B1, true, G_B0, G_A0, t + 2, true, t + 3, (void)0);
;             G_ENDTILE(8);
;         }
	v_mfma_f32_16x16x32_bf16 v[76:79], v[170:173], v[198:201], v[76:79]
	ds_read_b128 v[190:193], v162 offset:47104
	buffer_load_dwordx4 v[28:31], v160, s[12:15], s26 offen
	s_waitcnt vmcnt(11)
	v_cvt_pk_bf16_f32 v7, v6, v7
	v_cvt_pk_bf16_f32 v6, v4, v5
	v_mfma_f32_16x16x32_bf16 v[72:75], v[174:177], v[198:201], v[72:75]
	ds_write_b64 v161, v[6:7] offset:17408
	v_mfma_f32_16x16x32_bf16 v[68:71], v[182:185], v[198:201], v[68:71]
	v_mfma_f32_16x16x32_bf16 v[64:67], v[186:189], v[198:201], v[64:67]
	s_add_i32 s27, s9, 0xfffe0000
	s_waitcnt lgkmcnt(2)
	v_mfma_f32_16x16x32_bf16 v[60:63], v[170:173], v[178:181], v[60:63]
	ds_read_b128 v[198:201], v162 offset:33792
	v_mfma_f32_16x16x32_bf16 v[56:59], v[174:177], v[178:181], v[56:59]
	v_mfma_f32_16x16x32_bf16 v[52:55], v[182:185], v[178:181], v[52:55]
	v_mfma_f32_16x16x32_bf16 v[48:51], v[186:189], v[178:181], v[48:51]
	s_waitcnt lgkmcnt(2)
	v_mfma_f32_16x16x32_bf16 v[44:47], v[170:173], v[190:193], v[44:47]
	ds_read_b128 v[170:173], v162 offset:35840
	buffer_load_dwordx4 v[4:7], v160, s[12:15], s27 offen
	s_waitcnt vmcnt(11)
	v_cvt_pk_bf16_f32 v27, v26, v27
	v_cvt_pk_bf16_f32 v26, v24, v25
	v_mfma_f32_16x16x32_bf16 v[40:43], v[174:177], v[190:193], v[40:43]
	ds_read_b64_tr_b16 v[244:245], v165 offset:52224
	ds_read_b64_tr_b16 v[248:249], v165 offset:52256
	ds_read_b64_tr_b16 v[202:203], v165 offset:52288
	ds_read_b64_tr_b16 v[206:207], v165 offset:52320
	ds_read_b64_tr_b16 v[246:247], v166 offset:52224
	ds_read_b64_tr_b16 v[250:251], v166 offset:52256
	ds_read_b64_tr_b16 v[204:205], v166 offset:52288
	ds_read_b64_tr_b16 v[208:209], v166 offset:52320
	ds_write_b64 v161, v[26:27] offset:26112
	v_mfma_f32_16x16x32_bf16 v[36:39], v[182:185], v[190:193], v[36:39]
	v_mfma_f32_16x16x32_bf16 v[32:35], v[186:189], v[190:193], v[32:35]
	s_waitcnt lgkmcnt(4)
	v_mfma_f32_16x16x32_bf16 v[156:159], v[244:247], v[198:201], v[156:159]
	ds_read_b128 v[182:185], v162 offset:37888
	s_waitcnt lgkmcnt(4)
	v_mfma_f32_16x16x32_bf16 v[152:155], v[248:251], v[198:201], v[152:155]
	s_waitcnt lgkmcnt(3)
	v_mfma_f32_16x16x32_bf16 v[148:151], v[202:205], v[198:201], v[148:151]
	s_waitcnt lgkmcnt(2)
	v_mfma_f32_16x16x32_bf16 v[144:147], v[206:209], v[198:201], v[144:147]
	v_mfma_f32_16x16x32_bf16 v[140:143], v[244:247], v[170:173], v[140:143]
	ds_read_b128 v[186:189], v162 offset:39936
	buffer_load_dwordx4 v[24:27], v160, s[12:15], s9 offen
	s_waitcnt vmcnt(11)
	v_cvt_pk_bf16_f32 v23, v22, v23
	v_cvt_pk_bf16_f32 v22, v20, v21
	v_mfma_f32_16x16x32_bf16 v[136:139], v[248:251], v[170:173], v[136:139]
	ds_write_b64 v161, v[22:23] offset:256
	v_mfma_f32_16x16x32_bf16 v[132:135], v[202:205], v[170:173], v[132:135]
	v_mfma_f32_16x16x32_bf16 v[128:131], v[206:209], v[170:173], v[128:131]
	s_waitcnt lgkmcnt(2)
	v_mfma_f32_16x16x32_bf16 v[124:127], v[244:247], v[182:185], v[124:127]
	ds_read_b128 v[170:173], v162 offset:41984
	v_mfma_f32_16x16x32_bf16 v[120:123], v[248:251], v[182:185], v[120:123]
	v_mfma_f32_16x16x32_bf16 v[116:119], v[202:205], v[182:185], v[116:119]
	v_mfma_f32_16x16x32_bf16 v[112:115], v[206:209], v[182:185], v[112:115]
	s_waitcnt lgkmcnt(2)
	v_mfma_f32_16x16x32_bf16 v[108:111], v[244:247], v[186:189], v[108:111]
	ds_read_b128 v[182:185], v162 offset:44032
	buffer_load_dwordx4 v[20:23], v160, s[16:19], s25 offen
	s_waitcnt vmcnt(11)
	v_cvt_pk_bf16_f32 v11, v10, v11
	v_cvt_pk_bf16_f32 v10, v8, v9
	v_mfma_f32_16x16x32_bf16 v[104:107], v[248:251], v[186:189], v[104:107]
	ds_write_b64 v161, v[10:11] offset:8960
	v_mfma_f32_16x16x32_bf16 v[100:103], v[202:205], v[186:189], v[100:103]
	v_mfma_f32_16x16x32_bf16 v[96:99], v[206:209], v[186:189], v[96:99]
	s_waitcnt lgkmcnt(2)
	v_mfma_f32_16x16x32_bf16 v[92:95], v[244:247], v[170:173], v[92:95]
	ds_read_b128 v[186:189], v162 offset:46080
	v_mfma_f32_16x16x32_bf16 v[88:91], v[248:251], v[170:173], v[88:91]
	v_mfma_f32_16x16x32_bf16 v[84:87], v[202:205], v[170:173], v[84:87]
	v_mfma_f32_16x16x32_bf16 v[80:83], v[206:209], v[170:173], v[80:83]
	s_waitcnt lgkmcnt(2)
	v_mfma_f32_16x16x32_bf16 v[76:79], v[244:247], v[182:185], v[76:79]
	ds_read_b128 v[252:255], v162 offset:48128
	buffer_load_dwordx4 v[8:11], v160, s[16:19], s26 offen
	s_waitcnt vmcnt(11)
	v_cvt_pk_bf16_f32 v3, v2, v3
	v_cvt_pk_bf16_f32 v2, v0, v1
	v_mfma_f32_16x16x32_bf16 v[72:75], v[248:251], v[182:185], v[72:75]
	ds_write_b64 v161, v[2:3] offset:17664
	v_mfma_f32_16x16x32_bf16 v[68:71], v[202:205], v[182:185], v[68:71]
	v_mfma_f32_16x16x32_bf16 v[64:67], v[206:209], v[182:185], v[64:67]
	s_waitcnt lgkmcnt(2)
	v_mfma_f32_16x16x32_bf16 v[60:63], v[244:247], v[186:189], v[60:63]
	buffer_load_dwordx4 v[0:3], v160, s[16:19], s27 offen
	s_waitcnt vmcnt(11)
	v_cvt_pk_bf16_f32 v19, v18, v19
	v_cvt_pk_bf16_f32 v18, v16, v17
	v_mfma_f32_16x16x32_bf16 v[56:59], v[248:251], v[186:189], v[56:59]
	ds_write_b64 v161, v[18:19] offset:26368
	v_mfma_f32_16x16x32_bf16 v[52:55], v[202:205], v[186:189], v[52:55]
	buffer_load_dwordx4 v[16:19], v160, s[16:19], s9 offen
	v_mfma_f32_16x16x32_bf16 v[48:51], v[206:209], v[186:189], v[48:51]
	s_add_i32 s8, s8, 2
	s_add_i32 s9, s9, 0x100000
	s_addk_i32 s24, 0x100
	s_cmp_ge_i32 s8, s67
	s_waitcnt vmcnt(8)
	s_waitcnt lgkmcnt(0)
	s_barrier
	s_cbranch_scc1 .Lflush_P3
; #define G_DMA_A(kt, AO) do { G_DMA1(kt, AO, 0); G_DMA1(kt, AO, 1); G_DMA1(kt, AO, 2); G_DMA1(kt, AO, 3); if (MF == 9) G_DMA5(kt, AO); } while (0)
; #define G_ISSUE_B(kt) do { const unsigned _sb = (unsigned)(kt) * 4u * kstepB; \
;         _Pragma("unroll") for (int _i = 0; _i < 8; ++_i) sb[_i] = bload16(_i < 4 ? rsB0 : rsB1, vob, _sb + (_i & 3) * kstepB); } while (0)
; #define G_WRITE_B(BO) do { \
;         _Pragma("unroll") for (int _i = 0; _i < 8; ++_i) *(LAS u32x2*)(b_wr + (BO) + (_i & 3) * (16 * G_BSTRIDE) + (_i >> 2) * SLAB1) = pack4(__builtin_bit_cast(f32x4, sb[_i])); } while (0)
; #define G_ENDTILE(VM) do { asm volatile("s_waitcnt vmcnt(" #VM ")" ::: "memory"); \
;         asm volatile("s_waitcnt lgkmcnt(0)" ::: "memory"); __builtin_amdgcn_s_barrier(); asm volatile("" ::: "memory"); } while (0)
;     ...
;     __builtin_amdgcn_s_barrier();
;     G_DMA_A(0, G_A0); G_ISSUE_B(0); G_WRITE_B(G_B0);
;     __builtin_amdgcn_sched_barrier(0);
;     G_ISSUE_B(1);
;     __builtin_amdgcn_sched_barrier(0);
;     G_ENDTILE(8);
;     for (int ui = 0;; ++ui) {
; #pragma unroll
;         for (int m = 0; m < MF; ++m)
; #pragma unroll
;             for (int n = 0; n < 4; ++n) acc[m][n] = (f32x4){0.f, 0.f, 0.f, 0.f};
;         for (int t = 0; t < nt - 2; t += 2) {
;             G_TILE(G_A0, G_B0, true, G_B1, G_A1, t + 1, true, t + 2, (void)0);
.LBB0_378:
	s_mov_b32 m0, s72
	s_add_i32 s25, s24, 0xffffff80
	ds_read_b64_tr_b16 v[170:171], v165
	ds_read_b64_tr_b16 v[172:173], v166
	ds_read_b64_tr_b16 v[176:177], v166 offset:32
	ds_read_b128 v[178:181], v162
	ds_read_b64_tr_b16 v[174:175], v165 offset:32
	ds_read_b64_tr_b16 v[182:183], v165 offset:64
	ds_read_b64_tr_b16 v[186:187], v165 offset:96
	ds_read_b64_tr_b16 v[184:185], v166 offset:64
	ds_read_b64_tr_b16 v[188:189], v166 offset:96
	ds_read_b128 v[190:193], v162 offset:2048
	ds_read_b128 v[198:201], v162 offset:4096
	buffer_load_dwordx4 v163, s[20:23], s25 offen lds
	s_mov_b32 m0, s71
	v_mfma_f32_16x16x32_bf16 v[44:47], v[244:247], v[252:255], v[44:47]
	v_mfma_f32_16x16x32_bf16 v[40:43], v[248:251], v[252:255], v[40:43]
	v_mfma_f32_16x16x32_bf16 v[36:39], v[202:205], v[252:255], v[36:39]
	v_mfma_f32_16x16x32_bf16 v[32:35], v[206:209], v[252:255], v[32:35]
	s_waitcnt lgkmcnt(7)
	v_mfma_f32_16x16x32_bf16 v[156:159], v[170:173], v[178:181], v[156:159]
	buffer_load_dwordx4 v164, s[20:23], s25 offen lds
	s_waitcnt lgkmcnt(6)
	v_mfma_f32_16x16x32_bf16 v[152:155], v[174:177], v[178:181], v[152:155]
	s_waitcnt lgkmcnt(3)
	v_mfma_f32_16x16x32_bf16 v[148:151], v[182:185], v[178:181], v[148:151]
	s_waitcnt lgkmcnt(2)
	v_mfma_f32_16x16x32_bf16 v[144:147], v[186:189], v[178:181], v[144:147]
	s_waitcnt lgkmcnt(1)
	v_mfma_f32_16x16x32_bf16 v[140:143], v[170:173], v[190:193], v[140:143]
	s_mov_b32 m0, s70
	s_nop 0
	buffer_load_dwordx4 v167, s[20:23], s25 offen lds
	ds_read_b128 v[178:181], v162 offset:6144
	s_waitcnt vmcnt(10)
	v_cvt_pk_bf16_f32 v15, v14, v15
	v_cvt_pk_bf16_f32 v14, v12, v13
	v_mfma_f32_16x16x32_bf16 v[136:139], v[174:177], v[190:193], v[136:139]
	ds_write_b64 v161, v[14:15] offset:34816
	v_mfma_f32_16x16x32_bf16 v[132:135], v[182:185], v[190:193], v[132:135]
	s_mov_b32 m0, s68
	s_nop 0
	buffer_load_dwordx4 v168, s[20:23], s25 offen lds
	s_add_i32 s25, s9, 0xfff20000
	v_mfma_f32_16x16x32_bf16 v[128:131], v[186:189], v[190:193], v[128:131]
	s_waitcnt lgkmcnt(2)
	v_mfma_f32_16x16x32_bf16 v[124:127], v[170:173], v[198:201], v[124:127]
	ds_read_b128 v[190:193], v162 offset:8192
	v_mfma_f32_16x16x32_bf16 v[120:123], v[174:177], v[198:201], v[120:123]
	v_mfma_f32_16x16x32_bf16 v[116:119], v[182:185], v[198:201], v[116:119]
	v_mfma_f32_16x16x32_bf16 v[112:115], v[186:189], v[198:201], v[112:115]
	s_waitcnt lgkmcnt(2)
	v_mfma_f32_16x16x32_bf16 v[108:111], v[170:173], v[178:181], v[108:111]
	ds_read_b128 v[198:201], v162 offset:10240
	buffer_load_dwordx4 v[12:15], v160, s[12:15], s25 offen
	s_waitcnt vmcnt(10)
	v_cvt_pk_bf16_f32 v31, v30, v31
	v_cvt_pk_bf16_f32 v30, v28, v29
	v_mfma_f32_16x16x32_bf16 v[104:107], v[174:177], v[178:181], v[104:107]
	ds_write_b64 v161, v[30:31] offset:43520
	v_mfma_f32_16x16x32_bf16 v[100:103], v[182:185], v[178:181], v[100:103]
	v_mfma_f32_16x16x32_bf16 v[96:99], v[186:189], v[178:181], v[96:99]
	s_add_i32 s26, s9, 0xfff40000
	s_waitcnt lgkmcnt(2)
	v_mfma_f32_16x16x32_bf16 v[92:95], v[170:173], v[190:193], v[92:95]
	ds_read_b128 v[178:181], v162 offset:12288
	v_mfma_f32_16x16x32_bf16 v[88:91], v[174:177], v[190:193], v[88:91]
	v_mfma_f32_16x16x32_bf16 v[84:87], v[182:185], v[190:193], v[84:87]
	v_mfma_f32_16x16x32_bf16 v[80:83], v[186:189], v[190:193], v[80:83]
	s_waitcnt lgkmcnt(2)
	v_mfma_f32_16x16x32_bf16 v[76:79], v[170:173], v[198:201], v[76:79]
	ds_read_b128 v[190:193], v162 offset:14336
	v_cvt_pk_bf16_f32 v7, v6, v7
	v_cvt_pk_bf16_f32 v6, v4, v5
	v_mfma_f32_16x16x32_bf16 v[72:75], v[174:177], v[198:201], v[72:75]
	ds_write_b64 v161, v[6:7] offset:52224
	v_mfma_f32_16x16x32_bf16 v[68:71], v[182:185], v[198:201], v[68:71]
	v_mfma_f32_16x16x32_bf16 v[64:67], v[186:189], v[198:201], v[64:67]
	s_add_i32 s27, s9, 0xfff60000
	buffer_load_dwordx4 v[28:31], v160, s[12:15], s26 offen
	s_waitcnt lgkmcnt(2)
	v_mfma_f32_16x16x32_bf16 v[60:63], v[170:173], v[178:181], v[60:63]
	ds_read_b128 v[198:201], v162 offset:1024
	v_mfma_f32_16x16x32_bf16 v[56:59], v[174:177], v[178:181], v[56:59]
	v_mfma_f32_16x16x32_bf16 v[52:55], v[182:185], v[178:181], v[52:55]
	v_mfma_f32_16x16x32_bf16 v[48:51], v[186:189], v[178:181], v[48:51]
	s_waitcnt lgkmcnt(2)
	v_mfma_f32_16x16x32_bf16 v[44:47], v[170:173], v[190:193], v[44:47]
	ds_read_b128 v[170:173], v162 offset:3072
	buffer_load_dwordx4 v[4:7], v160, s[12:15], s27 offen
	s_waitcnt vmcnt(11)
	v_cvt_pk_bf16_f32 v27, v26, v27
	v_cvt_pk_bf16_f32 v26, v24, v25
	v_mfma_f32_16x16x32_bf16 v[40:43], v[174:177], v[190:193], v[40:43]
	ds_read_b64_tr_b16 v[244:245], v165 offset:17408
	ds_read_b64_tr_b16 v[248:249], v165 offset:17440
	ds_read_b64_tr_b16 v[202:203], v165 offset:17472
	ds_read_b64_tr_b16 v[206:207], v165 offset:17504
	ds_read_b64_tr_b16 v[246:247], v166 offset:17408
	ds_read_b64_tr_b16 v[250:251], v166 offset:17440
	ds_read_b64_tr_b16 v[204:205], v166 offset:17472
	ds_read_b64_tr_b16 v[208:209], v166 offset:17504
	ds_write_b64 v161, v[26:27] offset:60928
	v_mfma_f32_16x16x32_bf16 v[36:39], v[182:185], v[190:193], v[36:39]
	v_mfma_f32_16x16x32_bf16 v[32:35], v[186:189], v[190:193], v[32:35]
	s_add_i32 s45, s9, 0xfff80000
	s_waitcnt lgkmcnt(4)
	v_mfma_f32_16x16x32_bf16 v[156:159], v[244:247], v[198:201], v[156:159]
	ds_read_b128 v[182:185], v162 offset:5120
	s_waitcnt lgkmcnt(4)
	v_mfma_f32_16x16x32_bf16 v[152:155], v[248:251], v[198:201], v[152:155]
	s_waitcnt lgkmcnt(3)
	v_mfma_f32_16x16x32_bf16 v[148:151], v[202:205], v[198:201], v[148:151]
	s_waitcnt lgkmcnt(2)
	v_mfma_f32_16x16x32_bf16 v[144:147], v[206:209], v[198:201], v[144:147]
	v_mfma_f32_16x16x32_bf16 v[140:143], v[244:247], v[170:173], v[140:143]
	ds_read_b128 v[186:189], v162 offset:7168
	buffer_load_dwordx4 v[24:27], v160, s[12:15], s45 offen
	s_waitcnt vmcnt(11)
; #define G_DMA_A(kt, AO) do { G_DMA1(kt, AO, 0); G_DMA1(kt, AO, 1); G_DMA1(kt, AO, 2); G_DMA1(kt, AO, 3); if (MF == 9) G_DMA5(kt, AO); } while (0)
; #define G_ISSUE_B(kt) do { const unsigned _sb = (unsigned)(kt) * 4u * kstepB; \
;         _Pragma("unroll") for (int _i = 0; _i < 8; ++_i) sb[_i] = bload16(_i < 4 ? rsB0 : rsB1, vob, _sb + (_i & 3) * kstepB); } while (0)
; #define G_WRITE_B(BO) do { \
;         _Pragma("unroll") for (int _i = 0; _i < 8; ++_i) *(LAS u32x2*)(b_wr + (BO) + (_i & 3) * (16 * G_BSTRIDE) + (_i >> 2) * SLAB1) = pack4(__builtin_bit_cast(f32x4, sb[_i])); } while (0)
; #define G_ENDTILE(VM) do { asm volatile("s_waitcnt vmcnt(" #VM ")" ::: "memory"); \
;         asm volatile("s_waitcnt lgkmcnt(0)" ::: "memory"); __builtin_amdgcn_s_barrier(); asm volatile("" ::: "memory"); } while (0)
;     ...
;     __builtin_amdgcn_s_barrier();
;     G_DMA_A(0, G_A0); G_ISSUE_B(0); G_WRITE_B(G_B0);
;     __builtin_amdgcn_sched_barrier(0);
;     G_ISSUE_B(1);
;     __builtin_amdgcn_sched_barrier(0);
;     G_ENDTILE(8);
;     for (int ui = 0;; ++ui) {
; #pragma unroll
;         for (int m = 0; m < MF; ++m)
; #pragma unroll
;             for (int n = 0; n < 4; ++n) acc[m][n] = (f32x4){0.f, 0.f, 0.f, 0.f};
;         for (int t = 0; t < nt - 2; t += 2) {
;             G_TILE(G_A0, G_B0, true, G_B1, G_A1, t + 1, true, t + 2, (void)0);
;             G_ENDTILE(8);
;             G_TILE(G_A1, G_B1, true, G_B0, G_A0, t + 2, true, t + 3, (void)0);
	v_cvt_pk_bf16_f32 v23, v22, v23
	v_cvt_pk_bf16_f32 v22, v20, v21
	v_mfma_f32_16x16x32_bf16 v[136:139], v[248:251], v[170:173], v[136:139]
	ds_write_b64 v161, v[22:23] offset:35072
	v_mfma_f32_16x16x32_bf16 v[132:135], v[202:205], v[170:173], v[132:135]
	v_mfma_f32_16x16x32_bf16 v[128:131], v[206:209], v[170:173], v[128:131]
	s_waitcnt lgkmcnt(2)
	v_mfma_f32_16x16x32_bf16 v[124:127], v[244:247], v[182:185], v[124:127]
	ds_read_b128 v[170:173], v162 offset:9216
	v_mfma_f32_16x16x32_bf16 v[120:123], v[248:251], v[182:185], v[120:123]
	v_mfma_f32_16x16x32_bf16 v[116:119], v[202:205], v[182:185], v[116:119]
	v_mfma_f32_16x16x32_bf16 v[112:115], v[206:209], v[182:185], v[112:115]
	s_waitcnt lgkmcnt(2)
	v_mfma_f32_16x16x32_bf16 v[108:111], v[244:247], v[186:189], v[108:111]
	ds_read_b128 v[182:185], v162 offset:11264
	buffer_load_dwordx4 v[20:23], v160, s[16:19], s25 offen
	s_waitcnt vmcnt(10)
	v_cvt_pk_bf16_f32 v11, v10, v11
	v_cvt_pk_bf16_f32 v10, v8, v9
	v_mfma_f32_16x16x32_bf16 v[104:107], v[248:251], v[186:189], v[104:107]
	ds_write_b64 v161, v[10:11] offset:43776
	v_mfma_f32_16x16x32_bf16 v[100:103], v[202:205], v[186:189], v[100:103]
	v_mfma_f32_16x16x32_bf16 v[96:99], v[206:209], v[186:189], v[96:99]
	s_waitcnt lgkmcnt(2)
	v_mfma_f32_16x16x32_bf16 v[92:95], v[244:247], v[170:173], v[92:95]
	ds_read_b128 v[186:189], v162 offset:13312
	v_mfma_f32_16x16x32_bf16 v[88:91], v[248:251], v[170:173], v[88:91]
	v_mfma_f32_16x16x32_bf16 v[84:87], v[202:205], v[170:173], v[84:87]
	v_mfma_f32_16x16x32_bf16 v[80:83], v[206:209], v[170:173], v[80:83]
	s_waitcnt lgkmcnt(2)
	v_mfma_f32_16x16x32_bf16 v[76:79], v[244:247], v[182:185], v[76:79]
	ds_read_b128 v[252:255], v162 offset:15360
	v_cvt_pk_bf16_f32 v3, v2, v3
	v_cvt_pk_bf16_f32 v2, v0, v1
	v_mfma_f32_16x16x32_bf16 v[72:75], v[248:251], v[182:185], v[72:75]
	ds_write_b64 v161, v[2:3] offset:52480
	v_mfma_f32_16x16x32_bf16 v[68:71], v[202:205], v[182:185], v[68:71]
	v_mfma_f32_16x16x32_bf16 v[64:67], v[206:209], v[182:185], v[64:67]
	buffer_load_dwordx4 v[8:11], v160, s[16:19], s26 offen
	s_waitcnt lgkmcnt(2)
	v_mfma_f32_16x16x32_bf16 v[60:63], v[244:247], v[186:189], v[60:63]
	buffer_load_dwordx4 v[0:3], v160, s[16:19], s27 offen
	s_waitcnt vmcnt(11)
	v_cvt_pk_bf16_f32 v19, v18, v19
	v_cvt_pk_bf16_f32 v18, v16, v17
	v_mfma_f32_16x16x32_bf16 v[56:59], v[248:251], v[186:189], v[56:59]
	ds_write_b64 v161, v[18:19] offset:61184
	v_mfma_f32_16x16x32_bf16 v[52:55], v[202:205], v[186:189], v[52:55]
	buffer_load_dwordx4 v[16:19], v160, s[16:19], s45 offen
	v_mfma_f32_16x16x32_bf16 v[48:51], v[206:209], v[186:189], v[48:51]
	s_waitcnt vmcnt(8)
	s_mov_b32 m0, s59
	s_waitcnt lgkmcnt(0)
	s_barrier
	ds_read_b64_tr_b16 v[170:171], v165 offset:34816
	ds_read_b64_tr_b16 v[172:173], v166 offset:34816
	ds_read_b64_tr_b16 v[176:177], v166 offset:34848
	ds_read_b128 v[178:181], v162 offset:32768
	ds_read_b64_tr_b16 v[174:175], v165 offset:34848
	ds_read_b64_tr_b16 v[182:183], v165 offset:34880
	ds_read_b64_tr_b16 v[186:187], v165 offset:34912
	ds_read_b64_tr_b16 v[184:185], v166 offset:34880
	ds_read_b64_tr_b16 v[188:189], v166 offset:34912
	ds_read_b128 v[190:193], v162 offset:34816
	ds_read_b128 v[198:201], v162 offset:36864
	buffer_load_dwordx4 v163, s[20:23], s24 offen lds
	s_mov_b32 m0, s60
	v_mfma_f32_16x16x32_bf16 v[44:47], v[244:247], v[252:255], v[44:47]
	v_mfma_f32_16x16x32_bf16 v[40:43], v[248:251], v[252:255], v[40:43]
	v_mfma_f32_16x16x32_bf16 v[36:39], v[202:205], v[252:255], v[36:39]
	v_mfma_f32_16x16x32_bf16 v[32:35], v[206:209], v[252:255], v[32:35]
	s_waitcnt lgkmcnt(7)
	v_mfma_f32_16x16x32_bf16 v[156:159], v[170:173], v[178:181], v[156:159]
	buffer_load_dwordx4 v164, s[20:23], s24 offen lds
	s_add_i32 s25, s9, 0xfffa0000
	s_waitcnt lgkmcnt(6)
	v_mfma_f32_16x16x32_bf16 v[152:155], v[174:177], v[178:181], v[152:155]
	s_waitcnt lgkmcnt(3)
	v_mfma_f32_16x16x32_bf16 v[148:151], v[182:185], v[178:181], v[148:151]
	s_waitcnt lgkmcnt(2)
	v_mfma_f32_16x16x32_bf16 v[144:147], v[186:189], v[178:181], v[144:147]
	s_waitcnt lgkmcnt(1)
	v_mfma_f32_16x16x32_bf16 v[140:143], v[170:173], v[190:193], v[140:143]
	s_mov_b32 m0, s61
	s_nop 0
	buffer_load_dwordx4 v167, s[20:23], s24 offen lds
	ds_read_b128 v[178:181], v162 offset:38912
	s_waitcnt vmcnt(10)
	v_cvt_pk_bf16_f32 v15, v14, v15
	v_cvt_pk_bf16_f32 v14, v12, v13
	v_mfma_f32_16x16x32_bf16 v[136:139], v[174:177], v[190:193], v[136:139]
	ds_write_b64 v161, v[14:15]
	v_mfma_f32_16x16x32_bf16 v[132:135], v[182:185], v[190:193], v[132:135]
	s_mov_b32 m0, s62
	s_nop 0
	buffer_load_dwordx4 v168, s[20:23], s24 offen lds
	v_mfma_f32_16x16x32_bf16 v[128:131], v[186:189], v[190:193], v[128:131]
	s_waitcnt lgkmcnt(2)
	v_mfma_f32_16x16x32_bf16 v[124:127], v[170:173], v[198:201], v[124:127]
	ds_read_b128 v[190:193], v162 offset:40960
	v_mfma_f32_16x16x32_bf16 v[120:123], v[174:177], v[198:201], v[120:123]
	v_mfma_f32_16x16x32_bf16 v[116:119], v[182:185], v[198:201], v[116:119]
	v_mfma_f32_16x16x32_bf16 v[112:115], v[186:189], v[198:201], v[112:115]
	s_waitcnt lgkmcnt(2)
	v_mfma_f32_16x16x32_bf16 v[108:111], v[170:173], v[178:181], v[108:111]
	ds_read_b128 v[198:201], v162 offset:43008
	buffer_load_dwordx4 v[12:15], v160, s[12:15], s25 offen
	s_waitcnt vmcnt(11)
	v_cvt_pk_bf16_f32 v31, v30, v31
	v_cvt_pk_bf16_f32 v30, v28, v29
	v_mfma_f32_16x16x32_bf16 v[104:107], v[174:177], v[178:181], v[104:107]
	ds_write_b64 v161, v[30:31] offset:8704
	v_mfma_f32_16x16x32_bf16 v[100:103], v[182:185], v[178:181], v[100:103]
	v_mfma_f32_16x16x32_bf16 v[96:99], v[186:189], v[178:181], v[96:99]
	s_add_i32 s26, s9, 0xfffc0000
	s_waitcnt lgkmcnt(2)
; #define G_DMA_A(kt, AO) do { G_DMA1(kt, AO, 0); G_DMA1(kt, AO, 1); G_DMA1(kt, AO, 2); G_DMA1(kt, AO, 3); if (MF == 9) G_DMA5(kt, AO); } while (0)
; #define G_ISSUE_B(kt) do { const unsigned _sb = (unsigned)(kt) * 4u * kstepB; \
;         _Pragma("unroll") for (int _i = 0; _i < 8; ++_i) sb[_i] = bload16(_i < 4 ? rsB0 : rsB1, vob, _sb + (_i & 3) * kstepB); } while (0)
; #define G_WRITE_B(BO) do { \
;         _Pragma("unroll") for (int _i = 0; _i < 8; ++_i) *(LAS u32x2*)(b_wr + (BO) + (_i & 3) * (16 * G_BSTRIDE) + (_i >> 2) * SLAB1) = pack4(__builtin_bit_cast(f32x4, sb[_i])); } while (0)
; #define G_ENDTILE(VM) do { asm volatile("s_waitcnt vmcnt(" #VM ")" ::: "memory"); \
;         asm volatile("s_waitcnt lgkmcnt(0)" ::: "memory"); __builtin_amdgcn_s_barrier(); asm volatile("" ::: "memory"); } while (0)
;     ...
;     __builtin_amdgcn_s_barrier();
;     G_DMA_A(0, G_A0); G_ISSUE_B(0); G_WRITE_B(G_B0);
;     __builtin_amdgcn_sched_barrier(0);
;     G_ISSUE_B(1);
;     __builtin_amdgcn_sched_barrier(0);
;     G_ENDTILE(8);
;     for (int ui = 0;; ++ui) {
; #pragma unroll
;         for (int m = 0; m < MF; ++m)
; #pragma unroll
;             for (int n = 0; n < 4; ++n) acc[m][n] = (f32x4){0.f, 0.f, 0.f, 0.f};
;         for (int t = 0; t < nt - 2; t += 2) {
;             G_TILE(G_A0, G_B0, true, G_B1, G_A1, t + 1, true, t + 2, (void)0);
;             G_ENDTILE(8);
;             G_TILE(G_A1, G_B1, true, G_B0, G_A0, t + 2, true, t + 3, (void)0);
;             G_ENDTILE(8);
;         }
	v_mfma_f32_16x16x32_bf16 v[92:95], v[170:173], v[190:193], v[92:95]
	ds_read_b128 v[178:181], v162 offset:45056
	v_mfma_f32_16x16x32_bf16 v[88:91], v[174:177], v[190:193], v[88:91]
	v_mfma_f32_16x16x32_bf16 v[84:87], v[182:185], v[190:193], v[84:87]
	v_mfma_f32_16x16x32_bf16 v[80:83], v[186:189], v[190:193], v[80:83]
	s_waitcnt lgkmcnt(2)
	v_mfma_f32_16x16x32_bf16 v[76:79], v[170:173], v[198:201], v[76:79]
	ds_read_b128 v[190:193], v162 offset:47104
	buffer_load_dwordx4 v[28:31], v160, s[12:15], s26 offen
	s_waitcnt vmcnt(11)
	v_cvt_pk_bf16_f32 v7, v6, v7
	v_cvt_pk_bf16_f32 v6, v4, v5
	v_mfma_f32_16x16x32_bf16 v[72:75], v[174:177], v[198:201], v[72:75]
	ds_write_b64 v161, v[6:7] offset:17408
	v_mfma_f32_16x16x32_bf16 v[68:71], v[182:185], v[198:201], v[68:71]
	v_mfma_f32_16x16x32_bf16 v[64:67], v[186:189], v[198:201], v[64:67]
	s_add_i32 s27, s9, 0xfffe0000
	s_waitcnt lgkmcnt(2)
	v_mfma_f32_16x16x32_bf16 v[60:63], v[170:173], v[178:181], v[60:63]
	ds_read_b128 v[198:201], v162 offset:33792
	v_mfma_f32_16x16x32_bf16 v[56:59], v[174:177], v[178:181], v[56:59]
	v_mfma_f32_16x16x32_bf16 v[52:55], v[182:185], v[178:181], v[52:55]
	v_mfma_f32_16x16x32_bf16 v[48:51], v[186:189], v[178:181], v[48:51]
	s_waitcnt lgkmcnt(2)
	v_mfma_f32_16x16x32_bf16 v[44:47], v[170:173], v[190:193], v[44:47]
	ds_read_b128 v[170:173], v162 offset:35840
	buffer_load_dwordx4 v[4:7], v160, s[12:15], s27 offen
	s_waitcnt vmcnt(11)
	v_cvt_pk_bf16_f32 v27, v26, v27
	v_cvt_pk_bf16_f32 v26, v24, v25
	v_mfma_f32_16x16x32_bf16 v[40:43], v[174:177], v[190:193], v[40:43]
	ds_read_b64_tr_b16 v[244:245], v165 offset:52224
	ds_read_b64_tr_b16 v[248:249], v165 offset:52256
	ds_read_b64_tr_b16 v[202:203], v165 offset:52288
	ds_read_b64_tr_b16 v[206:207], v165 offset:52320
	ds_read_b64_tr_b16 v[246:247], v166 offset:52224
	ds_read_b64_tr_b16 v[250:251], v166 offset:52256
	ds_read_b64_tr_b16 v[204:205], v166 offset:52288
	ds_read_b64_tr_b16 v[208:209], v166 offset:52320
	ds_write_b64 v161, v[26:27] offset:26112
	v_mfma_f32_16x16x32_bf16 v[36:39], v[182:185], v[190:193], v[36:39]
	v_mfma_f32_16x16x32_bf16 v[32:35], v[186:189], v[190:193], v[32:35]
	s_waitcnt lgkmcnt(4)
	v_mfma_f32_16x16x32_bf16 v[156:159], v[244:247], v[198:201], v[156:159]
	ds_read_b128 v[182:185], v162 offset:37888
	s_waitcnt lgkmcnt(4)
	v_mfma_f32_16x16x32_bf16 v[152:155], v[248:251], v[198:201], v[152:155]
	s_waitcnt lgkmcnt(3)
	v_mfma_f32_16x16x32_bf16 v[148:151], v[202:205], v[198:201], v[148:151]
	s_waitcnt lgkmcnt(2)
	v_mfma_f32_16x16x32_bf16 v[144:147], v[206:209], v[198:201], v[144:147]
	v_mfma_f32_16x16x32_bf16 v[140:143], v[244:247], v[170:173], v[140:143]
	ds_read_b128 v[186:189], v162 offset:39936
	buffer_load_dwordx4 v[24:27], v160, s[12:15], s9 offen
	s_waitcnt vmcnt(11)
	v_cvt_pk_bf16_f32 v23, v22, v23
	v_cvt_pk_bf16_f32 v22, v20, v21
	v_mfma_f32_16x16x32_bf16 v[136:139], v[248:251], v[170:173], v[136:139]
	ds_write_b64 v161, v[22:23] offset:256
	v_mfma_f32_16x16x32_bf16 v[132:135], v[202:205], v[170:173], v[132:135]
	v_mfma_f32_16x16x32_bf16 v[128:131], v[206:209], v[170:173], v[128:131]
	s_waitcnt lgkmcnt(2)
	v_mfma_f32_16x16x32_bf16 v[124:127], v[244:247], v[182:185], v[124:127]
	ds_read_b128 v[170:173], v162 offset:41984
	v_mfma_f32_16x16x32_bf16 v[120:123], v[248:251], v[182:185], v[120:123]
	v_mfma_f32_16x16x32_bf16 v[116:119], v[202:205], v[182:185], v[116:119]
	v_mfma_f32_16x16x32_bf16 v[112:115], v[206:209], v[182:185], v[112:115]
	s_waitcnt lgkmcnt(2)
	v_mfma_f32_16x16x32_bf16 v[108:111], v[244:247], v[186:189], v[108:111]
	ds_read_b128 v[182:185], v162 offset:44032
	buffer_load_dwordx4 v[20:23], v160, s[16:19], s25 offen
	s_waitcnt vmcnt(11)
	v_cvt_pk_bf16_f32 v11, v10, v11
	v_cvt_pk_bf16_f32 v10, v8, v9
	v_mfma_f32_16x16x32_bf16 v[104:107], v[248:251], v[186:189], v[104:107]
	ds_write_b64 v161, v[10:11] offset:8960
	v_mfma_f32_16x16x32_bf16 v[100:103], v[202:205], v[186:189], v[100:103]
	v_mfma_f32_16x16x32_bf16 v[96:99], v[206:209], v[186:189], v[96:99]
	s_waitcnt lgkmcnt(2)
	v_mfma_f32_16x16x32_bf16 v[92:95], v[244:247], v[170:173], v[92:95]
	ds_read_b128 v[186:189], v162 offset:46080
	v_mfma_f32_16x16x32_bf16 v[88:91], v[248:251], v[170:173], v[88:91]
	v_mfma_f32_16x16x32_bf16 v[84:87], v[202:205], v[170:173], v[84:87]
	v_mfma_f32_16x16x32_bf16 v[80:83], v[206:209], v[170:173], v[80:83]
	s_waitcnt lgkmcnt(2)
	v_mfma_f32_16x16x32_bf16 v[76:79], v[244:247], v[182:185], v[76:79]
	ds_read_b128 v[252:255], v162 offset:48128
	buffer_load_dwordx4 v[8:11], v160, s[16:19], s26 offen
	s_waitcnt vmcnt(11)
	v_cvt_pk_bf16_f32 v3, v2, v3
	v_cvt_pk_bf16_f32 v2, v0, v1
	v_mfma_f32_16x16x32_bf16 v[72:75], v[248:251], v[182:185], v[72:75]
	ds_write_b64 v161, v[2:3] offset:17664
	v_mfma_f32_16x16x32_bf16 v[68:71], v[202:205], v[182:185], v[68:71]
	v_mfma_f32_16x16x32_bf16 v[64:67], v[206:209], v[182:185], v[64:67]
	s_waitcnt lgkmcnt(2)
	v_mfma_f32_16x16x32_bf16 v[60:63], v[244:247], v[186:189], v[60:63]
	buffer_load_dwordx4 v[0:3], v160, s[16:19], s27 offen
	s_waitcnt vmcnt(11)
	v_cvt_pk_bf16_f32 v19, v18, v19
	v_cvt_pk_bf16_f32 v18, v16, v17
	v_mfma_f32_16x16x32_bf16 v[56:59], v[248:251], v[186:189], v[56:59]
	ds_write_b64 v161, v[18:19] offset:26368
	v_mfma_f32_16x16x32_bf16 v[52:55], v[202:205], v[186:189], v[52:55]
	buffer_load_dwordx4 v[16:19], v160, s[16:19], s9 offen
	v_mfma_f32_16x16x32_bf16 v[48:51], v[206:209], v[186:189], v[48:51]
	s_add_i32 s8, s8, 2
	s_add_i32 s9, s9, 0x100000
	s_addk_i32 s24, 0x100
	s_cmp_ge_i32 s8, s67
	s_waitcnt vmcnt(8)
	s_waitcnt lgkmcnt(0)
	s_barrier
	s_cbranch_scc0 .LBB0_378

; #define G_DMA_A(kt, AO) do { G_DMA1(kt, AO, 0); G_DMA1(kt, AO, 1); G_DMA1(kt, AO, 2); G_DMA1(kt, AO, 3); if (MF == 9) G_DMA5(kt, AO); } while (0)
; #define G_ISSUE_B(kt) do { const unsigned _sb = (unsigned)(kt) * 4u * kstepB; \
;         _Pragma("unroll") for (int _i = 0; _i < 8; ++_i) sb[_i] = bload16(_i < 4 ? rsB0 : rsB1, vob, _sb + (_i & 3) * kstepB); } while (0)
; #define G_WRITE_B(BO) do { \
;         _Pragma("unroll") for (int _i = 0; _i < 8; ++_i) *(LAS u32x2*)(b_wr + (BO) + (_i & 3) * (16 * G_BSTRIDE) + (_i >> 2) * SLAB1) = pack4(__builtin_bit_cast(f32x4, sb[_i])); } while (0)
; #define G_ENDTILE(VM) do { asm volatile("s_waitcnt vmcnt(" #VM ")" ::: "memory"); \
;         asm volatile("s_waitcnt lgkmcnt(0)" ::: "memory"); __builtin_amdgcn_s_barrier(); asm volatile("" ::: "memory"); } while (0)
;     ...
;     __builtin_amdgcn_s_barrier();
;     G_DMA_A(0, G_A0); G_ISSUE_B(0); G_WRITE_B(G_B0);
;     __builtin_amdgcn_sched_barrier(0);
;     G_ISSUE_B(1);
;     __builtin_amdgcn_sched_barrier(0);
;     G_ENDTILE(8);
;     for (int ui = 0;; ++ui) {
; #pragma unroll
;         for (int m = 0; m < MF; ++m)
; #pragma unroll
;             for (int n = 0; n < 4; ++n) acc[m][n] = (f32x4){0.f, 0.f, 0.f, 0.f};
;         for (int t = 0; t < nt - 2; t += 2) {
;             G_TILE(G_A0, G_B0, true, G_B1, G_A1, t + 1, true, t + 2, (void)0);
.LBB0_649:
	s_andn2_b64 vcc, exec, s[40:41]
	v_mov_b32_e32 v175, 0
	s_cbranch_vccnz .LBB0_652
	s_mov_b32 s16, 0
	s_mov_b32 s17, 0x1e0000
	s_movk_i32 s36, 0x100
	s_cmp_lt_u32 s99, 9
	s_cbranch_scc1 .Lslow_P5
	s_mov_b32 m0, s85
	s_add_i32 s37, s36, 0xffffff80
	ds_read_b64_tr_b16 v[178:179], v188
	ds_read_b64_tr_b16 v[176:177], v187
	ds_read_b64_tr_b16 v[180:181], v187 offset:32
	ds_read_b64_tr_b16 v[198:199], v187 offset:64
	ds_read_b64_tr_b16 v[202:203], v187 offset:96
	ds_read_b128 v[206:209], v186
	ds_read_b64_tr_b16 v[182:183], v188 offset:32
	ds_read_b64_tr_b16 v[200:201], v188 offset:64
	ds_read_b64_tr_b16 v[204:205], v188 offset:96
	ds_read_b128 v[210:213], v186 offset:2048
	ds_read_b128 v[214:217], v186 offset:4096
	buffer_load_dwordx4 v189, s[20:23], s37 offen lds
	s_mov_b32 m0, s7
	s_waitcnt lgkmcnt(5)
	v_mfma_f32_16x16x32_bf16 v[172:175], v[176:179], v[206:209], 0
	buffer_load_dwordx4 v192, s[20:23], s37 offen lds
	s_waitcnt lgkmcnt(4)
	v_mfma_f32_16x16x32_bf16 v[168:171], v[180:183], v[206:209], 0
	s_waitcnt lgkmcnt(3)
	v_mfma_f32_16x16x32_bf16 v[164:167], v[198:201], v[206:209], 0
	s_waitcnt lgkmcnt(2)
	v_mfma_f32_16x16x32_bf16 v[160:163], v[202:205], v[206:209], 0
	s_waitcnt lgkmcnt(1)
	v_mfma_f32_16x16x32_bf16 v[156:159], v[176:179], v[210:213], 0
	s_mov_b32 m0, s6
	s_nop 0
	buffer_load_dwordx4 v191, s[20:23], s37 offen lds
	ds_read_b128 v[206:209], v186 offset:6144
	s_waitcnt vmcnt(10)
	v_cvt_pk_bf16_f32 v15, v14, v15
	v_cvt_pk_bf16_f32 v14, v12, v13
	v_mfma_f32_16x16x32_bf16 v[152:155], v[180:183], v[210:213], 0
	ds_write_b64 v185, v[14:15] offset:34816
	v_mfma_f32_16x16x32_bf16 v[148:151], v[198:201], v[210:213], 0
	s_mov_b32 m0, s47
	s_nop 0
	buffer_load_dwordx4 v190, s[20:23], s37 offen lds
	v_mfma_f32_16x16x32_bf16 v[144:147], v[202:205], v[210:213], 0
	s_waitcnt lgkmcnt(2)
	v_mfma_f32_16x16x32_bf16 v[132:135], v[176:179], v[214:217], 0
	s_mov_b32 m0, s48
	s_nop 0
	buffer_load_dwordx4 v193, s[20:23], s37 offen lds
	s_add_i32 s37, s17, 0xfff20000
	ds_read_b128 v[210:213], v186 offset:8192
	v_mfma_f32_16x16x32_bf16 v[124:127], v[180:183], v[214:217], 0
	v_mfma_f32_16x16x32_bf16 v[120:123], v[198:201], v[214:217], 0
	v_mfma_f32_16x16x32_bf16 v[140:143], v[202:205], v[214:217], 0
	s_waitcnt lgkmcnt(2)
	v_mfma_f32_16x16x32_bf16 v[136:139], v[176:179], v[206:209], 0
	ds_read_b128 v[214:217], v186 offset:10240
	buffer_load_dwordx4 v[12:15], v184, s[24:27], s37 offen
	s_waitcnt vmcnt(12)
	v_cvt_pk_bf16_f32 v3, v2, v3
	v_cvt_pk_bf16_f32 v2, v0, v1
	v_mfma_f32_16x16x32_bf16 v[128:131], v[180:183], v[206:209], 0
	ds_write_b64 v185, v[2:3] offset:43520
	v_mfma_f32_16x16x32_bf16 v[116:119], v[198:201], v[206:209], 0
	v_mfma_f32_16x16x32_bf16 v[112:115], v[202:205], v[206:209], 0
	s_add_i32 s38, s17, 0xfff40000
	s_waitcnt lgkmcnt(2)
	v_mfma_f32_16x16x32_bf16 v[100:103], v[176:179], v[210:213], 0
	ds_read_b128 v[206:209], v186 offset:12288
	v_mfma_f32_16x16x32_bf16 v[92:95], v[180:183], v[210:213], 0
	v_mfma_f32_16x16x32_bf16 v[88:91], v[198:201], v[210:213], 0
	v_mfma_f32_16x16x32_bf16 v[108:111], v[202:205], v[210:213], 0
	s_waitcnt lgkmcnt(2)
	v_mfma_f32_16x16x32_bf16 v[104:107], v[176:179], v[214:217], 0
	ds_read_b128 v[210:213], v186 offset:14336
	buffer_load_dwordx4 v[0:3], v184, s[24:27], s38 offen
	s_waitcnt vmcnt(12)
	v_cvt_pk_bf16_f32 v31, v30, v31
	v_cvt_pk_bf16_f32 v30, v28, v29
	v_mfma_f32_16x16x32_bf16 v[96:99], v[180:183], v[214:217], 0
	ds_write_b64 v185, v[30:31] offset:52224
	v_mfma_f32_16x16x32_bf16 v[84:87], v[198:201], v[214:217], 0
	v_mfma_f32_16x16x32_bf16 v[80:83], v[202:205], v[214:217], 0
	s_add_i32 s39, s17, 0xfff60000
	s_waitcnt lgkmcnt(2)
	v_mfma_f32_16x16x32_bf16 v[72:75], v[176:179], v[206:209], 0
	ds_read_b128 v[214:217], v186 offset:16384
	v_mfma_f32_16x16x32_bf16 v[64:67], v[180:183], v[206:209], 0
	v_mfma_f32_16x16x32_bf16 v[60:63], v[198:201], v[206:209], 0
	v_mfma_f32_16x16x32_bf16 v[76:79], v[202:205], v[206:209], 0
	s_waitcnt lgkmcnt(2)
	v_mfma_f32_16x16x32_bf16 v[68:71], v[176:179], v[210:213], 0
	ds_read_b128 v[206:209], v186 offset:1024
	buffer_load_dwordx4 v[28:31], v184, s[24:27], s39 offen
	s_waitcnt vmcnt(12)
	v_cvt_pk_bf16_f32 v27, v26, v27
	v_cvt_pk_bf16_f32 v26, v24, v25
	v_mfma_f32_16x16x32_bf16 v[56:59], v[180:183], v[210:213], 0
	ds_write_b64 v185, v[26:27] offset:60928
	v_mfma_f32_16x16x32_bf16 v[52:55], v[198:201], v[210:213], 0
	v_mfma_f32_16x16x32_bf16 v[48:51], v[202:205], v[210:213], 0
	s_add_i32 s42, s17, 0xfff80000
	ds_read_b128 v[210:213], v186 offset:3072
	s_waitcnt lgkmcnt(3)
	v_mfma_f32_16x16x32_bf16 v[44:47], v[176:179], v[214:217], 0
	ds_read_b64_tr_b16 v[246:247], v188 offset:17408
	ds_read_b64_tr_b16 v[220:221], v188 offset:17440
	ds_read_b64_tr_b16 v[244:245], v187 offset:17408
	ds_read_b64_tr_b16 v[218:219], v187 offset:17440
	v_mfma_f32_16x16x32_bf16 v[40:43], v[180:183], v[214:217], 0
	ds_read_b64_tr_b16 v[248:249], v187 offset:17472
	ds_read_b64_tr_b16 v[250:251], v188 offset:17472
	v_mfma_f32_16x16x32_bf16 v[36:39], v[198:201], v[214:217], 0
	ds_read_b64_tr_b16 v[252:253], v187 offset:17504
	ds_read_b64_tr_b16 v[254:255], v188 offset:17504
	v_mfma_f32_16x16x32_bf16 v[32:35], v[202:205], v[214:217], 0
	s_waitcnt lgkmcnt(5)
	v_mfma_f32_16x16x32_bf16 v[172:175], v[244:247], v[206:209], v[172:175]
	ds_read_b128 v[202:205], v186 offset:5120
	buffer_load_dwordx4 v[24:27], v184, s[24:27], s42 offen
	s_waitcnt vmcnt(12)
	v_cvt_pk_bf16_f32 v23, v22, v23
	v_cvt_pk_bf16_f32 v22, v20, v21
	s_waitcnt lgkmcnt(5)
	v_mfma_f32_16x16x32_bf16 v[168:171], v[218:221], v[206:209], v[168:171]
	ds_write_b64 v185, v[22:23] offset:34880
	s_waitcnt lgkmcnt(4)
; #define G_DMA_A(kt, AO) do { G_DMA1(kt, AO, 0); G_DMA1(kt, AO, 1); G_DMA1(kt, AO, 2); G_DMA1(kt, AO, 3); if (MF == 9) G_DMA5(kt, AO); } while (0)
; #define G_ISSUE_B(kt) do { const unsigned _sb = (unsigned)(kt) * 4u * kstepB; \
;         _Pragma("unroll") for (int _i = 0; _i < 8; ++_i) sb[_i] = bload16(_i < 4 ? rsB0 : rsB1, vob, _sb + (_i & 3) * kstepB); } while (0)
; #define G_WRITE_B(BO) do { \
;         _Pragma("unroll") for (int _i = 0; _i < 8; ++_i) *(LAS u32x2*)(b_wr + (BO) + (_i & 3) * (16 * G_BSTRIDE) + (_i >> 2) * SLAB1) = pack4(__builtin_bit_cast(f32x4, sb[_i])); } while (0)
; #define G_ENDTILE(VM) do { asm volatile("s_waitcnt vmcnt(" #VM ")" ::: "memory"); \
;         asm volatile("s_waitcnt lgkmcnt(0)" ::: "memory"); __builtin_amdgcn_s_barrier(); asm volatile("" ::: "memory"); } while (0)
;     ...
;     __builtin_amdgcn_s_barrier();
;     G_DMA_A(0, G_A0); G_ISSUE_B(0); G_WRITE_B(G_B0);
;     __builtin_amdgcn_sched_barrier(0);
;     G_ISSUE_B(1);
;     __builtin_amdgcn_sched_barrier(0);
;     G_ENDTILE(8);
;     for (int ui = 0;; ++ui) {
; #pragma unroll
;         for (int m = 0; m < MF; ++m)
; #pragma unroll
;             for (int n = 0; n < 4; ++n) acc[m][n] = (f32x4){0.f, 0.f, 0.f, 0.f};
;         for (int t = 0; t < nt - 2; t += 2) {
;             G_TILE(G_A0, G_B0, true, G_B1, G_A1, t + 1, true, t + 2, (void)0);
;             G_ENDTILE(8);
;             G_TILE(G_A1, G_B1, true, G_B0, G_A0, t + 2, true, t + 3, (void)0);
;             G_ENDTILE(8);
	v_mfma_f32_16x16x32_bf16 v[164:167], v[248:251], v[206:209], v[164:167]
	s_waitcnt lgkmcnt(2)
	v_mfma_f32_16x16x32_bf16 v[160:163], v[252:255], v[206:209], v[160:163]
	v_mfma_f32_16x16x32_bf16 v[156:159], v[244:247], v[210:213], v[156:159]
	ds_read_b128 v[206:209], v186 offset:7168
	v_mfma_f32_16x16x32_bf16 v[152:155], v[218:221], v[210:213], v[152:155]
	v_mfma_f32_16x16x32_bf16 v[148:151], v[248:251], v[210:213], v[148:151]
	v_mfma_f32_16x16x32_bf16 v[144:147], v[252:255], v[210:213], v[144:147]
	s_waitcnt lgkmcnt(2)
	v_mfma_f32_16x16x32_bf16 v[132:135], v[244:247], v[202:205], v[132:135]
	ds_read_b128 v[210:213], v186 offset:9216
	buffer_load_dwordx4 v[20:23], v184, s[28:31], s37 offen
	s_waitcnt vmcnt(12)
	v_cvt_pk_bf16_f32 v7, v6, v7
	v_cvt_pk_bf16_f32 v6, v4, v5
	v_mfma_f32_16x16x32_bf16 v[124:127], v[218:221], v[202:205], v[124:127]
	ds_write_b64 v185, v[6:7] offset:43584
	v_mfma_f32_16x16x32_bf16 v[120:123], v[248:251], v[202:205], v[120:123]
	v_mfma_f32_16x16x32_bf16 v[140:143], v[252:255], v[202:205], v[140:143]
	s_waitcnt lgkmcnt(2)
	v_mfma_f32_16x16x32_bf16 v[136:139], v[244:247], v[206:209], v[136:139]
	ds_read_b128 v[202:205], v186 offset:11264
	v_mfma_f32_16x16x32_bf16 v[128:131], v[218:221], v[206:209], v[128:131]
	v_mfma_f32_16x16x32_bf16 v[116:119], v[248:251], v[206:209], v[116:119]
	v_mfma_f32_16x16x32_bf16 v[112:115], v[252:255], v[206:209], v[112:115]
	s_waitcnt lgkmcnt(2)
	v_mfma_f32_16x16x32_bf16 v[100:103], v[244:247], v[210:213], v[100:103]
	ds_read_b128 v[206:209], v186 offset:13312
	buffer_load_dwordx4 v[4:7], v184, s[28:31], s38 offen
	s_waitcnt vmcnt(12)
	v_cvt_pk_bf16_f32 v11, v10, v11
	v_cvt_pk_bf16_f32 v10, v8, v9
	v_mfma_f32_16x16x32_bf16 v[92:95], v[218:221], v[210:213], v[92:95]
	ds_write_b64 v185, v[10:11] offset:52288
	v_mfma_f32_16x16x32_bf16 v[88:91], v[248:251], v[210:213], v[88:91]
	v_mfma_f32_16x16x32_bf16 v[108:111], v[252:255], v[210:213], v[108:111]
	s_waitcnt lgkmcnt(2)
	v_mfma_f32_16x16x32_bf16 v[104:107], v[244:247], v[202:205], v[104:107]
	ds_read_b128 v[210:213], v186 offset:15360
	v_mfma_f32_16x16x32_bf16 v[96:99], v[218:221], v[202:205], v[96:99]
	v_mfma_f32_16x16x32_bf16 v[84:87], v[248:251], v[202:205], v[84:87]
	v_mfma_f32_16x16x32_bf16 v[80:83], v[252:255], v[202:205], v[80:83]
	s_waitcnt lgkmcnt(2)
	v_mfma_f32_16x16x32_bf16 v[72:75], v[244:247], v[206:209], v[72:75]
	ds_read_b128 v[238:241], v186 offset:17408
	buffer_load_dwordx4 v[8:11], v184, s[28:31], s39 offen
	s_waitcnt vmcnt(12)
	v_cvt_pk_bf16_f32 v19, v18, v19
	v_cvt_pk_bf16_f32 v18, v16, v17
	v_mfma_f32_16x16x32_bf16 v[64:67], v[218:221], v[206:209], v[64:67]
	ds_write_b64 v185, v[18:19] offset:60992
	v_mfma_f32_16x16x32_bf16 v[60:63], v[248:251], v[206:209], v[60:63]
	v_mfma_f32_16x16x32_bf16 v[76:79], v[252:255], v[206:209], v[76:79]
	s_waitcnt lgkmcnt(2)
	v_mfma_f32_16x16x32_bf16 v[68:71], v[244:247], v[210:213], v[68:71]
	v_mfma_f32_16x16x32_bf16 v[56:59], v[218:221], v[210:213], v[56:59]
	v_mfma_f32_16x16x32_bf16 v[52:55], v[248:251], v[210:213], v[52:55]
	v_mfma_f32_16x16x32_bf16 v[48:51], v[252:255], v[210:213], v[48:51]
	s_waitcnt lgkmcnt(1)
	buffer_load_dwordx4 v[16:19], v184, s[28:31], s42 offen
	s_waitcnt vmcnt(8)
	s_mov_b32 m0, s46
	s_waitcnt lgkmcnt(0)
	s_barrier
	ds_read_b64_tr_b16 v[178:179], v188 offset:34816
	ds_read_b64_tr_b16 v[176:177], v187 offset:34816
	ds_read_b64_tr_b16 v[180:181], v187 offset:34848
	ds_read_b64_tr_b16 v[198:199], v187 offset:34880
	ds_read_b64_tr_b16 v[202:203], v187 offset:34912
	ds_read_b128 v[206:209], v186 offset:36864
	ds_read_b64_tr_b16 v[182:183], v188 offset:34848
	ds_read_b64_tr_b16 v[200:201], v188 offset:34880
	ds_read_b64_tr_b16 v[204:205], v188 offset:34912
	ds_read_b128 v[210:213], v186 offset:38912
	ds_read_b128 v[214:217], v186 offset:40960
	buffer_load_dwordx4 v189, s[20:23], s36 offen lds
	s_mov_b32 m0, s86
	v_mfma_f32_16x16x32_bf16 v[44:47], v[244:247], v[238:241], v[44:47]
	v_mfma_f32_16x16x32_bf16 v[40:43], v[218:221], v[238:241], v[40:43]
	v_mfma_f32_16x16x32_bf16 v[36:39], v[248:251], v[238:241], v[36:39]
	v_mfma_f32_16x16x32_bf16 v[32:35], v[252:255], v[238:241], v[32:35]
	s_waitcnt lgkmcnt(5)
	v_mfma_f32_16x16x32_bf16 v[172:175], v[176:179], v[206:209], v[172:175]
	buffer_load_dwordx4 v192, s[20:23], s36 offen lds
	s_add_i32 s37, s17, 0xfffa0000
	s_waitcnt lgkmcnt(4)
	v_mfma_f32_16x16x32_bf16 v[168:171], v[180:183], v[206:209], v[168:171]
	s_waitcnt lgkmcnt(3)
	v_mfma_f32_16x16x32_bf16 v[164:167], v[198:201], v[206:209], v[164:167]
	s_waitcnt lgkmcnt(2)
	v_mfma_f32_16x16x32_bf16 v[160:163], v[202:205], v[206:209], v[160:163]
	s_waitcnt lgkmcnt(1)
	v_mfma_f32_16x16x32_bf16 v[156:159], v[176:179], v[210:213], v[156:159]
	s_mov_b32 m0, s89
	s_nop 0
	buffer_load_dwordx4 v191, s[20:23], s36 offen lds
	ds_read_b128 v[206:209], v186 offset:43008
	s_waitcnt vmcnt(10)
	v_cvt_pk_bf16_f32 v15, v14, v15
	v_cvt_pk_bf16_f32 v14, v12, v13
	v_mfma_f32_16x16x32_bf16 v[152:155], v[180:183], v[210:213], v[152:155]
	ds_write_b64 v185, v[14:15]
	v_mfma_f32_16x16x32_bf16 v[148:151], v[198:201], v[210:213], v[148:151]
	s_mov_b32 m0, s90
	s_nop 0
	buffer_load_dwordx4 v190, s[20:23], s36 offen lds
	v_mfma_f32_16x16x32_bf16 v[144:147], v[202:205], v[210:213], v[144:147]
	s_waitcnt lgkmcnt(2)
	v_mfma_f32_16x16x32_bf16 v[132:135], v[176:179], v[214:217], v[132:135]
	s_mov_b32 m0, s91
	s_nop 0
	buffer_load_dwordx4 v193, s[20:23], s36 offen lds
	ds_read_b128 v[210:213], v186 offset:45056
	v_mfma_f32_16x16x32_bf16 v[124:127], v[180:183], v[214:217], v[124:127]
	v_mfma_f32_16x16x32_bf16 v[120:123], v[198:201], v[214:217], v[120:123]
	v_mfma_f32_16x16x32_bf16 v[140:143], v[202:205], v[214:217], v[140:143]
	s_waitcnt lgkmcnt(2)
; #define G_DMA_A(kt, AO) do { G_DMA1(kt, AO, 0); G_DMA1(kt, AO, 1); G_DMA1(kt, AO, 2); G_DMA1(kt, AO, 3); if (MF == 9) G_DMA5(kt, AO); } while (0)
; #define G_ISSUE_B(kt) do { const unsigned _sb = (unsigned)(kt) * 4u * kstepB; \
;         _Pragma("unroll") for (int _i = 0; _i < 8; ++_i) sb[_i] = bload16(_i < 4 ? rsB0 : rsB1, vob, _sb + (_i & 3) * kstepB); } while (0)
; #define G_WRITE_B(BO) do { \
;         _Pragma("unroll") for (int _i = 0; _i < 8; ++_i) *(LAS u32x2*)(b_wr + (BO) + (_i & 3) * (16 * G_BSTRIDE) + (_i >> 2) * SLAB1) = pack4(__builtin_bit_cast(f32x4, sb[_i])); } while (0)
; #define G_ENDTILE(VM) do { asm volatile("s_waitcnt vmcnt(" #VM ")" ::: "memory"); \
;         asm volatile("s_waitcnt lgkmcnt(0)" ::: "memory"); __builtin_amdgcn_s_barrier(); asm volatile("" ::: "memory"); } while (0)
;     ...
;     __builtin_amdgcn_s_barrier();
;     G_DMA_A(0, G_A0); G_ISSUE_B(0); G_WRITE_B(G_B0);
;     __builtin_amdgcn_sched_barrier(0);
;     G_ISSUE_B(1);
;     __builtin_amdgcn_sched_barrier(0);
;     G_ENDTILE(8);
;     for (int ui = 0;; ++ui) {
; #pragma unroll
;         for (int m = 0; m < MF; ++m)
; #pragma unroll
;             for (int n = 0; n < 4; ++n) acc[m][n] = (f32x4){0.f, 0.f, 0.f, 0.f};
;         for (int t = 0; t < nt - 2; t += 2) {
;             G_TILE(G_A0, G_B0, true, G_B1, G_A1, t + 1, true, t + 2, (void)0);
;             G_ENDTILE(8);
;             G_TILE(G_A1, G_B1, true, G_B0, G_A0, t + 2, true, t + 3, (void)0);
;             G_ENDTILE(8);
;         }
	v_mfma_f32_16x16x32_bf16 v[136:139], v[176:179], v[206:209], v[136:139]
	ds_read_b128 v[214:217], v186 offset:47104
	buffer_load_dwordx4 v[12:15], v184, s[24:27], s37 offen
	s_waitcnt vmcnt(12)
	v_cvt_pk_bf16_f32 v3, v2, v3
	v_cvt_pk_bf16_f32 v2, v0, v1
	v_mfma_f32_16x16x32_bf16 v[128:131], v[180:183], v[206:209], v[128:131]
	ds_write_b64 v185, v[2:3] offset:8704
	v_mfma_f32_16x16x32_bf16 v[116:119], v[198:201], v[206:209], v[116:119]
	v_mfma_f32_16x16x32_bf16 v[112:115], v[202:205], v[206:209], v[112:115]
	s_add_i32 s38, s17, 0xfffc0000
	s_waitcnt lgkmcnt(2)
	v_mfma_f32_16x16x32_bf16 v[100:103], v[176:179], v[210:213], v[100:103]
	ds_read_b128 v[206:209], v186 offset:49152
	v_mfma_f32_16x16x32_bf16 v[92:95], v[180:183], v[210:213], v[92:95]
	v_mfma_f32_16x16x32_bf16 v[88:91], v[198:201], v[210:213], v[88:91]
	v_mfma_f32_16x16x32_bf16 v[108:111], v[202:205], v[210:213], v[108:111]
	s_waitcnt lgkmcnt(2)
	v_mfma_f32_16x16x32_bf16 v[104:107], v[176:179], v[214:217], v[104:107]
	ds_read_b128 v[210:213], v186 offset:51200
	buffer_load_dwordx4 v[0:3], v184, s[24:27], s38 offen
	s_waitcnt vmcnt(12)
	v_cvt_pk_bf16_f32 v31, v30, v31
	v_cvt_pk_bf16_f32 v30, v28, v29
	v_mfma_f32_16x16x32_bf16 v[96:99], v[180:183], v[214:217], v[96:99]
	ds_write_b64 v185, v[30:31] offset:17408
	v_mfma_f32_16x16x32_bf16 v[84:87], v[198:201], v[214:217], v[84:87]
	v_mfma_f32_16x16x32_bf16 v[80:83], v[202:205], v[214:217], v[80:83]
	s_add_i32 s39, s17, 0xfffe0000
	s_waitcnt lgkmcnt(2)
	v_mfma_f32_16x16x32_bf16 v[72:75], v[176:179], v[206:209], v[72:75]
	ds_read_b128 v[214:217], v186 offset:53248
	v_mfma_f32_16x16x32_bf16 v[64:67], v[180:183], v[206:209], v[64:67]
	v_mfma_f32_16x16x32_bf16 v[60:63], v[198:201], v[206:209], v[60:63]
	v_mfma_f32_16x16x32_bf16 v[76:79], v[202:205], v[206:209], v[76:79]
	s_waitcnt lgkmcnt(2)
	v_mfma_f32_16x16x32_bf16 v[68:71], v[176:179], v[210:213], v[68:71]
	ds_read_b128 v[206:209], v186 offset:37888
	buffer_load_dwordx4 v[28:31], v184, s[24:27], s39 offen
	s_waitcnt vmcnt(12)
	v_cvt_pk_bf16_f32 v27, v26, v27
	v_cvt_pk_bf16_f32 v26, v24, v25
	v_mfma_f32_16x16x32_bf16 v[56:59], v[180:183], v[210:213], v[56:59]
	ds_write_b64 v185, v[26:27] offset:26112
	v_mfma_f32_16x16x32_bf16 v[52:55], v[198:201], v[210:213], v[52:55]
	v_mfma_f32_16x16x32_bf16 v[48:51], v[202:205], v[210:213], v[48:51]
	ds_read_b128 v[210:213], v186 offset:39936
	s_waitcnt lgkmcnt(3)
	v_mfma_f32_16x16x32_bf16 v[44:47], v[176:179], v[214:217], v[44:47]
	ds_read_b64_tr_b16 v[246:247], v188 offset:52224
	ds_read_b64_tr_b16 v[220:221], v188 offset:52256
	ds_read_b64_tr_b16 v[244:245], v187 offset:52224
	ds_read_b64_tr_b16 v[218:219], v187 offset:52256
	v_mfma_f32_16x16x32_bf16 v[40:43], v[180:183], v[214:217], v[40:43]
	ds_read_b64_tr_b16 v[248:249], v187 offset:52288
	ds_read_b64_tr_b16 v[250:251], v188 offset:52288
	v_mfma_f32_16x16x32_bf16 v[36:39], v[198:201], v[214:217], v[36:39]
	ds_read_b64_tr_b16 v[252:253], v187 offset:52320
	ds_read_b64_tr_b16 v[254:255], v188 offset:52320
	v_mfma_f32_16x16x32_bf16 v[32:35], v[202:205], v[214:217], v[32:35]
	s_waitcnt lgkmcnt(5)
	v_mfma_f32_16x16x32_bf16 v[172:175], v[244:247], v[206:209], v[172:175]
	ds_read_b128 v[202:205], v186 offset:41984
	buffer_load_dwordx4 v[24:27], v184, s[24:27], s17 offen
	s_waitcnt vmcnt(12)
	v_cvt_pk_bf16_f32 v23, v22, v23
	v_cvt_pk_bf16_f32 v22, v20, v21
	s_waitcnt lgkmcnt(5)
	v_mfma_f32_16x16x32_bf16 v[168:171], v[218:221], v[206:209], v[168:171]
	ds_write_b64 v185, v[22:23] offset:64
	s_waitcnt lgkmcnt(4)
	v_mfma_f32_16x16x32_bf16 v[164:167], v[248:251], v[206:209], v[164:167]
	s_waitcnt lgkmcnt(2)
	v_mfma_f32_16x16x32_bf16 v[160:163], v[252:255], v[206:209], v[160:163]
	v_mfma_f32_16x16x32_bf16 v[156:159], v[244:247], v[210:213], v[156:159]
	ds_read_b128 v[206:209], v186 offset:44032
	v_mfma_f32_16x16x32_bf16 v[152:155], v[218:221], v[210:213], v[152:155]
	v_mfma_f32_16x16x32_bf16 v[148:151], v[248:251], v[210:213], v[148:151]
	v_mfma_f32_16x16x32_bf16 v[144:147], v[252:255], v[210:213], v[144:147]
	s_waitcnt lgkmcnt(2)
	v_mfma_f32_16x16x32_bf16 v[132:135], v[244:247], v[202:205], v[132:135]
	ds_read_b128 v[210:213], v186 offset:46080
	buffer_load_dwordx4 v[20:23], v184, s[28:31], s37 offen
	s_waitcnt vmcnt(12)
	v_cvt_pk_bf16_f32 v7, v6, v7
	v_cvt_pk_bf16_f32 v6, v4, v5
	v_mfma_f32_16x16x32_bf16 v[124:127], v[218:221], v[202:205], v[124:127]
	ds_write_b64 v185, v[6:7] offset:8768
	v_mfma_f32_16x16x32_bf16 v[120:123], v[248:251], v[202:205], v[120:123]
	v_mfma_f32_16x16x32_bf16 v[140:143], v[252:255], v[202:205], v[140:143]
	s_waitcnt lgkmcnt(2)
	v_mfma_f32_16x16x32_bf16 v[136:139], v[244:247], v[206:209], v[136:139]
	ds_read_b128 v[202:205], v186 offset:48128
	v_mfma_f32_16x16x32_bf16 v[128:131], v[218:221], v[206:209], v[128:131]
	v_mfma_f32_16x16x32_bf16 v[116:119], v[248:251], v[206:209], v[116:119]
	v_mfma_f32_16x16x32_bf16 v[112:115], v[252:255], v[206:209], v[112:115]
	s_waitcnt lgkmcnt(2)
	v_mfma_f32_16x16x32_bf16 v[100:103], v[244:247], v[210:213], v[100:103]
	ds_read_b128 v[206:209], v186 offset:50176
	buffer_load_dwordx4 v[4:7], v184, s[28:31], s38 offen
	s_waitcnt vmcnt(12)
	v_cvt_pk_bf16_f32 v11, v10, v11
	v_cvt_pk_bf16_f32 v10, v8, v9
	v_mfma_f32_16x16x32_bf16 v[92:95], v[218:221], v[210:213], v[92:95]
	ds_write_b64 v185, v[10:11] offset:17472
	v_mfma_f32_16x16x32_bf16 v[88:91], v[248:251], v[210:213], v[88:91]
	v_mfma_f32_16x16x32_bf16 v[108:111], v[252:255], v[210:213], v[108:111]
	s_waitcnt lgkmcnt(2)
	v_mfma_f32_16x16x32_bf16 v[104:107], v[244:247], v[202:205], v[104:107]
	ds_read_b128 v[210:213], v186 offset:52224
	v_mfma_f32_16x16x32_bf16 v[96:99], v[218:221], v[202:205], v[96:99]
	v_mfma_f32_16x16x32_bf16 v[84:87], v[248:251], v[202:205], v[84:87]
	v_mfma_f32_16x16x32_bf16 v[80:83], v[252:255], v[202:205], v[80:83]
	s_waitcnt lgkmcnt(2)
	v_mfma_f32_16x16x32_bf16 v[72:75], v[244:247], v[206:209], v[72:75]
	ds_read_b128 v[238:241], v186 offset:54272
	buffer_load_dwordx4 v[8:11], v184, s[28:31], s39 offen
	s_waitcnt vmcnt(12)
	v_cvt_pk_bf16_f32 v19, v18, v19
	v_cvt_pk_bf16_f32 v18, v16, v17
	v_mfma_f32_16x16x32_bf16 v[64:67], v[218:221], v[206:209], v[64:67]
	ds_write_b64 v185, v[18:19] offset:26176
	v_mfma_f32_16x16x32_bf16 v[60:63], v[248:251], v[206:209], v[60:63]
	v_mfma_f32_16x16x32_bf16 v[76:79], v[252:255], v[206:209], v[76:79]
	s_waitcnt lgkmcnt(2)
	v_mfma_f32_16x16x32_bf16 v[68:71], v[244:247], v[210:213], v[68:71]
	v_mfma_f32_16x16x32_bf16 v[56:59], v[218:221], v[210:213], v[56:59]
	v_mfma_f32_16x16x32_bf16 v[52:55], v[248:251], v[210:213], v[52:55]
	v_mfma_f32_16x16x32_bf16 v[48:51], v[252:255], v[210:213], v[48:51]
	s_waitcnt lgkmcnt(1)
	buffer_load_dwordx4 v[16:19], v184, s[28:31], s17 offen
	s_add_i32 s16, s16, 2
	s_add_i32 s17, s17, 0x100000
	s_addk_i32 s36, 0x100
	s_cmp_ge_i32 s16, s97
	s_waitcnt vmcnt(8)
	s_waitcnt lgkmcnt(0)
	s_barrier
	s_cbranch_scc1 .Lflush_P5
; #define G_DMA_A(kt, AO) do { G_DMA1(kt, AO, 0); G_DMA1(kt, AO, 1); G_DMA1(kt, AO, 2); G_DMA1(kt, AO, 3); if (MF == 9) G_DMA5(kt, AO); } while (0)
; #define G_ISSUE_B(kt) do { const unsigned _sb = (unsigned)(kt) * 4u * kstepB; \
;         _Pragma("unroll") for (int _i = 0; _i < 8; ++_i) sb[_i] = bload16(_i < 4 ? rsB0 : rsB1, vob, _sb + (_i & 3) * kstepB); } while (0)
; #define G_WRITE_B(BO) do { \
;         _Pragma("unroll") for (int _i = 0; _i < 8; ++_i) *(LAS u32x2*)(b_wr + (BO) + (_i & 3) * (16 * G_BSTRIDE) + (_i >> 2) * SLAB1) = pack4(__builtin_bit_cast(f32x4, sb[_i])); } while (0)
; #define G_ENDTILE(VM) do { asm volatile("s_waitcnt vmcnt(" #VM ")" ::: "memory"); \
;         asm volatile("s_waitcnt lgkmcnt(0)" ::: "memory"); __builtin_amdgcn_s_barrier(); asm volatile("" ::: "memory"); } while (0)
;     ...
;     __builtin_amdgcn_s_barrier();
;     G_DMA_A(0, G_A0); G_ISSUE_B(0); G_WRITE_B(G_B0);
;     __builtin_amdgcn_sched_barrier(0);
;     G_ISSUE_B(1);
;     __builtin_amdgcn_sched_barrier(0);
;     G_ENDTILE(8);
;     for (int ui = 0;; ++ui) {
; #pragma unroll
;         for (int m = 0; m < MF; ++m)
; #pragma unroll
;             for (int n = 0; n < 4; ++n) acc[m][n] = (f32x4){0.f, 0.f, 0.f, 0.f};
;         for (int t = 0; t < nt - 2; t += 2) {
;             G_TILE(G_A0, G_B0, true, G_B1, G_A1, t + 1, true, t + 2, (void)0);
.LBB0_651:
	s_mov_b32 m0, s85
	s_add_i32 s37, s36, 0xffffff80
	ds_read_b64_tr_b16 v[178:179], v188
	ds_read_b64_tr_b16 v[176:177], v187
	ds_read_b64_tr_b16 v[180:181], v187 offset:32
	ds_read_b64_tr_b16 v[198:199], v187 offset:64
	ds_read_b64_tr_b16 v[202:203], v187 offset:96
	ds_read_b128 v[206:209], v186
	ds_read_b64_tr_b16 v[182:183], v188 offset:32
	ds_read_b64_tr_b16 v[200:201], v188 offset:64
	ds_read_b64_tr_b16 v[204:205], v188 offset:96
	ds_read_b128 v[210:213], v186 offset:2048
	ds_read_b128 v[214:217], v186 offset:4096
	buffer_load_dwordx4 v189, s[20:23], s37 offen lds
	s_mov_b32 m0, s7
	v_mfma_f32_16x16x32_bf16 v[44:47], v[244:247], v[238:241], v[44:47]
	v_mfma_f32_16x16x32_bf16 v[40:43], v[218:221], v[238:241], v[40:43]
	v_mfma_f32_16x16x32_bf16 v[36:39], v[248:251], v[238:241], v[36:39]
	v_mfma_f32_16x16x32_bf16 v[32:35], v[252:255], v[238:241], v[32:35]
	s_waitcnt lgkmcnt(5)
	v_mfma_f32_16x16x32_bf16 v[172:175], v[176:179], v[206:209], v[172:175]
	buffer_load_dwordx4 v192, s[20:23], s37 offen lds
	s_waitcnt lgkmcnt(4)
	v_mfma_f32_16x16x32_bf16 v[168:171], v[180:183], v[206:209], v[168:171]
	s_waitcnt lgkmcnt(3)
	v_mfma_f32_16x16x32_bf16 v[164:167], v[198:201], v[206:209], v[164:167]
	s_waitcnt lgkmcnt(2)
	v_mfma_f32_16x16x32_bf16 v[160:163], v[202:205], v[206:209], v[160:163]
	s_waitcnt lgkmcnt(1)
	v_mfma_f32_16x16x32_bf16 v[156:159], v[176:179], v[210:213], v[156:159]
	s_mov_b32 m0, s6
	s_nop 0
	buffer_load_dwordx4 v191, s[20:23], s37 offen lds
	ds_read_b128 v[206:209], v186 offset:6144
	s_waitcnt vmcnt(10)
	v_cvt_pk_bf16_f32 v15, v14, v15
	v_cvt_pk_bf16_f32 v14, v12, v13
	v_mfma_f32_16x16x32_bf16 v[152:155], v[180:183], v[210:213], v[152:155]
	ds_write_b64 v185, v[14:15] offset:34816
	v_mfma_f32_16x16x32_bf16 v[148:151], v[198:201], v[210:213], v[148:151]
	s_mov_b32 m0, s47
	s_nop 0
	buffer_load_dwordx4 v190, s[20:23], s37 offen lds
	v_mfma_f32_16x16x32_bf16 v[144:147], v[202:205], v[210:213], v[144:147]
	s_waitcnt lgkmcnt(2)
	v_mfma_f32_16x16x32_bf16 v[132:135], v[176:179], v[214:217], v[132:135]
	s_mov_b32 m0, s48
	s_nop 0
	buffer_load_dwordx4 v193, s[20:23], s37 offen lds
	s_add_i32 s37, s17, 0xfff20000
	ds_read_b128 v[210:213], v186 offset:8192
	v_mfma_f32_16x16x32_bf16 v[124:127], v[180:183], v[214:217], v[124:127]
	v_mfma_f32_16x16x32_bf16 v[120:123], v[198:201], v[214:217], v[120:123]
	v_mfma_f32_16x16x32_bf16 v[140:143], v[202:205], v[214:217], v[140:143]
	s_waitcnt lgkmcnt(2)
	v_mfma_f32_16x16x32_bf16 v[136:139], v[176:179], v[206:209], v[136:139]
	ds_read_b128 v[214:217], v186 offset:10240
	buffer_load_dwordx4 v[12:15], v184, s[24:27], s37 offen
	s_waitcnt vmcnt(12)
	v_cvt_pk_bf16_f32 v3, v2, v3
	v_cvt_pk_bf16_f32 v2, v0, v1
	v_mfma_f32_16x16x32_bf16 v[128:131], v[180:183], v[206:209], v[128:131]
	ds_write_b64 v185, v[2:3] offset:43520
	v_mfma_f32_16x16x32_bf16 v[116:119], v[198:201], v[206:209], v[116:119]
	v_mfma_f32_16x16x32_bf16 v[112:115], v[202:205], v[206:209], v[112:115]
	s_add_i32 s38, s17, 0xfff40000
	s_waitcnt lgkmcnt(2)
	v_mfma_f32_16x16x32_bf16 v[100:103], v[176:179], v[210:213], v[100:103]
	ds_read_b128 v[206:209], v186 offset:12288
	v_mfma_f32_16x16x32_bf16 v[92:95], v[180:183], v[210:213], v[92:95]
	v_mfma_f32_16x16x32_bf16 v[88:91], v[198:201], v[210:213], v[88:91]
	v_mfma_f32_16x16x32_bf16 v[108:111], v[202:205], v[210:213], v[108:111]
	s_waitcnt lgkmcnt(2)
	v_mfma_f32_16x16x32_bf16 v[104:107], v[176:179], v[214:217], v[104:107]
	ds_read_b128 v[210:213], v186 offset:14336
	buffer_load_dwordx4 v[0:3], v184, s[24:27], s38 offen
	s_waitcnt vmcnt(12)
	v_cvt_pk_bf16_f32 v31, v30, v31
	v_cvt_pk_bf16_f32 v30, v28, v29
	v_mfma_f32_16x16x32_bf16 v[96:99], v[180:183], v[214:217], v[96:99]
	ds_write_b64 v185, v[30:31] offset:52224
	v_mfma_f32_16x16x32_bf16 v[84:87], v[198:201], v[214:217], v[84:87]
	v_mfma_f32_16x16x32_bf16 v[80:83], v[202:205], v[214:217], v[80:83]
	s_add_i32 s39, s17, 0xfff60000
	s_waitcnt lgkmcnt(2)
	v_mfma_f32_16x16x32_bf16 v[72:75], v[176:179], v[206:209], v[72:75]
	ds_read_b128 v[214:217], v186 offset:16384
	v_mfma_f32_16x16x32_bf16 v[64:67], v[180:183], v[206:209], v[64:67]
	v_mfma_f32_16x16x32_bf16 v[60:63], v[198:201], v[206:209], v[60:63]
	v_mfma_f32_16x16x32_bf16 v[76:79], v[202:205], v[206:209], v[76:79]
	s_waitcnt lgkmcnt(2)
	v_mfma_f32_16x16x32_bf16 v[68:71], v[176:179], v[210:213], v[68:71]
	ds_read_b128 v[206:209], v186 offset:1024
	buffer_load_dwordx4 v[28:31], v184, s[24:27], s39 offen
	s_waitcnt vmcnt(12)
	v_cvt_pk_bf16_f32 v27, v26, v27
	v_cvt_pk_bf16_f32 v26, v24, v25
	v_mfma_f32_16x16x32_bf16 v[56:59], v[180:183], v[210:213], v[56:59]
	ds_write_b64 v185, v[26:27] offset:60928
	v_mfma_f32_16x16x32_bf16 v[52:55], v[198:201], v[210:213], v[52:55]
	v_mfma_f32_16x16x32_bf16 v[48:51], v[202:205], v[210:213], v[48:51]
	s_add_i32 s42, s17, 0xfff80000
	ds_read_b128 v[210:213], v186 offset:3072
	s_waitcnt lgkmcnt(3)
	v_mfma_f32_16x16x32_bf16 v[44:47], v[176:179], v[214:217], v[44:47]
	ds_read_b64_tr_b16 v[246:247], v188 offset:17408
	ds_read_b64_tr_b16 v[220:221], v188 offset:17440
	ds_read_b64_tr_b16 v[244:245], v187 offset:17408
	ds_read_b64_tr_b16 v[218:219], v187 offset:17440
	v_mfma_f32_16x16x32_bf16 v[40:43], v[180:183], v[214:217], v[40:43]
	ds_read_b64_tr_b16 v[248:249], v187 offset:17472
	ds_read_b64_tr_b16 v[250:251], v188 offset:17472
	v_mfma_f32_16x16x32_bf16 v[36:39], v[198:201], v[214:217], v[36:39]
	ds_read_b64_tr_b16 v[252:253], v187 offset:17504
	ds_read_b64_tr_b16 v[254:255], v188 offset:17504
	v_mfma_f32_16x16x32_bf16 v[32:35], v[202:205], v[214:217], v[32:35]
	s_waitcnt lgkmcnt(5)
; #define G_DMA_A(kt, AO) do { G_DMA1(kt, AO, 0); G_DMA1(kt, AO, 1); G_DMA1(kt, AO, 2); G_DMA1(kt, AO, 3); if (MF == 9) G_DMA5(kt, AO); } while (0)
; #define G_ISSUE_B(kt) do { const unsigned _sb = (unsigned)(kt) * 4u * kstepB; \
;         _Pragma("unroll") for (int _i = 0; _i < 8; ++_i) sb[_i] = bload16(_i < 4 ? rsB0 : rsB1, vob, _sb + (_i & 3) * kstepB); } while (0)
; #define G_WRITE_B(BO) do { \
;         _Pragma("unroll") for (int _i = 0; _i < 8; ++_i) *(LAS u32x2*)(b_wr + (BO) + (_i & 3) * (16 * G_BSTRIDE) + (_i >> 2) * SLAB1) = pack4(__builtin_bit_cast(f32x4, sb[_i])); } while (0)
; #define G_ENDTILE(VM) do { asm volatile("s_waitcnt vmcnt(" #VM ")" ::: "memory"); \
;         asm volatile("s_waitcnt lgkmcnt(0)" ::: "memory"); __builtin_amdgcn_s_barrier(); asm volatile("" ::: "memory"); } while (0)
;     ...
;     __builtin_amdgcn_s_barrier();
;     G_DMA_A(0, G_A0); G_ISSUE_B(0); G_WRITE_B(G_B0);
;     __builtin_amdgcn_sched_barrier(0);
;     G_ISSUE_B(1);
;     __builtin_amdgcn_sched_barrier(0);
;     G_ENDTILE(8);
;     for (int ui = 0;; ++ui) {
; #pragma unroll
;         for (int m = 0; m < MF; ++m)
; #pragma unroll
;             for (int n = 0; n < 4; ++n) acc[m][n] = (f32x4){0.f, 0.f, 0.f, 0.f};
;         for (int t = 0; t < nt - 2; t += 2) {
;             G_TILE(G_A0, G_B0, true, G_B1, G_A1, t + 1, true, t + 2, (void)0);
;             G_ENDTILE(8);
;             G_TILE(G_A1, G_B1, true, G_B0, G_A0, t + 2, true, t + 3, (void)0);
;             G_ENDTILE(8);
	v_mfma_f32_16x16x32_bf16 v[172:175], v[244:247], v[206:209], v[172:175]
	ds_read_b128 v[202:205], v186 offset:5120
	buffer_load_dwordx4 v[24:27], v184, s[24:27], s42 offen
	s_waitcnt vmcnt(12)
	v_cvt_pk_bf16_f32 v23, v22, v23
	v_cvt_pk_bf16_f32 v22, v20, v21
	s_waitcnt lgkmcnt(5)
	v_mfma_f32_16x16x32_bf16 v[168:171], v[218:221], v[206:209], v[168:171]
	ds_write_b64 v185, v[22:23] offset:34880
	s_waitcnt lgkmcnt(4)
	v_mfma_f32_16x16x32_bf16 v[164:167], v[248:251], v[206:209], v[164:167]
	s_waitcnt lgkmcnt(2)
	v_mfma_f32_16x16x32_bf16 v[160:163], v[252:255], v[206:209], v[160:163]
	v_mfma_f32_16x16x32_bf16 v[156:159], v[244:247], v[210:213], v[156:159]
	ds_read_b128 v[206:209], v186 offset:7168
	v_mfma_f32_16x16x32_bf16 v[152:155], v[218:221], v[210:213], v[152:155]
	v_mfma_f32_16x16x32_bf16 v[148:151], v[248:251], v[210:213], v[148:151]
	v_mfma_f32_16x16x32_bf16 v[144:147], v[252:255], v[210:213], v[144:147]
	s_waitcnt lgkmcnt(2)
	v_mfma_f32_16x16x32_bf16 v[132:135], v[244:247], v[202:205], v[132:135]
	ds_read_b128 v[210:213], v186 offset:9216
	buffer_load_dwordx4 v[20:23], v184, s[28:31], s37 offen
	s_waitcnt vmcnt(12)
	v_cvt_pk_bf16_f32 v7, v6, v7
	v_cvt_pk_bf16_f32 v6, v4, v5
	v_mfma_f32_16x16x32_bf16 v[124:127], v[218:221], v[202:205], v[124:127]
	ds_write_b64 v185, v[6:7] offset:43584
	v_mfma_f32_16x16x32_bf16 v[120:123], v[248:251], v[202:205], v[120:123]
	v_mfma_f32_16x16x32_bf16 v[140:143], v[252:255], v[202:205], v[140:143]
	s_waitcnt lgkmcnt(2)
	v_mfma_f32_16x16x32_bf16 v[136:139], v[244:247], v[206:209], v[136:139]
	ds_read_b128 v[202:205], v186 offset:11264
	v_mfma_f32_16x16x32_bf16 v[128:131], v[218:221], v[206:209], v[128:131]
	v_mfma_f32_16x16x32_bf16 v[116:119], v[248:251], v[206:209], v[116:119]
	v_mfma_f32_16x16x32_bf16 v[112:115], v[252:255], v[206:209], v[112:115]
	s_waitcnt lgkmcnt(2)
	v_mfma_f32_16x16x32_bf16 v[100:103], v[244:247], v[210:213], v[100:103]
	ds_read_b128 v[206:209], v186 offset:13312
	buffer_load_dwordx4 v[4:7], v184, s[28:31], s38 offen
	s_waitcnt vmcnt(12)
	v_cvt_pk_bf16_f32 v11, v10, v11
	v_cvt_pk_bf16_f32 v10, v8, v9
	v_mfma_f32_16x16x32_bf16 v[92:95], v[218:221], v[210:213], v[92:95]
	ds_write_b64 v185, v[10:11] offset:52288
	v_mfma_f32_16x16x32_bf16 v[88:91], v[248:251], v[210:213], v[88:91]
	v_mfma_f32_16x16x32_bf16 v[108:111], v[252:255], v[210:213], v[108:111]
	s_waitcnt lgkmcnt(2)
	v_mfma_f32_16x16x32_bf16 v[104:107], v[244:247], v[202:205], v[104:107]
	ds_read_b128 v[210:213], v186 offset:15360
	v_mfma_f32_16x16x32_bf16 v[96:99], v[218:221], v[202:205], v[96:99]
	v_mfma_f32_16x16x32_bf16 v[84:87], v[248:251], v[202:205], v[84:87]
	v_mfma_f32_16x16x32_bf16 v[80:83], v[252:255], v[202:205], v[80:83]
	s_waitcnt lgkmcnt(2)
	v_mfma_f32_16x16x32_bf16 v[72:75], v[244:247], v[206:209], v[72:75]
	ds_read_b128 v[238:241], v186 offset:17408
	buffer_load_dwordx4 v[8:11], v184, s[28:31], s39 offen
	s_waitcnt vmcnt(12)
	v_cvt_pk_bf16_f32 v19, v18, v19
	v_cvt_pk_bf16_f32 v18, v16, v17
	v_mfma_f32_16x16x32_bf16 v[64:67], v[218:221], v[206:209], v[64:67]
	ds_write_b64 v185, v[18:19] offset:60992
	v_mfma_f32_16x16x32_bf16 v[60:63], v[248:251], v[206:209], v[60:63]
	v_mfma_f32_16x16x32_bf16 v[76:79], v[252:255], v[206:209], v[76:79]
	s_waitcnt lgkmcnt(2)
	v_mfma_f32_16x16x32_bf16 v[68:71], v[244:247], v[210:213], v[68:71]
	v_mfma_f32_16x16x32_bf16 v[56:59], v[218:221], v[210:213], v[56:59]
	v_mfma_f32_16x16x32_bf16 v[52:55], v[248:251], v[210:213], v[52:55]
	v_mfma_f32_16x16x32_bf16 v[48:51], v[252:255], v[210:213], v[48:51]
	s_waitcnt lgkmcnt(1)
	buffer_load_dwordx4 v[16:19], v184, s[28:31], s42 offen
	s_waitcnt vmcnt(8)
	s_mov_b32 m0, s46
	s_waitcnt lgkmcnt(0)
	s_barrier
	ds_read_b64_tr_b16 v[178:179], v188 offset:34816
	ds_read_b64_tr_b16 v[176:177], v187 offset:34816
	ds_read_b64_tr_b16 v[180:181], v187 offset:34848
	ds_read_b64_tr_b16 v[198:199], v187 offset:34880
	ds_read_b64_tr_b16 v[202:203], v187 offset:34912
	ds_read_b128 v[206:209], v186 offset:36864
	ds_read_b64_tr_b16 v[182:183], v188 offset:34848
	ds_read_b64_tr_b16 v[200:201], v188 offset:34880
	ds_read_b64_tr_b16 v[204:205], v188 offset:34912
	ds_read_b128 v[210:213], v186 offset:38912
	ds_read_b128 v[214:217], v186 offset:40960
	buffer_load_dwordx4 v189, s[20:23], s36 offen lds
	s_mov_b32 m0, s86
	v_mfma_f32_16x16x32_bf16 v[44:47], v[244:247], v[238:241], v[44:47]
	v_mfma_f32_16x16x32_bf16 v[40:43], v[218:221], v[238:241], v[40:43]
	v_mfma_f32_16x16x32_bf16 v[36:39], v[248:251], v[238:241], v[36:39]
	v_mfma_f32_16x16x32_bf16 v[32:35], v[252:255], v[238:241], v[32:35]
	s_waitcnt lgkmcnt(5)
	v_mfma_f32_16x16x32_bf16 v[172:175], v[176:179], v[206:209], v[172:175]
	buffer_load_dwordx4 v192, s[20:23], s36 offen lds
	s_add_i32 s37, s17, 0xfffa0000
	s_waitcnt lgkmcnt(4)
	v_mfma_f32_16x16x32_bf16 v[168:171], v[180:183], v[206:209], v[168:171]
	s_waitcnt lgkmcnt(3)
	v_mfma_f32_16x16x32_bf16 v[164:167], v[198:201], v[206:209], v[164:167]
	s_waitcnt lgkmcnt(2)
	v_mfma_f32_16x16x32_bf16 v[160:163], v[202:205], v[206:209], v[160:163]
	s_waitcnt lgkmcnt(1)
	v_mfma_f32_16x16x32_bf16 v[156:159], v[176:179], v[210:213], v[156:159]
	s_mov_b32 m0, s89
	s_nop 0
	buffer_load_dwordx4 v191, s[20:23], s36 offen lds
	ds_read_b128 v[206:209], v186 offset:43008
	s_waitcnt vmcnt(10)
	v_cvt_pk_bf16_f32 v15, v14, v15
	v_cvt_pk_bf16_f32 v14, v12, v13
	v_mfma_f32_16x16x32_bf16 v[152:155], v[180:183], v[210:213], v[152:155]
	ds_write_b64 v185, v[14:15]
	v_mfma_f32_16x16x32_bf16 v[148:151], v[198:201], v[210:213], v[148:151]
	s_mov_b32 m0, s90
	s_nop 0
	buffer_load_dwordx4 v190, s[20:23], s36 offen lds
	v_mfma_f32_16x16x32_bf16 v[144:147], v[202:205], v[210:213], v[144:147]
	s_waitcnt lgkmcnt(2)
; #define G_DMA_A(kt, AO) do { G_DMA1(kt, AO, 0); G_DMA1(kt, AO, 1); G_DMA1(kt, AO, 2); G_DMA1(kt, AO, 3); if (MF == 9) G_DMA5(kt, AO); } while (0)
; #define G_ISSUE_B(kt) do { const unsigned _sb = (unsigned)(kt) * 4u * kstepB; \
;         _Pragma("unroll") for (int _i = 0; _i < 8; ++_i) sb[_i] = bload16(_i < 4 ? rsB0 : rsB1, vob, _sb + (_i & 3) * kstepB); } while (0)
; #define G_WRITE_B(BO) do { \
;         _Pragma("unroll") for (int _i = 0; _i < 8; ++_i) *(LAS u32x2*)(b_wr + (BO) + (_i & 3) * (16 * G_BSTRIDE) + (_i >> 2) * SLAB1) = pack4(__builtin_bit_cast(f32x4, sb[_i])); } while (0)
; #define G_ENDTILE(VM) do { asm volatile("s_waitcnt vmcnt(" #VM ")" ::: "memory"); \
;         asm volatile("s_waitcnt lgkmcnt(0)" ::: "memory"); __builtin_amdgcn_s_barrier(); asm volatile("" ::: "memory"); } while (0)
;     ...
;     __builtin_amdgcn_s_barrier();
;     G_DMA_A(0, G_A0); G_ISSUE_B(0); G_WRITE_B(G_B0);
;     __builtin_amdgcn_sched_barrier(0);
;     G_ISSUE_B(1);
;     __builtin_amdgcn_sched_barrier(0);
;     G_ENDTILE(8);
;     for (int ui = 0;; ++ui) {
; #pragma unroll
;         for (int m = 0; m < MF; ++m)
; #pragma unroll
;             for (int n = 0; n < 4; ++n) acc[m][n] = (f32x4){0.f, 0.f, 0.f, 0.f};
;         for (int t = 0; t < nt - 2; t += 2) {
;             G_TILE(G_A0, G_B0, true, G_B1, G_A1, t + 1, true, t + 2, (void)0);
	v_mfma_f32_16x16x32_bf16 v[132:135], v[176:179], v[214:217], v[132:135]
	s_mov_b32 m0, s91
	s_nop 0
	buffer_load_dwordx4 v193, s[20:23], s36 offen lds
	ds_read_b128 v[210:213], v186 offset:45056
	v_mfma_f32_16x16x32_bf16 v[124:127], v[180:183], v[214:217], v[124:127]
	v_mfma_f32_16x16x32_bf16 v[120:123], v[198:201], v[214:217], v[120:123]
	v_mfma_f32_16x16x32_bf16 v[140:143], v[202:205], v[214:217], v[140:143]
	s_waitcnt lgkmcnt(2)
	v_mfma_f32_16x16x32_bf16 v[136:139], v[176:179], v[206:209], v[136:139]
	ds_read_b128 v[214:217], v186 offset:47104
	buffer_load_dwordx4 v[12:15], v184, s[24:27], s37 offen
	s_waitcnt vmcnt(12)
	v_cvt_pk_bf16_f32 v3, v2, v3
	v_cvt_pk_bf16_f32 v2, v0, v1
	v_mfma_f32_16x16x32_bf16 v[128:131], v[180:183], v[206:209], v[128:131]
	ds_write_b64 v185, v[2:3] offset:8704
	v_mfma_f32_16x16x32_bf16 v[116:119], v[198:201], v[206:209], v[116:119]
	v_mfma_f32_16x16x32_bf16 v[112:115], v[202:205], v[206:209], v[112:115]
	s_add_i32 s38, s17, 0xfffc0000
	s_waitcnt lgkmcnt(2)
	v_mfma_f32_16x16x32_bf16 v[100:103], v[176:179], v[210:213], v[100:103]
	ds_read_b128 v[206:209], v186 offset:49152
	v_mfma_f32_16x16x32_bf16 v[92:95], v[180:183], v[210:213], v[92:95]
	v_mfma_f32_16x16x32_bf16 v[88:91], v[198:201], v[210:213], v[88:91]
	v_mfma_f32_16x16x32_bf16 v[108:111], v[202:205], v[210:213], v[108:111]
	s_waitcnt lgkmcnt(2)
	v_mfma_f32_16x16x32_bf16 v[104:107], v[176:179], v[214:217], v[104:107]
	ds_read_b128 v[210:213], v186 offset:51200
	buffer_load_dwordx4 v[0:3], v184, s[24:27], s38 offen
	s_waitcnt vmcnt(12)
	v_cvt_pk_bf16_f32 v31, v30, v31
	v_cvt_pk_bf16_f32 v30, v28, v29
	v_mfma_f32_16x16x32_bf16 v[96:99], v[180:183], v[214:217], v[96:99]
	ds_write_b64 v185, v[30:31] offset:17408
	v_mfma_f32_16x16x32_bf16 v[84:87], v[198:201], v[214:217], v[84:87]
	v_mfma_f32_16x16x32_bf16 v[80:83], v[202:205], v[214:217], v[80:83]
	s_add_i32 s39, s17, 0xfffe0000
	s_waitcnt lgkmcnt(2)
	v_mfma_f32_16x16x32_bf16 v[72:75], v[176:179], v[206:209], v[72:75]
	ds_read_b128 v[214:217], v186 offset:53248
	v_mfma_f32_16x16x32_bf16 v[64:67], v[180:183], v[206:209], v[64:67]
	v_mfma_f32_16x16x32_bf16 v[60:63], v[198:201], v[206:209], v[60:63]
	v_mfma_f32_16x16x32_bf16 v[76:79], v[202:205], v[206:209], v[76:79]
	s_waitcnt lgkmcnt(2)
	v_mfma_f32_16x16x32_bf16 v[68:71], v[176:179], v[210:213], v[68:71]
	ds_read_b128 v[206:209], v186 offset:37888
	buffer_load_dwordx4 v[28:31], v184, s[24:27], s39 offen
	s_waitcnt vmcnt(12)
	v_cvt_pk_bf16_f32 v27, v26, v27
	v_cvt_pk_bf16_f32 v26, v24, v25
	v_mfma_f32_16x16x32_bf16 v[56:59], v[180:183], v[210:213], v[56:59]
	ds_write_b64 v185, v[26:27] offset:26112
	v_mfma_f32_16x16x32_bf16 v[52:55], v[198:201], v[210:213], v[52:55]
	v_mfma_f32_16x16x32_bf16 v[48:51], v[202:205], v[210:213], v[48:51]
	ds_read_b128 v[210:213], v186 offset:39936
	s_waitcnt lgkmcnt(3)
	v_mfma_f32_16x16x32_bf16 v[44:47], v[176:179], v[214:217], v[44:47]
	ds_read_b64_tr_b16 v[246:247], v188 offset:52224
	ds_read_b64_tr_b16 v[220:221], v188 offset:52256
	ds_read_b64_tr_b16 v[244:245], v187 offset:52224
	ds_read_b64_tr_b16 v[218:219], v187 offset:52256
	v_mfma_f32_16x16x32_bf16 v[40:43], v[180:183], v[214:217], v[40:43]
	ds_read_b64_tr_b16 v[248:249], v187 offset:52288
	ds_read_b64_tr_b16 v[250:251], v188 offset:52288
	v_mfma_f32_16x16x32_bf16 v[36:39], v[198:201], v[214:217], v[36:39]
	ds_read_b64_tr_b16 v[252:253], v187 offset:52320
	ds_read_b64_tr_b16 v[254:255], v188 offset:52320
	v_mfma_f32_16x16x32_bf16 v[32:35], v[202:205], v[214:217], v[32:35]
	s_waitcnt lgkmcnt(5)
	v_mfma_f32_16x16x32_bf16 v[172:175], v[244:247], v[206:209], v[172:175]
	ds_read_b128 v[202:205], v186 offset:41984
	buffer_load_dwordx4 v[24:27], v184, s[24:27], s17 offen
	s_waitcnt vmcnt(12)
; #define G_DMA_A(kt, AO) do { G_DMA1(kt, AO, 0); G_DMA1(kt, AO, 1); G_DMA1(kt, AO, 2); G_DMA1(kt, AO, 3); if (MF == 9) G_DMA5(kt, AO); } while (0)
; #define G_ISSUE_B(kt) do { const unsigned _sb = (unsigned)(kt) * 4u * kstepB; \
;         _Pragma("unroll") for (int _i = 0; _i < 8; ++_i) sb[_i] = bload16(_i < 4 ? rsB0 : rsB1, vob, _sb + (_i & 3) * kstepB); } while (0)
; #define G_WRITE_B(BO) do { \
;         _Pragma("unroll") for (int _i = 0; _i < 8; ++_i) *(LAS u32x2*)(b_wr + (BO) + (_i & 3) * (16 * G_BSTRIDE) + (_i >> 2) * SLAB1) = pack4(__builtin_bit_cast(f32x4, sb[_i])); } while (0)
; #define G_ENDTILE(VM) do { asm volatile("s_waitcnt vmcnt(" #VM ")" ::: "memory"); \
;         asm volatile("s_waitcnt lgkmcnt(0)" ::: "memory"); __builtin_amdgcn_s_barrier(); asm volatile("" ::: "memory"); } while (0)
;     ...
;     __builtin_amdgcn_s_barrier();
;     G_DMA_A(0, G_A0); G_ISSUE_B(0); G_WRITE_B(G_B0);
;     __builtin_amdgcn_sched_barrier(0);
;     G_ISSUE_B(1);
;     __builtin_amdgcn_sched_barrier(0);
;     G_ENDTILE(8);
;     for (int ui = 0;; ++ui) {
; #pragma unroll
;         for (int m = 0; m < MF; ++m)
; #pragma unroll
;             for (int n = 0; n < 4; ++n) acc[m][n] = (f32x4){0.f, 0.f, 0.f, 0.f};
;         for (int t = 0; t < nt - 2; t += 2) {
;             G_TILE(G_A0, G_B0, true, G_B1, G_A1, t + 1, true, t + 2, (void)0);
;             G_ENDTILE(8);
;             G_TILE(G_A1, G_B1, true, G_B0, G_A0, t + 2, true, t + 3, (void)0);
;             G_ENDTILE(8);
;         }
	v_cvt_pk_bf16_f32 v23, v22, v23
	v_cvt_pk_bf16_f32 v22, v20, v21
	s_waitcnt lgkmcnt(5)
	v_mfma_f32_16x16x32_bf16 v[168:171], v[218:221], v[206:209], v[168:171]
	ds_write_b64 v185, v[22:23] offset:64
	s_waitcnt lgkmcnt(4)
	v_mfma_f32_16x16x32_bf16 v[164:167], v[248:251], v[206:209], v[164:167]
	s_waitcnt lgkmcnt(2)
	v_mfma_f32_16x16x32_bf16 v[160:163], v[252:255], v[206:209], v[160:163]
	v_mfma_f32_16x16x32_bf16 v[156:159], v[244:247], v[210:213], v[156:159]
	ds_read_b128 v[206:209], v186 offset:44032
	v_mfma_f32_16x16x32_bf16 v[152:155], v[218:221], v[210:213], v[152:155]
	v_mfma_f32_16x16x32_bf16 v[148:151], v[248:251], v[210:213], v[148:151]
	v_mfma_f32_16x16x32_bf16 v[144:147], v[252:255], v[210:213], v[144:147]
	s_waitcnt lgkmcnt(2)
	v_mfma_f32_16x16x32_bf16 v[132:135], v[244:247], v[202:205], v[132:135]
	ds_read_b128 v[210:213], v186 offset:46080
	buffer_load_dwordx4 v[20:23], v184, s[28:31], s37 offen
	s_waitcnt vmcnt(12)
	v_cvt_pk_bf16_f32 v7, v6, v7
	v_cvt_pk_bf16_f32 v6, v4, v5
	v_mfma_f32_16x16x32_bf16 v[124:127], v[218:221], v[202:205], v[124:127]
	ds_write_b64 v185, v[6:7] offset:8768
	v_mfma_f32_16x16x32_bf16 v[120:123], v[248:251], v[202:205], v[120:123]
	v_mfma_f32_16x16x32_bf16 v[140:143], v[252:255], v[202:205], v[140:143]
	s_waitcnt lgkmcnt(2)
	v_mfma_f32_16x16x32_bf16 v[136:139], v[244:247], v[206:209], v[136:139]
	ds_read_b128 v[202:205], v186 offset:48128
	v_mfma_f32_16x16x32_bf16 v[128:131], v[218:221], v[206:209], v[128:131]
	v_mfma_f32_16x16x32_bf16 v[116:119], v[248:251], v[206:209], v[116:119]
	v_mfma_f32_16x16x32_bf16 v[112:115], v[252:255], v[206:209], v[112:115]
	s_waitcnt lgkmcnt(2)
	v_mfma_f32_16x16x32_bf16 v[100:103], v[244:247], v[210:213], v[100:103]
	ds_read_b128 v[206:209], v186 offset:50176
	buffer_load_dwordx4 v[4:7], v184, s[28:31], s38 offen
	s_waitcnt vmcnt(12)
	v_cvt_pk_bf16_f32 v11, v10, v11
	v_cvt_pk_bf16_f32 v10, v8, v9
	v_mfma_f32_16x16x32_bf16 v[92:95], v[218:221], v[210:213], v[92:95]
	ds_write_b64 v185, v[10:11] offset:17472
	v_mfma_f32_16x16x32_bf16 v[88:91], v[248:251], v[210:213], v[88:91]
	v_mfma_f32_16x16x32_bf16 v[108:111], v[252:255], v[210:213], v[108:111]
	s_waitcnt lgkmcnt(2)
	v_mfma_f32_16x16x32_bf16 v[104:107], v[244:247], v[202:205], v[104:107]
	ds_read_b128 v[210:213], v186 offset:52224
	v_mfma_f32_16x16x32_bf16 v[96:99], v[218:221], v[202:205], v[96:99]
	v_mfma_f32_16x16x32_bf16 v[84:87], v[248:251], v[202:205], v[84:87]
	v_mfma_f32_16x16x32_bf16 v[80:83], v[252:255], v[202:205], v[80:83]
	s_waitcnt lgkmcnt(2)
	v_mfma_f32_16x16x32_bf16 v[72:75], v[244:247], v[206:209], v[72:75]
	ds_read_b128 v[238:241], v186 offset:54272
	buffer_load_dwordx4 v[8:11], v184, s[28:31], s39 offen
	s_waitcnt vmcnt(12)
	v_cvt_pk_bf16_f32 v19, v18, v19
	v_cvt_pk_bf16_f32 v18, v16, v17
	v_mfma_f32_16x16x32_bf16 v[64:67], v[218:221], v[206:209], v[64:67]
	ds_write_b64 v185, v[18:19] offset:26176
	v_mfma_f32_16x16x32_bf16 v[60:63], v[248:251], v[206:209], v[60:63]
	v_mfma_f32_16x16x32_bf16 v[76:79], v[252:255], v[206:209], v[76:79]
	s_waitcnt lgkmcnt(2)
	v_mfma_f32_16x16x32_bf16 v[68:71], v[244:247], v[210:213], v[68:71]
	v_mfma_f32_16x16x32_bf16 v[56:59], v[218:221], v[210:213], v[56:59]
	v_mfma_f32_16x16x32_bf16 v[52:55], v[248:251], v[210:213], v[52:55]
	v_mfma_f32_16x16x32_bf16 v[48:51], v[252:255], v[210:213], v[48:51]
	s_waitcnt lgkmcnt(1)
	buffer_load_dwordx4 v[16:19], v184, s[28:31], s17 offen
	s_add_i32 s16, s16, 2
	s_add_i32 s17, s17, 0x100000
	s_addk_i32 s36, 0x100
	s_cmp_ge_i32 s16, s97
	s_waitcnt vmcnt(8)
	s_waitcnt lgkmcnt(0)
	s_barrier
	s_cbranch_scc0 .LBB0_651

; #define G_DMA_A(kt, AO) do { G_DMA1(kt, AO, 0); G_DMA1(kt, AO, 1); G_DMA1(kt, AO, 2); G_DMA1(kt, AO, 3); if (MF == 9) G_DMA5(kt, AO); } while (0)
; #define G_ISSUE_B(kt) do { const unsigned _sb = (unsigned)(kt) * 4u * kstepB; \
;         _Pragma("unroll") for (int _i = 0; _i < 8; ++_i) sb[_i] = bload16(_i < 4 ? rsB0 : rsB1, vob, _sb + (_i & 3) * kstepB); } while (0)
; #define G_WRITE_B(BO) do { \
;         _Pragma("unroll") for (int _i = 0; _i < 8; ++_i) *(LAS u32x2*)(b_wr + (BO) + (_i & 3) * (16 * G_BSTRIDE) + (_i >> 2) * SLAB1) = pack4(__builtin_bit_cast(f32x4, sb[_i])); } while (0)
; #define G_ENDTILE(VM) do { asm volatile("s_waitcnt vmcnt(" #VM ")" ::: "memory"); \
;         asm volatile("s_waitcnt lgkmcnt(0)" ::: "memory"); __builtin_amdgcn_s_barrier(); asm volatile("" ::: "memory"); } while (0)
;     ...
;     __builtin_amdgcn_s_barrier();
;     G_DMA_A(0, G_A0); G_ISSUE_B(0); G_WRITE_B(G_B0);
;     __builtin_amdgcn_sched_barrier(0);
;     G_ISSUE_B(1);
;     __builtin_amdgcn_sched_barrier(0);
;     G_ENDTILE(8);
;     for (int ui = 0;; ++ui) {
; #pragma unroll
;         for (int m = 0; m < MF; ++m)
; #pragma unroll
;             for (int n = 0; n < 4; ++n) acc[m][n] = (f32x4){0.f, 0.f, 0.f, 0.f};
;         for (int t = 0; t < nt - 2; t += 2) {
;             G_TILE(G_A0, G_B0, true, G_B1, G_A1, t + 1, true, t + 2, (void)0);
;             G_ENDTILE(8);
;             G_TILE(G_A1, G_B1, true, G_B0, G_A0, t + 2, true, t + 3, (void)0);
;             G_ENDTILE(8);
;         }
.Lchk5_s36:
	s_waitcnt lgkmcnt(1)
	buffer_load_dwordx4 v[16:19], v184, s[28:31], s17 offen
	s_add_i32 s16, s16, 2
	s_add_i32 s17, s17, 0x100000
	s_addk_i32 s36, 0x100
	s_cmp_ge_i32 s16, s97
	s_waitcnt vmcnt(8)
	s_waitcnt lgkmcnt(0)
	s_barrier
	s_cbranch_scc0 .Lchk5_loop
	s_cmp_le_u32 s99, 8
	s_cbranch_scc1 .Lchk5_s37
	v_mfma_f32_16x16x32_bf16 v[44:47], v[244:247], v[238:241], v[44:47]
	v_mfma_f32_16x16x32_bf16 v[40:43], v[218:221], v[238:241], v[40:43]
	v_mfma_f32_16x16x32_bf16 v[36:39], v[248:251], v[238:241], v[36:39]
	v_mfma_f32_16x16x32_bf16 v[32:35], v[252:255], v[238:241], v[32:35]

; #define G_DMA_A(kt, AO) do { G_DMA1(kt, AO, 0); G_DMA1(kt, AO, 1); G_DMA1(kt, AO, 2); G_DMA1(kt, AO, 3); if (MF == 9) G_DMA5(kt, AO); } while (0)
; #define G_ISSUE_B(kt) do { const unsigned _sb = (unsigned)(kt) * 4u * kstepB; \
;         _Pragma("unroll") for (int _i = 0; _i < 8; ++_i) sb[_i] = bload16(_i < 4 ? rsB0 : rsB1, vob, _sb + (_i & 3) * kstepB); } while (0)
; #define G_WRITE_B(BO) do { \
;         _Pragma("unroll") for (int _i = 0; _i < 8; ++_i) *(LAS u32x2*)(b_wr + (BO) + (_i & 3) * (16 * G_BSTRIDE) + (_i >> 2) * SLAB1) = pack4(__builtin_bit_cast(f32x4, sb[_i])); } while (0)
; #define G_ENDTILE(VM) do { asm volatile("s_waitcnt vmcnt(" #VM ")" ::: "memory"); \
;         asm volatile("s_waitcnt lgkmcnt(0)" ::: "memory"); __builtin_amdgcn_s_barrier(); asm volatile("" ::: "memory"); } while (0)
;     ...
;     __builtin_amdgcn_s_barrier();
;     G_DMA_A(0, G_A0); G_ISSUE_B(0); G_WRITE_B(G_B0);
;     __builtin_amdgcn_sched_barrier(0);
;     G_ISSUE_B(1);
;     __builtin_amdgcn_sched_barrier(0);
;     G_ENDTILE(8);
;     for (int ui = 0;; ++ui) {
; #pragma unroll
;         for (int m = 0; m < MF; ++m)
; #pragma unroll
;             for (int n = 0; n < 4; ++n) acc[m][n] = (f32x4){0.f, 0.f, 0.f, 0.f};
;         for (int t = 0; t < nt - 2; t += 2) {
;             G_TILE(G_A0, G_B0, true, G_B1, G_A1, t + 1, true, t + 2, (void)0);
.LBB0_861:
	s_andn2_b64 vcc, exec, s[28:29]
	v_mov_b32_e32 v175, 0
	s_cbranch_vccnz .LBB0_864
	s_mov_b32 s8, 0
	s_mov_b32 s9, 0x1e0000
	s_movk_i32 s36, 0x100
	s_waitcnt vmcnt(1)
	s_waitcnt vmcnt(0)
	s_cmp_lt_u32 s99, 9
	s_cbranch_scc1 .Lslow_P6
	s_mov_b32 m0, s85
	s_add_i32 s38, s36, 0xffffff80
	ds_read_b64_tr_b16 v[178:179], v206
	ds_read_b64_tr_b16 v[176:177], v205
	ds_read_b64_tr_b16 v[180:181], v205 offset:32
	ds_read_b64_tr_b16 v[184:185], v205 offset:64
	ds_read_b64_tr_b16 v[188:189], v205 offset:96
	ds_read_b128 v[192:195], v199
	ds_read_b64_tr_b16 v[182:183], v206 offset:32
	ds_read_b64_tr_b16 v[186:187], v206 offset:64
	ds_read_b64_tr_b16 v[190:191], v206 offset:96
	ds_read_b128 v[208:211], v199 offset:2048
	ds_read_b128 v[212:215], v199 offset:4096
	buffer_load_dwordx4 v200, s[20:23], s38 offen lds
	s_mov_b32 m0, s86
	s_waitcnt lgkmcnt(0)
	v_mfma_f32_16x16x32_bf16 v[172:175], v[176:179], v[192:195], 0
	buffer_load_dwordx4 v201, s[20:23], s38 offen lds
	v_mfma_f32_16x16x32_bf16 v[168:171], v[180:183], v[192:195], 0
	v_mfma_f32_16x16x32_bf16 v[164:167], v[184:187], v[192:195], 0
	v_mfma_f32_16x16x32_bf16 v[160:163], v[188:191], v[192:195], 0
	v_mfma_f32_16x16x32_bf16 v[156:159], v[176:179], v[208:211], 0
	s_mov_b32 m0, s87
	s_nop 0
	buffer_load_dwordx4 v202, s[20:23], s38 offen lds
	ds_read_b128 v[192:195], v199 offset:6144
	s_waitcnt vmcnt(10)
	v_cvt_pk_bf16_f32 v23, v22, v23
	v_cvt_pk_bf16_f32 v22, v20, v21
	v_mfma_f32_16x16x32_bf16 v[152:155], v[180:183], v[208:211], 0
	ds_write_b64 v198, v[22:23] offset:34816
	v_mfma_f32_16x16x32_bf16 v[148:151], v[184:187], v[208:211], 0
	s_mov_b32 m0, s88
	s_nop 0
	buffer_load_dwordx4 v203, s[20:23], s38 offen lds
	v_mfma_f32_16x16x32_bf16 v[144:147], v[188:191], v[208:211], 0
	v_mfma_f32_16x16x32_bf16 v[132:135], v[176:179], v[212:215], 0
	s_mov_b32 m0, s89
	s_nop 0
	buffer_load_dwordx4 v204, s[20:23], s38 offen lds
	s_add_i32 s38, s9, 0xfff20000
	ds_read_b128 v[208:211], v199 offset:8192
	v_mfma_f32_16x16x32_bf16 v[124:127], v[180:183], v[212:215], 0
	v_mfma_f32_16x16x32_bf16 v[120:123], v[184:187], v[212:215], 0
	v_mfma_f32_16x16x32_bf16 v[140:143], v[188:191], v[212:215], 0
	s_waitcnt lgkmcnt(2)
	v_mfma_f32_16x16x32_bf16 v[136:139], v[176:179], v[192:195], 0
	ds_read_b128 v[212:215], v199 offset:10240
	buffer_load_dwordx4 v[20:23], v197, s[24:27], s38 offen
	s_waitcnt vmcnt(11)
	v_cvt_pk_bf16_f32 v31, v30, v31
	v_cvt_pk_bf16_f32 v30, v28, v29
	v_mfma_f32_16x16x32_bf16 v[128:131], v[180:183], v[192:195], 0
	ds_write_b64 v198, v[30:31] offset:43520
	v_mfma_f32_16x16x32_bf16 v[116:119], v[184:187], v[192:195], 0
	v_mfma_f32_16x16x32_bf16 v[112:115], v[188:191], v[192:195], 0
	s_add_i32 s39, s9, 0xfff40000
	s_waitcnt lgkmcnt(2)
	v_mfma_f32_16x16x32_bf16 v[100:103], v[176:179], v[208:211], 0
	ds_read_b128 v[192:195], v199 offset:12288
	v_mfma_f32_16x16x32_bf16 v[92:95], v[180:183], v[208:211], 0
	v_mfma_f32_16x16x32_bf16 v[88:91], v[184:187], v[208:211], 0
	v_mfma_f32_16x16x32_bf16 v[108:111], v[188:191], v[208:211], 0
	s_waitcnt lgkmcnt(2)
	v_mfma_f32_16x16x32_bf16 v[104:107], v[176:179], v[212:215], 0
	ds_read_b128 v[208:211], v199 offset:14336
	v_cvt_pk_bf16_f32 v19, v18, v19
	v_cvt_pk_bf16_f32 v18, v16, v17
	v_mfma_f32_16x16x32_bf16 v[96:99], v[180:183], v[212:215], 0
	ds_write_b64 v198, v[18:19] offset:52224
	v_mfma_f32_16x16x32_bf16 v[84:87], v[184:187], v[212:215], 0
	v_mfma_f32_16x16x32_bf16 v[80:83], v[188:191], v[212:215], 0
	s_add_i32 s43, s9, 0xfff60000
	buffer_load_dwordx4 v[28:31], v197, s[24:27], s39 offen
	s_waitcnt lgkmcnt(2)
	v_mfma_f32_16x16x32_bf16 v[72:75], v[176:179], v[192:195], 0
	ds_read_b128 v[212:215], v199 offset:16384
	v_mfma_f32_16x16x32_bf16 v[64:67], v[180:183], v[192:195], 0
	v_mfma_f32_16x16x32_bf16 v[60:63], v[184:187], v[192:195], 0
	v_mfma_f32_16x16x32_bf16 v[76:79], v[188:191], v[192:195], 0
	s_waitcnt lgkmcnt(2)
	v_mfma_f32_16x16x32_bf16 v[68:71], v[176:179], v[208:211], 0
	ds_read_b128 v[192:195], v199 offset:1024
	buffer_load_dwordx4 v[16:19], v197, s[24:27], s43 offen
	s_waitcnt vmcnt(12)
	v_cvt_pk_bf16_f32 v27, v26, v27
	v_cvt_pk_bf16_f32 v26, v24, v25
	v_mfma_f32_16x16x32_bf16 v[56:59], v[180:183], v[208:211], 0
	ds_write_b64 v198, v[26:27] offset:60928
	v_mfma_f32_16x16x32_bf16 v[52:55], v[184:187], v[208:211], 0
	v_mfma_f32_16x16x32_bf16 v[48:51], v[188:191], v[208:211], 0
	s_add_i32 s45, s9, 0xfff80000
	ds_read_b128 v[208:211], v199 offset:3072
	s_waitcnt lgkmcnt(3)
	v_mfma_f32_16x16x32_bf16 v[44:47], v[176:179], v[212:215], 0
	ds_read_b64_tr_b16 v[246:247], v206 offset:17408
	ds_read_b64_tr_b16 v[218:219], v206 offset:17440
	ds_read_b64_tr_b16 v[244:245], v205 offset:17408
	ds_read_b64_tr_b16 v[216:217], v205 offset:17440
	v_mfma_f32_16x16x32_bf16 v[40:43], v[180:183], v[212:215], 0
	ds_read_b64_tr_b16 v[248:249], v205 offset:17472
	ds_read_b64_tr_b16 v[250:251], v206 offset:17472
	v_mfma_f32_16x16x32_bf16 v[36:39], v[184:187], v[212:215], 0
	ds_read_b64_tr_b16 v[252:253], v205 offset:17504
	ds_read_b64_tr_b16 v[254:255], v206 offset:17504
	v_mfma_f32_16x16x32_bf16 v[32:35], v[188:191], v[212:215], 0
	s_waitcnt lgkmcnt(5)
	v_mfma_f32_16x16x32_bf16 v[172:175], v[244:247], v[192:195], v[172:175]
	ds_read_b128 v[188:191], v199 offset:5120
	buffer_load_dwordx4 v[24:27], v197, s[24:27], s45 offen
	s_waitcnt vmcnt(12)
	v_cvt_pk_bf16_f32 v15, v14, v15
	v_cvt_pk_bf16_f32 v14, v12, v13
	s_waitcnt lgkmcnt(5)
	v_mfma_f32_16x16x32_bf16 v[168:171], v[216:219], v[192:195], v[168:171]
	ds_write_b64 v198, v[14:15] offset:35072
	s_waitcnt lgkmcnt(4)
	v_mfma_f32_16x16x32_bf16 v[164:167], v[248:251], v[192:195], v[164:167]
	s_waitcnt lgkmcnt(2)
; #define G_DMA_A(kt, AO) do { G_DMA1(kt, AO, 0); G_DMA1(kt, AO, 1); G_DMA1(kt, AO, 2); G_DMA1(kt, AO, 3); if (MF == 9) G_DMA5(kt, AO); } while (0)
; #define G_ISSUE_B(kt) do { const unsigned _sb = (unsigned)(kt) * 4u * kstepB; \
;         _Pragma("unroll") for (int _i = 0; _i < 8; ++_i) sb[_i] = bload16(_i < 4 ? rsB0 : rsB1, vob, _sb + (_i & 3) * kstepB); } while (0)
; #define G_WRITE_B(BO) do { \
;         _Pragma("unroll") for (int _i = 0; _i < 8; ++_i) *(LAS u32x2*)(b_wr + (BO) + (_i & 3) * (16 * G_BSTRIDE) + (_i >> 2) * SLAB1) = pack4(__builtin_bit_cast(f32x4, sb[_i])); } while (0)
; #define G_ENDTILE(VM) do { asm volatile("s_waitcnt vmcnt(" #VM ")" ::: "memory"); \
;         asm volatile("s_waitcnt lgkmcnt(0)" ::: "memory"); __builtin_amdgcn_s_barrier(); asm volatile("" ::: "memory"); } while (0)
;     ...
;     __builtin_amdgcn_s_barrier();
;     G_DMA_A(0, G_A0); G_ISSUE_B(0); G_WRITE_B(G_B0);
;     __builtin_amdgcn_sched_barrier(0);
;     G_ISSUE_B(1);
;     __builtin_amdgcn_sched_barrier(0);
;     G_ENDTILE(8);
;     for (int ui = 0;; ++ui) {
; #pragma unroll
;         for (int m = 0; m < MF; ++m)
; #pragma unroll
;             for (int n = 0; n < 4; ++n) acc[m][n] = (f32x4){0.f, 0.f, 0.f, 0.f};
;         for (int t = 0; t < nt - 2; t += 2) {
;             G_TILE(G_A0, G_B0, true, G_B1, G_A1, t + 1, true, t + 2, (void)0);
;             G_ENDTILE(8);
;             G_TILE(G_A1, G_B1, true, G_B0, G_A0, t + 2, true, t + 3, (void)0);
;             G_ENDTILE(8);
	v_mfma_f32_16x16x32_bf16 v[160:163], v[252:255], v[192:195], v[160:163]
	v_mfma_f32_16x16x32_bf16 v[156:159], v[244:247], v[208:211], v[156:159]
	ds_read_b128 v[192:195], v199 offset:7168
	v_mfma_f32_16x16x32_bf16 v[152:155], v[216:219], v[208:211], v[152:155]
	v_mfma_f32_16x16x32_bf16 v[148:151], v[248:251], v[208:211], v[148:151]
	v_mfma_f32_16x16x32_bf16 v[144:147], v[252:255], v[208:211], v[144:147]
	s_waitcnt lgkmcnt(2)
	v_mfma_f32_16x16x32_bf16 v[132:135], v[244:247], v[188:191], v[132:135]
	ds_read_b128 v[208:211], v199 offset:9216
	buffer_load_dwordx4 v[12:15], v197, s[16:19], s38 offen
	s_waitcnt vmcnt(11)
	v_cvt_pk_bf16_f32 v7, v6, v7
	v_cvt_pk_bf16_f32 v6, v4, v5
	v_mfma_f32_16x16x32_bf16 v[124:127], v[216:219], v[188:191], v[124:127]
	ds_write_b64 v198, v[6:7] offset:43776
	v_mfma_f32_16x16x32_bf16 v[120:123], v[248:251], v[188:191], v[120:123]
	v_mfma_f32_16x16x32_bf16 v[140:143], v[252:255], v[188:191], v[140:143]
	s_waitcnt lgkmcnt(2)
	v_mfma_f32_16x16x32_bf16 v[136:139], v[244:247], v[192:195], v[136:139]
	ds_read_b128 v[188:191], v199 offset:11264
	v_mfma_f32_16x16x32_bf16 v[128:131], v[216:219], v[192:195], v[128:131]
	v_mfma_f32_16x16x32_bf16 v[116:119], v[248:251], v[192:195], v[116:119]
	v_mfma_f32_16x16x32_bf16 v[112:115], v[252:255], v[192:195], v[112:115]
	s_waitcnt lgkmcnt(2)
	v_mfma_f32_16x16x32_bf16 v[100:103], v[244:247], v[208:211], v[100:103]
	ds_read_b128 v[192:195], v199 offset:13312
	v_cvt_pk_bf16_f32 v3, v2, v3
	v_cvt_pk_bf16_f32 v2, v0, v1
	v_mfma_f32_16x16x32_bf16 v[92:95], v[216:219], v[208:211], v[92:95]
	ds_write_b64 v198, v[2:3] offset:52480
	v_mfma_f32_16x16x32_bf16 v[88:91], v[248:251], v[208:211], v[88:91]
	v_mfma_f32_16x16x32_bf16 v[108:111], v[252:255], v[208:211], v[108:111]
	buffer_load_dwordx4 v[4:7], v197, s[16:19], s39 offen
	s_waitcnt lgkmcnt(2)
	v_mfma_f32_16x16x32_bf16 v[104:107], v[244:247], v[188:191], v[104:107]
	ds_read_b128 v[208:211], v199 offset:15360
	v_mfma_f32_16x16x32_bf16 v[96:99], v[216:219], v[188:191], v[96:99]
	v_mfma_f32_16x16x32_bf16 v[84:87], v[248:251], v[188:191], v[84:87]
	v_mfma_f32_16x16x32_bf16 v[80:83], v[252:255], v[188:191], v[80:83]
	s_waitcnt lgkmcnt(2)
	v_mfma_f32_16x16x32_bf16 v[72:75], v[244:247], v[192:195], v[72:75]
	ds_read_b128 v[236:239], v199 offset:17408
	buffer_load_dwordx4 v[0:3], v197, s[16:19], s43 offen
	s_waitcnt vmcnt(12)
	v_cvt_pk_bf16_f32 v11, v10, v11
	v_cvt_pk_bf16_f32 v10, v8, v9
	v_mfma_f32_16x16x32_bf16 v[64:67], v[216:219], v[192:195], v[64:67]
	ds_write_b64 v198, v[10:11] offset:61184
	v_mfma_f32_16x16x32_bf16 v[60:63], v[248:251], v[192:195], v[60:63]
	v_mfma_f32_16x16x32_bf16 v[76:79], v[252:255], v[192:195], v[76:79]
	s_waitcnt lgkmcnt(2)
	v_mfma_f32_16x16x32_bf16 v[68:71], v[244:247], v[208:211], v[68:71]
	v_mfma_f32_16x16x32_bf16 v[56:59], v[216:219], v[208:211], v[56:59]
	v_mfma_f32_16x16x32_bf16 v[52:55], v[248:251], v[208:211], v[52:55]
	v_mfma_f32_16x16x32_bf16 v[48:51], v[252:255], v[208:211], v[48:51]
	s_waitcnt lgkmcnt(1)
	buffer_load_dwordx4 v[8:11], v197, s[16:19], s45 offen
	s_waitcnt vmcnt(8)
	s_mov_b32 m0, s49
	s_waitcnt lgkmcnt(0)
	s_barrier
	ds_read_b64_tr_b16 v[178:179], v206 offset:34816
	ds_read_b64_tr_b16 v[176:177], v205 offset:34816
	ds_read_b64_tr_b16 v[180:181], v205 offset:34848
	ds_read_b64_tr_b16 v[184:185], v205 offset:34880
	ds_read_b64_tr_b16 v[188:189], v205 offset:34912
	ds_read_b128 v[192:195], v199 offset:36864
	ds_read_b64_tr_b16 v[182:183], v206 offset:34848
	ds_read_b64_tr_b16 v[186:187], v206 offset:34880
	ds_read_b64_tr_b16 v[190:191], v206 offset:34912
	ds_read_b128 v[208:211], v199 offset:38912
	ds_read_b128 v[212:215], v199 offset:40960
	buffer_load_dwordx4 v200, s[20:23], s36 offen lds
	s_mov_b32 m0, s68
	v_mfma_f32_16x16x32_bf16 v[44:47], v[244:247], v[236:239], v[44:47]
	v_mfma_f32_16x16x32_bf16 v[40:43], v[216:219], v[236:239], v[40:43]
	v_mfma_f32_16x16x32_bf16 v[36:39], v[248:251], v[236:239], v[36:39]
	v_mfma_f32_16x16x32_bf16 v[32:35], v[252:255], v[236:239], v[32:35]
	s_waitcnt lgkmcnt(5)
	v_mfma_f32_16x16x32_bf16 v[172:175], v[176:179], v[192:195], v[172:175]
	buffer_load_dwordx4 v201, s[20:23], s36 offen lds
	s_add_i32 s38, s9, 0xfffa0000
	s_waitcnt lgkmcnt(4)
	v_mfma_f32_16x16x32_bf16 v[168:171], v[180:183], v[192:195], v[168:171]
	s_waitcnt lgkmcnt(3)
	v_mfma_f32_16x16x32_bf16 v[164:167], v[184:187], v[192:195], v[164:167]
	s_waitcnt lgkmcnt(2)
	v_mfma_f32_16x16x32_bf16 v[160:163], v[188:191], v[192:195], v[160:163]
	s_waitcnt lgkmcnt(1)
	v_mfma_f32_16x16x32_bf16 v[156:159], v[176:179], v[208:211], v[156:159]
	s_mov_b32 m0, s77
	s_nop 0
	buffer_load_dwordx4 v202, s[20:23], s36 offen lds
	ds_read_b128 v[192:195], v199 offset:43008
	s_waitcnt vmcnt(10)
	v_cvt_pk_bf16_f32 v23, v22, v23
	v_cvt_pk_bf16_f32 v22, v20, v21
	v_mfma_f32_16x16x32_bf16 v[152:155], v[180:183], v[208:211], v[152:155]
	ds_write_b64 v198, v[22:23]
	v_mfma_f32_16x16x32_bf16 v[148:151], v[184:187], v[208:211], v[148:151]
	s_mov_b32 m0, s78
	s_nop 0
	buffer_load_dwordx4 v203, s[20:23], s36 offen lds
	v_mfma_f32_16x16x32_bf16 v[144:147], v[188:191], v[208:211], v[144:147]
	s_waitcnt lgkmcnt(2)
	v_mfma_f32_16x16x32_bf16 v[132:135], v[176:179], v[212:215], v[132:135]
	s_mov_b32 m0, s79
	s_nop 0
	buffer_load_dwordx4 v204, s[20:23], s36 offen lds
	ds_read_b128 v[208:211], v199 offset:45056
	v_mfma_f32_16x16x32_bf16 v[124:127], v[180:183], v[212:215], v[124:127]
	v_mfma_f32_16x16x32_bf16 v[120:123], v[184:187], v[212:215], v[120:123]
	v_mfma_f32_16x16x32_bf16 v[140:143], v[188:191], v[212:215], v[140:143]
	s_waitcnt lgkmcnt(2)
; #define G_DMA_A(kt, AO) do { G_DMA1(kt, AO, 0); G_DMA1(kt, AO, 1); G_DMA1(kt, AO, 2); G_DMA1(kt, AO, 3); if (MF == 9) G_DMA5(kt, AO); } while (0)
; #define G_ISSUE_B(kt) do { const unsigned _sb = (unsigned)(kt) * 4u * kstepB; \
;         _Pragma("unroll") for (int _i = 0; _i < 8; ++_i) sb[_i] = bload16(_i < 4 ? rsB0 : rsB1, vob, _sb + (_i & 3) * kstepB); } while (0)
; #define G_WRITE_B(BO) do { \
;         _Pragma("unroll") for (int _i = 0; _i < 8; ++_i) *(LAS u32x2*)(b_wr + (BO) + (_i & 3) * (16 * G_BSTRIDE) + (_i >> 2) * SLAB1) = pack4(__builtin_bit_cast(f32x4, sb[_i])); } while (0)
; #define G_ENDTILE(VM) do { asm volatile("s_waitcnt vmcnt(" #VM ")" ::: "memory"); \
;         asm volatile("s_waitcnt lgkmcnt(0)" ::: "memory"); __builtin_amdgcn_s_barrier(); asm volatile("" ::: "memory"); } while (0)
;     ...
;     __builtin_amdgcn_s_barrier();
;     G_DMA_A(0, G_A0); G_ISSUE_B(0); G_WRITE_B(G_B0);
;     __builtin_amdgcn_sched_barrier(0);
;     G_ISSUE_B(1);
;     __builtin_amdgcn_sched_barrier(0);
;     G_ENDTILE(8);
;     for (int ui = 0;; ++ui) {
; #pragma unroll
;         for (int m = 0; m < MF; ++m)
; #pragma unroll
;             for (int n = 0; n < 4; ++n) acc[m][n] = (f32x4){0.f, 0.f, 0.f, 0.f};
;         for (int t = 0; t < nt - 2; t += 2) {
;             G_TILE(G_A0, G_B0, true, G_B1, G_A1, t + 1, true, t + 2, (void)0);
;             G_ENDTILE(8);
;             G_TILE(G_A1, G_B1, true, G_B0, G_A0, t + 2, true, t + 3, (void)0);
;             G_ENDTILE(8);
;         }
	v_mfma_f32_16x16x32_bf16 v[136:139], v[176:179], v[192:195], v[136:139]
	ds_read_b128 v[212:215], v199 offset:47104
	buffer_load_dwordx4 v[20:23], v197, s[24:27], s38 offen
	s_waitcnt vmcnt(12)
	v_cvt_pk_bf16_f32 v31, v30, v31
	v_cvt_pk_bf16_f32 v30, v28, v29
	v_mfma_f32_16x16x32_bf16 v[128:131], v[180:183], v[192:195], v[128:131]
	ds_write_b64 v198, v[30:31] offset:8704
	v_mfma_f32_16x16x32_bf16 v[116:119], v[184:187], v[192:195], v[116:119]
	v_mfma_f32_16x16x32_bf16 v[112:115], v[188:191], v[192:195], v[112:115]
	s_add_i32 s39, s9, 0xfffc0000
	s_waitcnt lgkmcnt(2)
	v_mfma_f32_16x16x32_bf16 v[100:103], v[176:179], v[208:211], v[100:103]
	ds_read_b128 v[192:195], v199 offset:49152
	v_mfma_f32_16x16x32_bf16 v[92:95], v[180:183], v[208:211], v[92:95]
	v_mfma_f32_16x16x32_bf16 v[88:91], v[184:187], v[208:211], v[88:91]
	v_mfma_f32_16x16x32_bf16 v[108:111], v[188:191], v[208:211], v[108:111]
	s_waitcnt lgkmcnt(2)
	v_mfma_f32_16x16x32_bf16 v[104:107], v[176:179], v[212:215], v[104:107]
	ds_read_b128 v[208:211], v199 offset:51200
	buffer_load_dwordx4 v[28:31], v197, s[24:27], s39 offen
	s_waitcnt vmcnt(12)
	v_cvt_pk_bf16_f32 v19, v18, v19
	v_cvt_pk_bf16_f32 v18, v16, v17
	v_mfma_f32_16x16x32_bf16 v[96:99], v[180:183], v[212:215], v[96:99]
	ds_write_b64 v198, v[18:19] offset:17408
	v_mfma_f32_16x16x32_bf16 v[84:87], v[184:187], v[212:215], v[84:87]
	v_mfma_f32_16x16x32_bf16 v[80:83], v[188:191], v[212:215], v[80:83]
	s_add_i32 s43, s9, 0xfffe0000
	s_waitcnt lgkmcnt(2)
	v_mfma_f32_16x16x32_bf16 v[72:75], v[176:179], v[192:195], v[72:75]
	ds_read_b128 v[212:215], v199 offset:53248
	v_mfma_f32_16x16x32_bf16 v[64:67], v[180:183], v[192:195], v[64:67]
	v_mfma_f32_16x16x32_bf16 v[60:63], v[184:187], v[192:195], v[60:63]
	v_mfma_f32_16x16x32_bf16 v[76:79], v[188:191], v[192:195], v[76:79]
	s_waitcnt lgkmcnt(2)
	v_mfma_f32_16x16x32_bf16 v[68:71], v[176:179], v[208:211], v[68:71]
	ds_read_b128 v[192:195], v199 offset:37888
	buffer_load_dwordx4 v[16:19], v197, s[24:27], s43 offen
	s_waitcnt vmcnt(12)
	v_cvt_pk_bf16_f32 v27, v26, v27
	v_cvt_pk_bf16_f32 v26, v24, v25
	v_mfma_f32_16x16x32_bf16 v[56:59], v[180:183], v[208:211], v[56:59]
	ds_write_b64 v198, v[26:27] offset:26112
	v_mfma_f32_16x16x32_bf16 v[52:55], v[184:187], v[208:211], v[52:55]
	v_mfma_f32_16x16x32_bf16 v[48:51], v[188:191], v[208:211], v[48:51]
	s_waitcnt lgkmcnt(2)
	v_mfma_f32_16x16x32_bf16 v[44:47], v[176:179], v[212:215], v[44:47]
	ds_read_b128 v[176:179], v199 offset:39936
	v_mfma_f32_16x16x32_bf16 v[40:43], v[180:183], v[212:215], v[40:43]
	ds_read_b64_tr_b16 v[244:245], v205 offset:52224
	ds_read_b64_tr_b16 v[248:249], v205 offset:52256
	ds_read_b64_tr_b16 v[216:217], v205 offset:52288
	ds_read_b64_tr_b16 v[220:221], v205 offset:52320
	ds_read_b64_tr_b16 v[246:247], v206 offset:52224
	ds_read_b64_tr_b16 v[250:251], v206 offset:52256
	ds_read_b64_tr_b16 v[218:219], v206 offset:52288
	ds_read_b64_tr_b16 v[222:223], v206 offset:52320
	v_mfma_f32_16x16x32_bf16 v[36:39], v[184:187], v[212:215], v[36:39]
	v_mfma_f32_16x16x32_bf16 v[32:35], v[188:191], v[212:215], v[32:35]
	s_waitcnt lgkmcnt(3)
	v_mfma_f32_16x16x32_bf16 v[172:175], v[244:247], v[192:195], v[172:175]
	ds_read_b128 v[184:187], v199 offset:41984
	buffer_load_dwordx4 v[24:27], v197, s[24:27], s9 offen
	s_waitcnt vmcnt(12)
	v_cvt_pk_bf16_f32 v15, v14, v15
	v_cvt_pk_bf16_f32 v14, v12, v13
	s_waitcnt lgkmcnt(3)
	v_mfma_f32_16x16x32_bf16 v[168:171], v[248:251], v[192:195], v[168:171]
	ds_write_b64 v198, v[14:15] offset:256
	s_waitcnt lgkmcnt(3)
	v_mfma_f32_16x16x32_bf16 v[164:167], v[216:219], v[192:195], v[164:167]
	s_waitcnt lgkmcnt(2)
	v_mfma_f32_16x16x32_bf16 v[160:163], v[220:223], v[192:195], v[160:163]
	v_mfma_f32_16x16x32_bf16 v[156:159], v[244:247], v[176:179], v[156:159]
	ds_read_b128 v[188:191], v199 offset:44032
	v_mfma_f32_16x16x32_bf16 v[152:155], v[248:251], v[176:179], v[152:155]
	v_mfma_f32_16x16x32_bf16 v[148:151], v[216:219], v[176:179], v[148:151]
	v_mfma_f32_16x16x32_bf16 v[144:147], v[220:223], v[176:179], v[144:147]
	s_waitcnt lgkmcnt(2)
	v_mfma_f32_16x16x32_bf16 v[132:135], v[244:247], v[184:187], v[132:135]
	ds_read_b128 v[176:179], v199 offset:46080
	buffer_load_dwordx4 v[12:15], v197, s[16:19], s38 offen
	s_waitcnt vmcnt(12)
	v_cvt_pk_bf16_f32 v7, v6, v7
	v_cvt_pk_bf16_f32 v6, v4, v5
	v_mfma_f32_16x16x32_bf16 v[124:127], v[248:251], v[184:187], v[124:127]
	ds_write_b64 v198, v[6:7] offset:8960
	v_mfma_f32_16x16x32_bf16 v[120:123], v[216:219], v[184:187], v[120:123]
	v_mfma_f32_16x16x32_bf16 v[140:143], v[220:223], v[184:187], v[140:143]
	s_waitcnt lgkmcnt(2)
	v_mfma_f32_16x16x32_bf16 v[136:139], v[244:247], v[188:191], v[136:139]
	ds_read_b128 v[184:187], v199 offset:48128
	v_mfma_f32_16x16x32_bf16 v[128:131], v[248:251], v[188:191], v[128:131]
	v_mfma_f32_16x16x32_bf16 v[116:119], v[216:219], v[188:191], v[116:119]
	v_mfma_f32_16x16x32_bf16 v[112:115], v[220:223], v[188:191], v[112:115]
	s_waitcnt lgkmcnt(2)
	v_mfma_f32_16x16x32_bf16 v[100:103], v[244:247], v[176:179], v[100:103]
	ds_read_b128 v[188:191], v199 offset:50176
	buffer_load_dwordx4 v[4:7], v197, s[16:19], s39 offen
	s_waitcnt vmcnt(12)
	v_cvt_pk_bf16_f32 v3, v2, v3
	v_cvt_pk_bf16_f32 v2, v0, v1
	v_mfma_f32_16x16x32_bf16 v[92:95], v[248:251], v[176:179], v[92:95]
	ds_write_b64 v198, v[2:3] offset:17664
	v_mfma_f32_16x16x32_bf16 v[88:91], v[216:219], v[176:179], v[88:91]
	v_mfma_f32_16x16x32_bf16 v[108:111], v[220:223], v[176:179], v[108:111]
	s_waitcnt lgkmcnt(2)
	v_mfma_f32_16x16x32_bf16 v[104:107], v[244:247], v[184:187], v[104:107]
	ds_read_b128 v[176:179], v199 offset:52224
	v_mfma_f32_16x16x32_bf16 v[96:99], v[248:251], v[184:187], v[96:99]
	v_mfma_f32_16x16x32_bf16 v[84:87], v[216:219], v[184:187], v[84:87]
	v_mfma_f32_16x16x32_bf16 v[80:83], v[220:223], v[184:187], v[80:83]
	s_waitcnt lgkmcnt(2)
	v_mfma_f32_16x16x32_bf16 v[72:75], v[244:247], v[188:191], v[72:75]
	ds_read_b128 v[252:255], v199 offset:54272
	buffer_load_dwordx4 v[0:3], v197, s[16:19], s43 offen
	s_waitcnt vmcnt(12)
	v_cvt_pk_bf16_f32 v11, v10, v11
	v_cvt_pk_bf16_f32 v10, v8, v9
	v_mfma_f32_16x16x32_bf16 v[64:67], v[248:251], v[188:191], v[64:67]
	ds_write_b64 v198, v[10:11] offset:26368
	v_mfma_f32_16x16x32_bf16 v[60:63], v[216:219], v[188:191], v[60:63]
	v_mfma_f32_16x16x32_bf16 v[76:79], v[220:223], v[188:191], v[76:79]
	s_waitcnt lgkmcnt(2)
	v_mfma_f32_16x16x32_bf16 v[68:71], v[244:247], v[176:179], v[68:71]
	v_mfma_f32_16x16x32_bf16 v[56:59], v[248:251], v[176:179], v[56:59]
	v_mfma_f32_16x16x32_bf16 v[52:55], v[216:219], v[176:179], v[52:55]
	v_mfma_f32_16x16x32_bf16 v[48:51], v[220:223], v[176:179], v[48:51]
	s_waitcnt lgkmcnt(1)
	buffer_load_dwordx4 v[8:11], v197, s[16:19], s9 offen
	s_add_i32 s8, s8, 2
	s_add_i32 s9, s9, 0x100000
	s_addk_i32 s36, 0x100
	s_cmp_ge_i32 s8, s84
	s_waitcnt vmcnt(8)
	s_waitcnt lgkmcnt(0)
	s_barrier
	s_cbranch_scc1 .Lflush_P6
; #define G_DMA_A(kt, AO) do { G_DMA1(kt, AO, 0); G_DMA1(kt, AO, 1); G_DMA1(kt, AO, 2); G_DMA1(kt, AO, 3); if (MF == 9) G_DMA5(kt, AO); } while (0)
; #define G_ISSUE_B(kt) do { const unsigned _sb = (unsigned)(kt) * 4u * kstepB; \
;         _Pragma("unroll") for (int _i = 0; _i < 8; ++_i) sb[_i] = bload16(_i < 4 ? rsB0 : rsB1, vob, _sb + (_i & 3) * kstepB); } while (0)
; #define G_WRITE_B(BO) do { \
;         _Pragma("unroll") for (int _i = 0; _i < 8; ++_i) *(LAS u32x2*)(b_wr + (BO) + (_i & 3) * (16 * G_BSTRIDE) + (_i >> 2) * SLAB1) = pack4(__builtin_bit_cast(f32x4, sb[_i])); } while (0)
; #define G_ENDTILE(VM) do { asm volatile("s_waitcnt vmcnt(" #VM ")" ::: "memory"); \
;         asm volatile("s_waitcnt lgkmcnt(0)" ::: "memory"); __builtin_amdgcn_s_barrier(); asm volatile("" ::: "memory"); } while (0)
;     ...
;     __builtin_amdgcn_s_barrier();
;     G_DMA_A(0, G_A0); G_ISSUE_B(0); G_WRITE_B(G_B0);
;     __builtin_amdgcn_sched_barrier(0);
;     G_ISSUE_B(1);
;     __builtin_amdgcn_sched_barrier(0);
;     G_ENDTILE(8);
;     for (int ui = 0;; ++ui) {
; #pragma unroll
;         for (int m = 0; m < MF; ++m)
; #pragma unroll
;             for (int n = 0; n < 4; ++n) acc[m][n] = (f32x4){0.f, 0.f, 0.f, 0.f};
;         for (int t = 0; t < nt - 2; t += 2) {
;             G_TILE(G_A0, G_B0, true, G_B1, G_A1, t + 1, true, t + 2, (void)0);
.LBB0_863:
	s_mov_b32 m0, s85
	s_add_i32 s38, s36, 0xffffff80
	ds_read_b64_tr_b16 v[178:179], v206
	ds_read_b64_tr_b16 v[176:177], v205
	ds_read_b64_tr_b16 v[180:181], v205 offset:32
	ds_read_b64_tr_b16 v[184:185], v205 offset:64
	ds_read_b64_tr_b16 v[188:189], v205 offset:96
	ds_read_b128 v[192:195], v199
	ds_read_b64_tr_b16 v[182:183], v206 offset:32
	ds_read_b64_tr_b16 v[186:187], v206 offset:64
	ds_read_b64_tr_b16 v[190:191], v206 offset:96
	ds_read_b128 v[208:211], v199 offset:2048
	ds_read_b128 v[212:215], v199 offset:4096
	buffer_load_dwordx4 v200, s[20:23], s38 offen lds
	s_mov_b32 m0, s86
	v_mfma_f32_16x16x32_bf16 v[44:47], v[244:247], v[252:255], v[44:47]
	v_mfma_f32_16x16x32_bf16 v[40:43], v[248:251], v[252:255], v[40:43]
	v_mfma_f32_16x16x32_bf16 v[36:39], v[216:219], v[252:255], v[36:39]
	v_mfma_f32_16x16x32_bf16 v[32:35], v[220:223], v[252:255], v[32:35]
	s_waitcnt lgkmcnt(0)
	v_mfma_f32_16x16x32_bf16 v[172:175], v[176:179], v[192:195], v[172:175]
	buffer_load_dwordx4 v201, s[20:23], s38 offen lds
	v_mfma_f32_16x16x32_bf16 v[168:171], v[180:183], v[192:195], v[168:171]
	v_mfma_f32_16x16x32_bf16 v[164:167], v[184:187], v[192:195], v[164:167]
	v_mfma_f32_16x16x32_bf16 v[160:163], v[188:191], v[192:195], v[160:163]
	v_mfma_f32_16x16x32_bf16 v[156:159], v[176:179], v[208:211], v[156:159]
	s_mov_b32 m0, s87
	s_nop 0
	buffer_load_dwordx4 v202, s[20:23], s38 offen lds
	ds_read_b128 v[192:195], v199 offset:6144
	s_waitcnt vmcnt(10)
	v_cvt_pk_bf16_f32 v23, v22, v23
	v_cvt_pk_bf16_f32 v22, v20, v21
	v_mfma_f32_16x16x32_bf16 v[152:155], v[180:183], v[208:211], v[152:155]
	ds_write_b64 v198, v[22:23] offset:34816
	v_mfma_f32_16x16x32_bf16 v[148:151], v[184:187], v[208:211], v[148:151]
	s_mov_b32 m0, s88
	s_nop 0
	buffer_load_dwordx4 v203, s[20:23], s38 offen lds
	v_mfma_f32_16x16x32_bf16 v[144:147], v[188:191], v[208:211], v[144:147]
	v_mfma_f32_16x16x32_bf16 v[132:135], v[176:179], v[212:215], v[132:135]
	s_mov_b32 m0, s89
	s_nop 0
	buffer_load_dwordx4 v204, s[20:23], s38 offen lds
	s_add_i32 s38, s9, 0xfff20000
	ds_read_b128 v[208:211], v199 offset:8192
	v_mfma_f32_16x16x32_bf16 v[124:127], v[180:183], v[212:215], v[124:127]
	v_mfma_f32_16x16x32_bf16 v[120:123], v[184:187], v[212:215], v[120:123]
	v_mfma_f32_16x16x32_bf16 v[140:143], v[188:191], v[212:215], v[140:143]
	s_waitcnt lgkmcnt(2)
	v_mfma_f32_16x16x32_bf16 v[136:139], v[176:179], v[192:195], v[136:139]
	ds_read_b128 v[212:215], v199 offset:10240
	buffer_load_dwordx4 v[20:23], v197, s[24:27], s38 offen
	s_waitcnt vmcnt(11)
	v_cvt_pk_bf16_f32 v31, v30, v31
	v_cvt_pk_bf16_f32 v30, v28, v29
	v_mfma_f32_16x16x32_bf16 v[128:131], v[180:183], v[192:195], v[128:131]
	ds_write_b64 v198, v[30:31] offset:43520
	v_mfma_f32_16x16x32_bf16 v[116:119], v[184:187], v[192:195], v[116:119]
	v_mfma_f32_16x16x32_bf16 v[112:115], v[188:191], v[192:195], v[112:115]
	s_add_i32 s39, s9, 0xfff40000
	s_waitcnt lgkmcnt(2)
	v_mfma_f32_16x16x32_bf16 v[100:103], v[176:179], v[208:211], v[100:103]
	ds_read_b128 v[192:195], v199 offset:12288
	v_mfma_f32_16x16x32_bf16 v[92:95], v[180:183], v[208:211], v[92:95]
	v_mfma_f32_16x16x32_bf16 v[88:91], v[184:187], v[208:211], v[88:91]
	v_mfma_f32_16x16x32_bf16 v[108:111], v[188:191], v[208:211], v[108:111]
	s_waitcnt lgkmcnt(2)
	v_mfma_f32_16x16x32_bf16 v[104:107], v[176:179], v[212:215], v[104:107]
	ds_read_b128 v[208:211], v199 offset:14336
	v_cvt_pk_bf16_f32 v19, v18, v19
	v_cvt_pk_bf16_f32 v18, v16, v17
	v_mfma_f32_16x16x32_bf16 v[96:99], v[180:183], v[212:215], v[96:99]
	ds_write_b64 v198, v[18:19] offset:52224
	v_mfma_f32_16x16x32_bf16 v[84:87], v[184:187], v[212:215], v[84:87]
	v_mfma_f32_16x16x32_bf16 v[80:83], v[188:191], v[212:215], v[80:83]
	s_add_i32 s43, s9, 0xfff60000
	buffer_load_dwordx4 v[28:31], v197, s[24:27], s39 offen
	s_waitcnt lgkmcnt(2)
	v_mfma_f32_16x16x32_bf16 v[72:75], v[176:179], v[192:195], v[72:75]
	ds_read_b128 v[212:215], v199 offset:16384
	v_mfma_f32_16x16x32_bf16 v[64:67], v[180:183], v[192:195], v[64:67]
	v_mfma_f32_16x16x32_bf16 v[60:63], v[184:187], v[192:195], v[60:63]
	v_mfma_f32_16x16x32_bf16 v[76:79], v[188:191], v[192:195], v[76:79]
	s_waitcnt lgkmcnt(2)
	v_mfma_f32_16x16x32_bf16 v[68:71], v[176:179], v[208:211], v[68:71]
	ds_read_b128 v[192:195], v199 offset:1024
	buffer_load_dwordx4 v[16:19], v197, s[24:27], s43 offen
	s_waitcnt vmcnt(12)
	v_cvt_pk_bf16_f32 v27, v26, v27
	v_cvt_pk_bf16_f32 v26, v24, v25
	v_mfma_f32_16x16x32_bf16 v[56:59], v[180:183], v[208:211], v[56:59]
	ds_write_b64 v198, v[26:27] offset:60928
	v_mfma_f32_16x16x32_bf16 v[52:55], v[184:187], v[208:211], v[52:55]
	v_mfma_f32_16x16x32_bf16 v[48:51], v[188:191], v[208:211], v[48:51]
	s_add_i32 s45, s9, 0xfff80000
	ds_read_b128 v[208:211], v199 offset:3072
	s_waitcnt lgkmcnt(3)
	v_mfma_f32_16x16x32_bf16 v[44:47], v[176:179], v[212:215], v[44:47]
	ds_read_b64_tr_b16 v[246:247], v206 offset:17408
	ds_read_b64_tr_b16 v[218:219], v206 offset:17440
	ds_read_b64_tr_b16 v[244:245], v205 offset:17408
	ds_read_b64_tr_b16 v[216:217], v205 offset:17440
	v_mfma_f32_16x16x32_bf16 v[40:43], v[180:183], v[212:215], v[40:43]
	ds_read_b64_tr_b16 v[248:249], v205 offset:17472
	ds_read_b64_tr_b16 v[250:251], v206 offset:17472
	v_mfma_f32_16x16x32_bf16 v[36:39], v[184:187], v[212:215], v[36:39]
	ds_read_b64_tr_b16 v[252:253], v205 offset:17504
	ds_read_b64_tr_b16 v[254:255], v206 offset:17504
	v_mfma_f32_16x16x32_bf16 v[32:35], v[188:191], v[212:215], v[32:35]
	s_waitcnt lgkmcnt(5)
	v_mfma_f32_16x16x32_bf16 v[172:175], v[244:247], v[192:195], v[172:175]
	ds_read_b128 v[188:191], v199 offset:5120
	buffer_load_dwordx4 v[24:27], v197, s[24:27], s45 offen
	s_waitcnt vmcnt(12)
; #define G_DMA_A(kt, AO) do { G_DMA1(kt, AO, 0); G_DMA1(kt, AO, 1); G_DMA1(kt, AO, 2); G_DMA1(kt, AO, 3); if (MF == 9) G_DMA5(kt, AO); } while (0)
; #define G_ISSUE_B(kt) do { const unsigned _sb = (unsigned)(kt) * 4u * kstepB; \
;         _Pragma("unroll") for (int _i = 0; _i < 8; ++_i) sb[_i] = bload16(_i < 4 ? rsB0 : rsB1, vob, _sb + (_i & 3) * kstepB); } while (0)
; #define G_WRITE_B(BO) do { \
;         _Pragma("unroll") for (int _i = 0; _i < 8; ++_i) *(LAS u32x2*)(b_wr + (BO) + (_i & 3) * (16 * G_BSTRIDE) + (_i >> 2) * SLAB1) = pack4(__builtin_bit_cast(f32x4, sb[_i])); } while (0)
; #define G_ENDTILE(VM) do { asm volatile("s_waitcnt vmcnt(" #VM ")" ::: "memory"); \
;         asm volatile("s_waitcnt lgkmcnt(0)" ::: "memory"); __builtin_amdgcn_s_barrier(); asm volatile("" ::: "memory"); } while (0)
;     ...
;     __builtin_amdgcn_s_barrier();
;     G_DMA_A(0, G_A0); G_ISSUE_B(0); G_WRITE_B(G_B0);
;     __builtin_amdgcn_sched_barrier(0);
;     G_ISSUE_B(1);
;     __builtin_amdgcn_sched_barrier(0);
;     G_ENDTILE(8);
;     for (int ui = 0;; ++ui) {
; #pragma unroll
;         for (int m = 0; m < MF; ++m)
; #pragma unroll
;             for (int n = 0; n < 4; ++n) acc[m][n] = (f32x4){0.f, 0.f, 0.f, 0.f};
;         for (int t = 0; t < nt - 2; t += 2) {
;             G_TILE(G_A0, G_B0, true, G_B1, G_A1, t + 1, true, t + 2, (void)0);
;             G_ENDTILE(8);
;             G_TILE(G_A1, G_B1, true, G_B0, G_A0, t + 2, true, t + 3, (void)0);
;             G_ENDTILE(8);
	v_cvt_pk_bf16_f32 v15, v14, v15
	v_cvt_pk_bf16_f32 v14, v12, v13
	s_waitcnt lgkmcnt(5)
	v_mfma_f32_16x16x32_bf16 v[168:171], v[216:219], v[192:195], v[168:171]
	ds_write_b64 v198, v[14:15] offset:35072
	s_waitcnt lgkmcnt(4)
	v_mfma_f32_16x16x32_bf16 v[164:167], v[248:251], v[192:195], v[164:167]
	s_waitcnt lgkmcnt(2)
	v_mfma_f32_16x16x32_bf16 v[160:163], v[252:255], v[192:195], v[160:163]
	v_mfma_f32_16x16x32_bf16 v[156:159], v[244:247], v[208:211], v[156:159]
	ds_read_b128 v[192:195], v199 offset:7168
	v_mfma_f32_16x16x32_bf16 v[152:155], v[216:219], v[208:211], v[152:155]
	v_mfma_f32_16x16x32_bf16 v[148:151], v[248:251], v[208:211], v[148:151]
	v_mfma_f32_16x16x32_bf16 v[144:147], v[252:255], v[208:211], v[144:147]
	s_waitcnt lgkmcnt(2)
	v_mfma_f32_16x16x32_bf16 v[132:135], v[244:247], v[188:191], v[132:135]
	ds_read_b128 v[208:211], v199 offset:9216
	buffer_load_dwordx4 v[12:15], v197, s[16:19], s38 offen
	s_waitcnt vmcnt(11)
	v_cvt_pk_bf16_f32 v7, v6, v7
	v_cvt_pk_bf16_f32 v6, v4, v5
	v_mfma_f32_16x16x32_bf16 v[124:127], v[216:219], v[188:191], v[124:127]
	ds_write_b64 v198, v[6:7] offset:43776
	v_mfma_f32_16x16x32_bf16 v[120:123], v[248:251], v[188:191], v[120:123]
	v_mfma_f32_16x16x32_bf16 v[140:143], v[252:255], v[188:191], v[140:143]
	s_waitcnt lgkmcnt(2)
	v_mfma_f32_16x16x32_bf16 v[136:139], v[244:247], v[192:195], v[136:139]
	ds_read_b128 v[188:191], v199 offset:11264
	v_mfma_f32_16x16x32_bf16 v[128:131], v[216:219], v[192:195], v[128:131]
	v_mfma_f32_16x16x32_bf16 v[116:119], v[248:251], v[192:195], v[116:119]
	v_mfma_f32_16x16x32_bf16 v[112:115], v[252:255], v[192:195], v[112:115]
	s_waitcnt lgkmcnt(2)
	v_mfma_f32_16x16x32_bf16 v[100:103], v[244:247], v[208:211], v[100:103]
	ds_read_b128 v[192:195], v199 offset:13312
	v_cvt_pk_bf16_f32 v3, v2, v3
	v_cvt_pk_bf16_f32 v2, v0, v1
	v_mfma_f32_16x16x32_bf16 v[92:95], v[216:219], v[208:211], v[92:95]
	ds_write_b64 v198, v[2:3] offset:52480
	v_mfma_f32_16x16x32_bf16 v[88:91], v[248:251], v[208:211], v[88:91]
	v_mfma_f32_16x16x32_bf16 v[108:111], v[252:255], v[208:211], v[108:111]
	buffer_load_dwordx4 v[4:7], v197, s[16:19], s39 offen
	s_waitcnt lgkmcnt(2)
	v_mfma_f32_16x16x32_bf16 v[104:107], v[244:247], v[188:191], v[104:107]
	ds_read_b128 v[208:211], v199 offset:15360
	v_mfma_f32_16x16x32_bf16 v[96:99], v[216:219], v[188:191], v[96:99]
	v_mfma_f32_16x16x32_bf16 v[84:87], v[248:251], v[188:191], v[84:87]
	v_mfma_f32_16x16x32_bf16 v[80:83], v[252:255], v[188:191], v[80:83]
	s_waitcnt lgkmcnt(2)
	v_mfma_f32_16x16x32_bf16 v[72:75], v[244:247], v[192:195], v[72:75]
	ds_read_b128 v[236:239], v199 offset:17408
	buffer_load_dwordx4 v[0:3], v197, s[16:19], s43 offen
	s_waitcnt vmcnt(12)
	v_cvt_pk_bf16_f32 v11, v10, v11
	v_cvt_pk_bf16_f32 v10, v8, v9
	v_mfma_f32_16x16x32_bf16 v[64:67], v[216:219], v[192:195], v[64:67]
	ds_write_b64 v198, v[10:11] offset:61184
	v_mfma_f32_16x16x32_bf16 v[60:63], v[248:251], v[192:195], v[60:63]
	v_mfma_f32_16x16x32_bf16 v[76:79], v[252:255], v[192:195], v[76:79]
	s_waitcnt lgkmcnt(2)
	v_mfma_f32_16x16x32_bf16 v[68:71], v[244:247], v[208:211], v[68:71]
	v_mfma_f32_16x16x32_bf16 v[56:59], v[216:219], v[208:211], v[56:59]
	v_mfma_f32_16x16x32_bf16 v[52:55], v[248:251], v[208:211], v[52:55]
	v_mfma_f32_16x16x32_bf16 v[48:51], v[252:255], v[208:211], v[48:51]
	s_waitcnt lgkmcnt(1)
	buffer_load_dwordx4 v[8:11], v197, s[16:19], s45 offen
	s_waitcnt vmcnt(8)
	s_mov_b32 m0, s49
	s_waitcnt lgkmcnt(0)
	s_barrier
	ds_read_b64_tr_b16 v[178:179], v206 offset:34816
	ds_read_b64_tr_b16 v[176:177], v205 offset:34816
	ds_read_b64_tr_b16 v[180:181], v205 offset:34848
	ds_read_b64_tr_b16 v[184:185], v205 offset:34880
	ds_read_b64_tr_b16 v[188:189], v205 offset:34912
	ds_read_b128 v[192:195], v199 offset:36864
	ds_read_b64_tr_b16 v[182:183], v206 offset:34848
	ds_read_b64_tr_b16 v[186:187], v206 offset:34880
	ds_read_b64_tr_b16 v[190:191], v206 offset:34912
	ds_read_b128 v[208:211], v199 offset:38912
	ds_read_b128 v[212:215], v199 offset:40960
	buffer_load_dwordx4 v200, s[20:23], s36 offen lds
	s_mov_b32 m0, s68
	v_mfma_f32_16x16x32_bf16 v[44:47], v[244:247], v[236:239], v[44:47]
	v_mfma_f32_16x16x32_bf16 v[40:43], v[216:219], v[236:239], v[40:43]
	v_mfma_f32_16x16x32_bf16 v[36:39], v[248:251], v[236:239], v[36:39]
	v_mfma_f32_16x16x32_bf16 v[32:35], v[252:255], v[236:239], v[32:35]
	s_waitcnt lgkmcnt(5)
	v_mfma_f32_16x16x32_bf16 v[172:175], v[176:179], v[192:195], v[172:175]
	buffer_load_dwordx4 v201, s[20:23], s36 offen lds
	s_add_i32 s38, s9, 0xfffa0000
	s_waitcnt lgkmcnt(4)
	v_mfma_f32_16x16x32_bf16 v[168:171], v[180:183], v[192:195], v[168:171]
	s_waitcnt lgkmcnt(3)
	v_mfma_f32_16x16x32_bf16 v[164:167], v[184:187], v[192:195], v[164:167]
	s_waitcnt lgkmcnt(2)
	v_mfma_f32_16x16x32_bf16 v[160:163], v[188:191], v[192:195], v[160:163]
	s_waitcnt lgkmcnt(1)
	v_mfma_f32_16x16x32_bf16 v[156:159], v[176:179], v[208:211], v[156:159]
	s_mov_b32 m0, s77
	s_nop 0
	buffer_load_dwordx4 v202, s[20:23], s36 offen lds
	ds_read_b128 v[192:195], v199 offset:43008
	s_waitcnt vmcnt(10)
	v_cvt_pk_bf16_f32 v23, v22, v23
	v_cvt_pk_bf16_f32 v22, v20, v21
	v_mfma_f32_16x16x32_bf16 v[152:155], v[180:183], v[208:211], v[152:155]
	ds_write_b64 v198, v[22:23]
	v_mfma_f32_16x16x32_bf16 v[148:151], v[184:187], v[208:211], v[148:151]
	s_mov_b32 m0, s78
	s_nop 0
	buffer_load_dwordx4 v203, s[20:23], s36 offen lds
	v_mfma_f32_16x16x32_bf16 v[144:147], v[188:191], v[208:211], v[144:147]
	s_waitcnt lgkmcnt(2)
; #define G_DMA_A(kt, AO) do { G_DMA1(kt, AO, 0); G_DMA1(kt, AO, 1); G_DMA1(kt, AO, 2); G_DMA1(kt, AO, 3); if (MF == 9) G_DMA5(kt, AO); } while (0)
; #define G_ISSUE_B(kt) do { const unsigned _sb = (unsigned)(kt) * 4u * kstepB; \
;         _Pragma("unroll") for (int _i = 0; _i < 8; ++_i) sb[_i] = bload16(_i < 4 ? rsB0 : rsB1, vob, _sb + (_i & 3) * kstepB); } while (0)
; #define G_WRITE_B(BO) do { \
;         _Pragma("unroll") for (int _i = 0; _i < 8; ++_i) *(LAS u32x2*)(b_wr + (BO) + (_i & 3) * (16 * G_BSTRIDE) + (_i >> 2) * SLAB1) = pack4(__builtin_bit_cast(f32x4, sb[_i])); } while (0)
; #define G_ENDTILE(VM) do { asm volatile("s_waitcnt vmcnt(" #VM ")" ::: "memory"); \
;         asm volatile("s_waitcnt lgkmcnt(0)" ::: "memory"); __builtin_amdgcn_s_barrier(); asm volatile("" ::: "memory"); } while (0)
;     ...
;     __builtin_amdgcn_s_barrier();
;     G_DMA_A(0, G_A0); G_ISSUE_B(0); G_WRITE_B(G_B0);
;     __builtin_amdgcn_sched_barrier(0);
;     G_ISSUE_B(1);
;     __builtin_amdgcn_sched_barrier(0);
;     G_ENDTILE(8);
;     for (int ui = 0;; ++ui) {
; #pragma unroll
;         for (int m = 0; m < MF; ++m)
; #pragma unroll
;             for (int n = 0; n < 4; ++n) acc[m][n] = (f32x4){0.f, 0.f, 0.f, 0.f};
;         for (int t = 0; t < nt - 2; t += 2) {
;             G_TILE(G_A0, G_B0, true, G_B1, G_A1, t + 1, true, t + 2, (void)0);
	v_mfma_f32_16x16x32_bf16 v[132:135], v[176:179], v[212:215], v[132:135]
	s_mov_b32 m0, s79
	s_nop 0
	buffer_load_dwordx4 v204, s[20:23], s36 offen lds
	ds_read_b128 v[208:211], v199 offset:45056
	v_mfma_f32_16x16x32_bf16 v[124:127], v[180:183], v[212:215], v[124:127]
	v_mfma_f32_16x16x32_bf16 v[120:123], v[184:187], v[212:215], v[120:123]
	v_mfma_f32_16x16x32_bf16 v[140:143], v[188:191], v[212:215], v[140:143]
	s_waitcnt lgkmcnt(2)
	v_mfma_f32_16x16x32_bf16 v[136:139], v[176:179], v[192:195], v[136:139]
	ds_read_b128 v[212:215], v199 offset:47104
	buffer_load_dwordx4 v[20:23], v197, s[24:27], s38 offen
	s_waitcnt vmcnt(12)
	v_cvt_pk_bf16_f32 v31, v30, v31
	v_cvt_pk_bf16_f32 v30, v28, v29
	v_mfma_f32_16x16x32_bf16 v[128:131], v[180:183], v[192:195], v[128:131]
	ds_write_b64 v198, v[30:31] offset:8704
	v_mfma_f32_16x16x32_bf16 v[116:119], v[184:187], v[192:195], v[116:119]
	v_mfma_f32_16x16x32_bf16 v[112:115], v[188:191], v[192:195], v[112:115]
	s_add_i32 s39, s9, 0xfffc0000
	s_waitcnt lgkmcnt(2)
	v_mfma_f32_16x16x32_bf16 v[100:103], v[176:179], v[208:211], v[100:103]
	ds_read_b128 v[192:195], v199 offset:49152
	v_mfma_f32_16x16x32_bf16 v[92:95], v[180:183], v[208:211], v[92:95]
	v_mfma_f32_16x16x32_bf16 v[88:91], v[184:187], v[208:211], v[88:91]
	v_mfma_f32_16x16x32_bf16 v[108:111], v[188:191], v[208:211], v[108:111]
	s_waitcnt lgkmcnt(2)
	v_mfma_f32_16x16x32_bf16 v[104:107], v[176:179], v[212:215], v[104:107]
	ds_read_b128 v[208:211], v199 offset:51200
	buffer_load_dwordx4 v[28:31], v197, s[24:27], s39 offen
	s_waitcnt vmcnt(12)
	v_cvt_pk_bf16_f32 v19, v18, v19
	v_cvt_pk_bf16_f32 v18, v16, v17
	v_mfma_f32_16x16x32_bf16 v[96:99], v[180:183], v[212:215], v[96:99]
	ds_write_b64 v198, v[18:19] offset:17408
	v_mfma_f32_16x16x32_bf16 v[84:87], v[184:187], v[212:215], v[84:87]
	v_mfma_f32_16x16x32_bf16 v[80:83], v[188:191], v[212:215], v[80:83]
	s_add_i32 s43, s9, 0xfffe0000
	s_waitcnt lgkmcnt(2)
	v_mfma_f32_16x16x32_bf16 v[72:75], v[176:179], v[192:195], v[72:75]
	ds_read_b128 v[212:215], v199 offset:53248
	v_mfma_f32_16x16x32_bf16 v[64:67], v[180:183], v[192:195], v[64:67]
	v_mfma_f32_16x16x32_bf16 v[60:63], v[184:187], v[192:195], v[60:63]
	v_mfma_f32_16x16x32_bf16 v[76:79], v[188:191], v[192:195], v[76:79]
	s_waitcnt lgkmcnt(2)
	v_mfma_f32_16x16x32_bf16 v[68:71], v[176:179], v[208:211], v[68:71]
	ds_read_b128 v[192:195], v199 offset:37888
	buffer_load_dwordx4 v[16:19], v197, s[24:27], s43 offen
	s_waitcnt vmcnt(12)
	v_cvt_pk_bf16_f32 v27, v26, v27
	v_cvt_pk_bf16_f32 v26, v24, v25
	v_mfma_f32_16x16x32_bf16 v[56:59], v[180:183], v[208:211], v[56:59]
	ds_write_b64 v198, v[26:27] offset:26112
	v_mfma_f32_16x16x32_bf16 v[52:55], v[184:187], v[208:211], v[52:55]
	v_mfma_f32_16x16x32_bf16 v[48:51], v[188:191], v[208:211], v[48:51]
	s_waitcnt lgkmcnt(2)
	v_mfma_f32_16x16x32_bf16 v[44:47], v[176:179], v[212:215], v[44:47]
	ds_read_b128 v[176:179], v199 offset:39936
	v_mfma_f32_16x16x32_bf16 v[40:43], v[180:183], v[212:215], v[40:43]
	ds_read_b64_tr_b16 v[244:245], v205 offset:52224
	ds_read_b64_tr_b16 v[248:249], v205 offset:52256
	ds_read_b64_tr_b16 v[216:217], v205 offset:52288
	ds_read_b64_tr_b16 v[220:221], v205 offset:52320
	ds_read_b64_tr_b16 v[246:247], v206 offset:52224
	ds_read_b64_tr_b16 v[250:251], v206 offset:52256
	ds_read_b64_tr_b16 v[218:219], v206 offset:52288
	ds_read_b64_tr_b16 v[222:223], v206 offset:52320
	v_mfma_f32_16x16x32_bf16 v[36:39], v[184:187], v[212:215], v[36:39]
	v_mfma_f32_16x16x32_bf16 v[32:35], v[188:191], v[212:215], v[32:35]
	s_waitcnt lgkmcnt(3)
	v_mfma_f32_16x16x32_bf16 v[172:175], v[244:247], v[192:195], v[172:175]
	ds_read_b128 v[184:187], v199 offset:41984
	buffer_load_dwordx4 v[24:27], v197, s[24:27], s9 offen
	s_waitcnt vmcnt(12)
; #define G_DMA_A(kt, AO) do { G_DMA1(kt, AO, 0); G_DMA1(kt, AO, 1); G_DMA1(kt, AO, 2); G_DMA1(kt, AO, 3); if (MF == 9) G_DMA5(kt, AO); } while (0)
; #define G_ISSUE_B(kt) do { const unsigned _sb = (unsigned)(kt) * 4u * kstepB; \
;         _Pragma("unroll") for (int _i = 0; _i < 8; ++_i) sb[_i] = bload16(_i < 4 ? rsB0 : rsB1, vob, _sb + (_i & 3) * kstepB); } while (0)
; #define G_WRITE_B(BO) do { \
;         _Pragma("unroll") for (int _i = 0; _i < 8; ++_i) *(LAS u32x2*)(b_wr + (BO) + (_i & 3) * (16 * G_BSTRIDE) + (_i >> 2) * SLAB1) = pack4(__builtin_bit_cast(f32x4, sb[_i])); } while (0)
; #define G_ENDTILE(VM) do { asm volatile("s_waitcnt vmcnt(" #VM ")" ::: "memory"); \
;         asm volatile("s_waitcnt lgkmcnt(0)" ::: "memory"); __builtin_amdgcn_s_barrier(); asm volatile("" ::: "memory"); } while (0)
;     ...
;     __builtin_amdgcn_s_barrier();
;     G_DMA_A(0, G_A0); G_ISSUE_B(0); G_WRITE_B(G_B0);
;     __builtin_amdgcn_sched_barrier(0);
;     G_ISSUE_B(1);
;     __builtin_amdgcn_sched_barrier(0);
;     G_ENDTILE(8);
;     for (int ui = 0;; ++ui) {
; #pragma unroll
;         for (int m = 0; m < MF; ++m)
; #pragma unroll
;             for (int n = 0; n < 4; ++n) acc[m][n] = (f32x4){0.f, 0.f, 0.f, 0.f};
;         for (int t = 0; t < nt - 2; t += 2) {
;             G_TILE(G_A0, G_B0, true, G_B1, G_A1, t + 1, true, t + 2, (void)0);
;             G_ENDTILE(8);
;             G_TILE(G_A1, G_B1, true, G_B0, G_A0, t + 2, true, t + 3, (void)0);
;             G_ENDTILE(8);
;         }
	v_cvt_pk_bf16_f32 v15, v14, v15
	v_cvt_pk_bf16_f32 v14, v12, v13
	s_waitcnt lgkmcnt(3)
	v_mfma_f32_16x16x32_bf16 v[168:171], v[248:251], v[192:195], v[168:171]
	ds_write_b64 v198, v[14:15] offset:256
	s_waitcnt lgkmcnt(3)
	v_mfma_f32_16x16x32_bf16 v[164:167], v[216:219], v[192:195], v[164:167]
	s_waitcnt lgkmcnt(2)
	v_mfma_f32_16x16x32_bf16 v[160:163], v[220:223], v[192:195], v[160:163]
	v_mfma_f32_16x16x32_bf16 v[156:159], v[244:247], v[176:179], v[156:159]
	ds_read_b128 v[188:191], v199 offset:44032
	v_mfma_f32_16x16x32_bf16 v[152:155], v[248:251], v[176:179], v[152:155]
	v_mfma_f32_16x16x32_bf16 v[148:151], v[216:219], v[176:179], v[148:151]
	v_mfma_f32_16x16x32_bf16 v[144:147], v[220:223], v[176:179], v[144:147]
	s_waitcnt lgkmcnt(2)
	v_mfma_f32_16x16x32_bf16 v[132:135], v[244:247], v[184:187], v[132:135]
	ds_read_b128 v[176:179], v199 offset:46080
	buffer_load_dwordx4 v[12:15], v197, s[16:19], s38 offen
	s_waitcnt vmcnt(12)
	v_cvt_pk_bf16_f32 v7, v6, v7
	v_cvt_pk_bf16_f32 v6, v4, v5
	v_mfma_f32_16x16x32_bf16 v[124:127], v[248:251], v[184:187], v[124:127]
	ds_write_b64 v198, v[6:7] offset:8960
	v_mfma_f32_16x16x32_bf16 v[120:123], v[216:219], v[184:187], v[120:123]
	v_mfma_f32_16x16x32_bf16 v[140:143], v[220:223], v[184:187], v[140:143]
	s_waitcnt lgkmcnt(2)
	v_mfma_f32_16x16x32_bf16 v[136:139], v[244:247], v[188:191], v[136:139]
	ds_read_b128 v[184:187], v199 offset:48128
	v_mfma_f32_16x16x32_bf16 v[128:131], v[248:251], v[188:191], v[128:131]
	v_mfma_f32_16x16x32_bf16 v[116:119], v[216:219], v[188:191], v[116:119]
	v_mfma_f32_16x16x32_bf16 v[112:115], v[220:223], v[188:191], v[112:115]
	s_waitcnt lgkmcnt(2)
	v_mfma_f32_16x16x32_bf16 v[100:103], v[244:247], v[176:179], v[100:103]
	ds_read_b128 v[188:191], v199 offset:50176
	buffer_load_dwordx4 v[4:7], v197, s[16:19], s39 offen
	s_waitcnt vmcnt(12)
	v_cvt_pk_bf16_f32 v3, v2, v3
	v_cvt_pk_bf16_f32 v2, v0, v1
	v_mfma_f32_16x16x32_bf16 v[92:95], v[248:251], v[176:179], v[92:95]
	ds_write_b64 v198, v[2:3] offset:17664
	v_mfma_f32_16x16x32_bf16 v[88:91], v[216:219], v[176:179], v[88:91]
	v_mfma_f32_16x16x32_bf16 v[108:111], v[220:223], v[176:179], v[108:111]
	s_waitcnt lgkmcnt(2)
	v_mfma_f32_16x16x32_bf16 v[104:107], v[244:247], v[184:187], v[104:107]
	ds_read_b128 v[176:179], v199 offset:52224
	v_mfma_f32_16x16x32_bf16 v[96:99], v[248:251], v[184:187], v[96:99]
	v_mfma_f32_16x16x32_bf16 v[84:87], v[216:219], v[184:187], v[84:87]
	v_mfma_f32_16x16x32_bf16 v[80:83], v[220:223], v[184:187], v[80:83]
	s_waitcnt lgkmcnt(2)
	v_mfma_f32_16x16x32_bf16 v[72:75], v[244:247], v[188:191], v[72:75]
	ds_read_b128 v[252:255], v199 offset:54272
	buffer_load_dwordx4 v[0:3], v197, s[16:19], s43 offen
	s_waitcnt vmcnt(12)
	v_cvt_pk_bf16_f32 v11, v10, v11
	v_cvt_pk_bf16_f32 v10, v8, v9
	v_mfma_f32_16x16x32_bf16 v[64:67], v[248:251], v[188:191], v[64:67]
	ds_write_b64 v198, v[10:11] offset:26368
	v_mfma_f32_16x16x32_bf16 v[60:63], v[216:219], v[188:191], v[60:63]
	v_mfma_f32_16x16x32_bf16 v[76:79], v[220:223], v[188:191], v[76:79]
	s_waitcnt lgkmcnt(2)
	v_mfma_f32_16x16x32_bf16 v[68:71], v[244:247], v[176:179], v[68:71]
	v_mfma_f32_16x16x32_bf16 v[56:59], v[248:251], v[176:179], v[56:59]
	v_mfma_f32_16x16x32_bf16 v[52:55], v[216:219], v[176:179], v[52:55]
	v_mfma_f32_16x16x32_bf16 v[48:51], v[220:223], v[176:179], v[48:51]
	s_waitcnt lgkmcnt(1)
	buffer_load_dwordx4 v[8:11], v197, s[16:19], s9 offen
	s_add_i32 s8, s8, 2
	s_add_i32 s9, s9, 0x100000
	s_addk_i32 s36, 0x100
	s_cmp_ge_i32 s8, s84
	s_waitcnt vmcnt(8)
	s_waitcnt lgkmcnt(0)
	s_barrier
	s_cbranch_scc0 .LBB0_863

; #define G_DMA_A(kt, AO) do { G_DMA1(kt, AO, 0); G_DMA1(kt, AO, 1); G_DMA1(kt, AO, 2); G_DMA1(kt, AO, 3); if (MF == 9) G_DMA5(kt, AO); } while (0)
; #define G_ISSUE_B(kt) do { const unsigned _sb = (unsigned)(kt) * 4u * kstepB; \
;         _Pragma("unroll") for (int _i = 0; _i < 8; ++_i) sb[_i] = bload16(_i < 4 ? rsB0 : rsB1, vob, _sb + (_i & 3) * kstepB); } while (0)
; #define G_WRITE_B(BO) do { \
;         _Pragma("unroll") for (int _i = 0; _i < 8; ++_i) *(LAS u32x2*)(b_wr + (BO) + (_i & 3) * (16 * G_BSTRIDE) + (_i >> 2) * SLAB1) = pack4(__builtin_bit_cast(f32x4, sb[_i])); } while (0)
; #define G_ENDTILE(VM) do { asm volatile("s_waitcnt vmcnt(" #VM ")" ::: "memory"); \
;         asm volatile("s_waitcnt lgkmcnt(0)" ::: "memory"); __builtin_amdgcn_s_barrier(); asm volatile("" ::: "memory"); } while (0)
;     ...
;     __builtin_amdgcn_s_barrier();
;     G_DMA_A(0, G_A0); G_ISSUE_B(0); G_WRITE_B(G_B0);
;     __builtin_amdgcn_sched_barrier(0);
;     G_ISSUE_B(1);
;     __builtin_amdgcn_sched_barrier(0);
;     G_ENDTILE(8);
;     for (int ui = 0;; ++ui) {
; #pragma unroll
;         for (int m = 0; m < MF; ++m)
; #pragma unroll
;             for (int n = 0; n < 4; ++n) acc[m][n] = (f32x4){0.f, 0.f, 0.f, 0.f};
;         for (int t = 0; t < nt - 2; t += 2) {
;             G_TILE(G_A0, G_B0, true, G_B1, G_A1, t + 1, true, t + 2, (void)0);
;             G_ENDTILE(8);
;             G_TILE(G_A1, G_B1, true, G_B0, G_A0, t + 2, true, t + 3, (void)0);
;             G_ENDTILE(8);
;         }
.Lchk6_s36:
	s_waitcnt lgkmcnt(1)
	buffer_load_dwordx4 v[8:11], v197, s[16:19], s9 offen
	s_add_i32 s8, s8, 2
	s_add_i32 s9, s9, 0x100000
	s_addk_i32 s36, 0x100
	s_cmp_ge_i32 s8, s84
	s_waitcnt vmcnt(8)
	s_waitcnt lgkmcnt(0)
	s_barrier
	s_cbranch_scc0 .Lchk6_loop
	s_cmp_le_u32 s99, 8
	s_cbranch_scc1 .Lchk6_s37
	v_mfma_f32_16x16x32_bf16 v[44:47], v[244:247], v[252:255], v[44:47]
	v_mfma_f32_16x16x32_bf16 v[40:43], v[248:251], v[252:255], v[40:43]
	v_mfma_f32_16x16x32_bf16 v[36:39], v[216:219], v[252:255], v[36:39]
	v_mfma_f32_16x16x32_bf16 v[32:35], v[220:223], v[252:255], v[32:35]

; #define G_DMA_A(kt, AO) do { G_DMA1(kt, AO, 0); G_DMA1(kt, AO, 1); G_DMA1(kt, AO, 2); G_DMA1(kt, AO, 3); if (MF == 9) G_DMA5(kt, AO); } while (0)
; #define G_ISSUE_B(kt) do { const unsigned _sb = (unsigned)(kt) * 4u * kstepB; \
;         _Pragma("unroll") for (int _i = 0; _i < 8; ++_i) sb[_i] = bload16(_i < 4 ? rsB0 : rsB1, vob, _sb + (_i & 3) * kstepB); } while (0)
; #define G_WRITE_B(BO) do { \
;         _Pragma("unroll") for (int _i = 0; _i < 8; ++_i) *(LAS u32x2*)(b_wr + (BO) + (_i & 3) * (16 * G_BSTRIDE) + (_i >> 2) * SLAB1) = pack4(__builtin_bit_cast(f32x4, sb[_i])); } while (0)
; #define G_ENDTILE(VM) do { asm volatile("s_waitcnt vmcnt(" #VM ")" ::: "memory"); \
;         asm volatile("s_waitcnt lgkmcnt(0)" ::: "memory"); __builtin_amdgcn_s_barrier(); asm volatile("" ::: "memory"); } while (0)
;     ...
;     __builtin_amdgcn_s_barrier();
;     G_DMA_A(0, G_A0); G_ISSUE_B(0); G_WRITE_B(G_B0);
;     __builtin_amdgcn_sched_barrier(0);
;     G_ISSUE_B(1);
;     __builtin_amdgcn_sched_barrier(0);
;     G_ENDTILE(8);
;     for (int ui = 0;; ++ui) {
; #pragma unroll
;         for (int m = 0; m < MF; ++m)
; #pragma unroll
;             for (int n = 0; n < 4; ++n) acc[m][n] = (f32x4){0.f, 0.f, 0.f, 0.f};
;         for (int t = 0; t < nt - 2; t += 2) {
;             G_TILE(G_A0, G_B0, true, G_B1, G_A1, t + 1, true, t + 2, (void)0);
.LBB0_897:
	s_andn2_b64 vcc, exec, s[28:29]
	v_mov_b32_e32 v159, 0
	s_cbranch_vccnz .LBB0_900
	s_mov_b32 s12, 0
	s_mov_b32 s13, 0x1e0000
	s_movk_i32 s45, 0x100
	s_waitcnt lgkmcnt(0)
	s_mov_b32 m0, s64
	s_add_i32 s69, s45, 0xffffff80
	ds_read_b64_tr_b16 v[170:171], v166
	ds_read_b64_tr_b16 v[172:173], v167
	ds_read_b64_tr_b16 v[176:177], v167 offset:32
	ds_read_b128 v[178:181], v162
	ds_read_b64_tr_b16 v[174:175], v166 offset:32
	ds_read_b64_tr_b16 v[182:183], v166 offset:64
	ds_read_b64_tr_b16 v[186:187], v166 offset:96
	ds_read_b64_tr_b16 v[184:185], v167 offset:64
	ds_read_b64_tr_b16 v[188:189], v167 offset:96
	ds_read_b128 v[190:193], v162 offset:2048
	ds_read_b128 v[198:201], v162 offset:4096
	buffer_load_dwordx4 v163, s[20:23], s69 offen lds
	s_mov_b32 m0, s63
	s_waitcnt lgkmcnt(7)
	v_mfma_f32_16x16x32_bf16 v[156:159], v[170:173], v[178:181], 0
	buffer_load_dwordx4 v165, s[20:23], s69 offen lds
	s_waitcnt lgkmcnt(6)
	v_mfma_f32_16x16x32_bf16 v[152:155], v[174:177], v[178:181], 0
	s_waitcnt lgkmcnt(3)
	v_mfma_f32_16x16x32_bf16 v[148:151], v[182:185], v[178:181], 0
	s_waitcnt lgkmcnt(2)
	v_mfma_f32_16x16x32_bf16 v[144:147], v[186:189], v[178:181], 0
	s_waitcnt lgkmcnt(1)
	v_mfma_f32_16x16x32_bf16 v[140:143], v[170:173], v[190:193], 0
	s_mov_b32 m0, s62
	s_nop 0
	buffer_load_dwordx4 v164, s[20:23], s69 offen lds
	ds_read_b128 v[178:181], v162 offset:6144
	s_waitcnt vmcnt(10)
	v_cvt_pk_bf16_f32 v15, v14, v15
	v_cvt_pk_bf16_f32 v14, v12, v13
	v_mfma_f32_16x16x32_bf16 v[136:139], v[174:177], v[190:193], 0
	ds_write_b64 v161, v[14:15] offset:34816
	v_mfma_f32_16x16x32_bf16 v[132:135], v[182:185], v[190:193], 0
	s_mov_b32 m0, s31
	s_nop 0
	buffer_load_dwordx4 v168, s[20:23], s69 offen lds
	s_add_i32 s69, s13, 0xfff20000
	v_mfma_f32_16x16x32_bf16 v[128:131], v[186:189], v[190:193], 0
	s_waitcnt lgkmcnt(2)
	v_mfma_f32_16x16x32_bf16 v[124:127], v[170:173], v[198:201], 0
	ds_read_b128 v[190:193], v162 offset:8192
	v_mfma_f32_16x16x32_bf16 v[120:123], v[174:177], v[198:201], 0
	v_mfma_f32_16x16x32_bf16 v[116:119], v[182:185], v[198:201], 0
	v_mfma_f32_16x16x32_bf16 v[112:115], v[186:189], v[198:201], 0
	s_waitcnt lgkmcnt(2)
	v_mfma_f32_16x16x32_bf16 v[108:111], v[170:173], v[178:181], 0
	ds_read_b128 v[198:201], v162 offset:10240
	buffer_load_dwordx4 v[12:15], v160, s[24:27], s69 offen
	s_waitcnt vmcnt(11)
	v_cvt_pk_bf16_f32 v3, v2, v3
	v_cvt_pk_bf16_f32 v2, v0, v1
	v_mfma_f32_16x16x32_bf16 v[104:107], v[174:177], v[178:181], 0
	ds_write_b64 v161, v[2:3] offset:43520
	v_mfma_f32_16x16x32_bf16 v[100:103], v[182:185], v[178:181], 0
	v_mfma_f32_16x16x32_bf16 v[96:99], v[186:189], v[178:181], 0
	s_add_i32 s74, s13, 0xfff40000
	s_waitcnt lgkmcnt(2)
	v_mfma_f32_16x16x32_bf16 v[92:95], v[170:173], v[190:193], 0
	ds_read_b128 v[178:181], v162 offset:12288
	v_mfma_f32_16x16x32_bf16 v[88:91], v[174:177], v[190:193], 0
	v_mfma_f32_16x16x32_bf16 v[84:87], v[182:185], v[190:193], 0
	v_mfma_f32_16x16x32_bf16 v[80:83], v[186:189], v[190:193], 0
	s_waitcnt lgkmcnt(2)
	v_mfma_f32_16x16x32_bf16 v[76:79], v[170:173], v[198:201], 0
	ds_read_b128 v[190:193], v162 offset:14336
	buffer_load_dwordx4 v[0:3], v160, s[24:27], s74 offen
	s_waitcnt vmcnt(11)
	v_cvt_pk_bf16_f32 v31, v30, v31
	v_cvt_pk_bf16_f32 v30, v28, v29
	v_mfma_f32_16x16x32_bf16 v[72:75], v[174:177], v[198:201], 0
	ds_write_b64 v161, v[30:31] offset:52224
	v_mfma_f32_16x16x32_bf16 v[68:71], v[182:185], v[198:201], 0
	v_mfma_f32_16x16x32_bf16 v[64:67], v[186:189], v[198:201], 0
	s_add_i32 s75, s13, 0xfff60000
	s_waitcnt lgkmcnt(2)
	v_mfma_f32_16x16x32_bf16 v[60:63], v[170:173], v[178:181], 0
	ds_read_b128 v[198:201], v162 offset:1024
	v_mfma_f32_16x16x32_bf16 v[56:59], v[174:177], v[178:181], 0
	v_mfma_f32_16x16x32_bf16 v[52:55], v[182:185], v[178:181], 0
	v_mfma_f32_16x16x32_bf16 v[48:51], v[186:189], v[178:181], 0
	s_waitcnt lgkmcnt(2)
	v_mfma_f32_16x16x32_bf16 v[44:47], v[170:173], v[190:193], 0
	ds_read_b128 v[170:173], v162 offset:3072
	buffer_load_dwordx4 v[28:31], v160, s[24:27], s75 offen
	s_waitcnt vmcnt(11)
	v_cvt_pk_bf16_f32 v27, v26, v27
	v_cvt_pk_bf16_f32 v26, v24, v25
	v_mfma_f32_16x16x32_bf16 v[40:43], v[174:177], v[190:193], 0
	ds_read_b64_tr_b16 v[244:245], v166 offset:17408
	ds_read_b64_tr_b16 v[248:249], v166 offset:17440
	ds_read_b64_tr_b16 v[202:203], v166 offset:17472
	ds_read_b64_tr_b16 v[206:207], v166 offset:17504
	ds_read_b64_tr_b16 v[246:247], v167 offset:17408
	ds_read_b64_tr_b16 v[250:251], v167 offset:17440
	ds_read_b64_tr_b16 v[204:205], v167 offset:17472
	ds_read_b64_tr_b16 v[208:209], v167 offset:17504
	ds_write_b64 v161, v[26:27] offset:60928
	v_mfma_f32_16x16x32_bf16 v[36:39], v[182:185], v[190:193], 0
	v_mfma_f32_16x16x32_bf16 v[32:35], v[186:189], v[190:193], 0
	s_add_i32 s76, s13, 0xfff80000
	s_waitcnt lgkmcnt(4)
	v_mfma_f32_16x16x32_bf16 v[156:159], v[244:247], v[198:201], v[156:159]
	ds_read_b128 v[182:185], v162 offset:5120
	s_waitcnt lgkmcnt(4)
	v_mfma_f32_16x16x32_bf16 v[152:155], v[248:251], v[198:201], v[152:155]
	s_waitcnt lgkmcnt(3)
	v_mfma_f32_16x16x32_bf16 v[148:151], v[202:205], v[198:201], v[148:151]
	s_waitcnt lgkmcnt(2)
	v_mfma_f32_16x16x32_bf16 v[144:147], v[206:209], v[198:201], v[144:147]
	v_mfma_f32_16x16x32_bf16 v[140:143], v[244:247], v[170:173], v[140:143]
	ds_read_b128 v[186:189], v162 offset:7168
	buffer_load_dwordx4 v[24:27], v160, s[24:27], s76 offen
	s_waitcnt vmcnt(11)
	v_cvt_pk_bf16_f32 v23, v22, v23
	v_cvt_pk_bf16_f32 v22, v20, v21
	v_mfma_f32_16x16x32_bf16 v[136:139], v[248:251], v[170:173], v[136:139]
	ds_write_b64 v161, v[22:23] offset:35072
	v_mfma_f32_16x16x32_bf16 v[132:135], v[202:205], v[170:173], v[132:135]
	v_mfma_f32_16x16x32_bf16 v[128:131], v[206:209], v[170:173], v[128:131]
	s_waitcnt lgkmcnt(2)
; #define G_DMA_A(kt, AO) do { G_DMA1(kt, AO, 0); G_DMA1(kt, AO, 1); G_DMA1(kt, AO, 2); G_DMA1(kt, AO, 3); if (MF == 9) G_DMA5(kt, AO); } while (0)
; #define G_ISSUE_B(kt) do { const unsigned _sb = (unsigned)(kt) * 4u * kstepB; \
;         _Pragma("unroll") for (int _i = 0; _i < 8; ++_i) sb[_i] = bload16(_i < 4 ? rsB0 : rsB1, vob, _sb + (_i & 3) * kstepB); } while (0)
; #define G_WRITE_B(BO) do { \
;         _Pragma("unroll") for (int _i = 0; _i < 8; ++_i) *(LAS u32x2*)(b_wr + (BO) + (_i & 3) * (16 * G_BSTRIDE) + (_i >> 2) * SLAB1) = pack4(__builtin_bit_cast(f32x4, sb[_i])); } while (0)
; #define G_ENDTILE(VM) do { asm volatile("s_waitcnt vmcnt(" #VM ")" ::: "memory"); \
;         asm volatile("s_waitcnt lgkmcnt(0)" ::: "memory"); __builtin_amdgcn_s_barrier(); asm volatile("" ::: "memory"); } while (0)
;     ...
;     __builtin_amdgcn_s_barrier();
;     G_DMA_A(0, G_A0); G_ISSUE_B(0); G_WRITE_B(G_B0);
;     __builtin_amdgcn_sched_barrier(0);
;     G_ISSUE_B(1);
;     __builtin_amdgcn_sched_barrier(0);
;     G_ENDTILE(8);
;     for (int ui = 0;; ++ui) {
; #pragma unroll
;         for (int m = 0; m < MF; ++m)
; #pragma unroll
;             for (int n = 0; n < 4; ++n) acc[m][n] = (f32x4){0.f, 0.f, 0.f, 0.f};
;         for (int t = 0; t < nt - 2; t += 2) {
;             G_TILE(G_A0, G_B0, true, G_B1, G_A1, t + 1, true, t + 2, (void)0);
;             G_ENDTILE(8);
;             G_TILE(G_A1, G_B1, true, G_B0, G_A0, t + 2, true, t + 3, (void)0);
;             G_ENDTILE(8);
	v_mfma_f32_16x16x32_bf16 v[124:127], v[244:247], v[182:185], v[124:127]
	ds_read_b128 v[170:173], v162 offset:9216
	v_mfma_f32_16x16x32_bf16 v[120:123], v[248:251], v[182:185], v[120:123]
	v_mfma_f32_16x16x32_bf16 v[116:119], v[202:205], v[182:185], v[116:119]
	v_mfma_f32_16x16x32_bf16 v[112:115], v[206:209], v[182:185], v[112:115]
	s_waitcnt lgkmcnt(2)
	v_mfma_f32_16x16x32_bf16 v[108:111], v[244:247], v[186:189], v[108:111]
	ds_read_b128 v[182:185], v162 offset:11264
	buffer_load_dwordx4 v[20:23], v160, s[16:19], s69 offen
	s_waitcnt vmcnt(11)
	v_cvt_pk_bf16_f32 v7, v6, v7
	v_cvt_pk_bf16_f32 v6, v4, v5
	v_mfma_f32_16x16x32_bf16 v[104:107], v[248:251], v[186:189], v[104:107]
	ds_write_b64 v161, v[6:7] offset:43776
	v_mfma_f32_16x16x32_bf16 v[100:103], v[202:205], v[186:189], v[100:103]
	v_mfma_f32_16x16x32_bf16 v[96:99], v[206:209], v[186:189], v[96:99]
	s_waitcnt lgkmcnt(2)
	v_mfma_f32_16x16x32_bf16 v[92:95], v[244:247], v[170:173], v[92:95]
	ds_read_b128 v[186:189], v162 offset:13312
	v_mfma_f32_16x16x32_bf16 v[88:91], v[248:251], v[170:173], v[88:91]
	v_mfma_f32_16x16x32_bf16 v[84:87], v[202:205], v[170:173], v[84:87]
	v_mfma_f32_16x16x32_bf16 v[80:83], v[206:209], v[170:173], v[80:83]
	s_waitcnt lgkmcnt(2)
	v_mfma_f32_16x16x32_bf16 v[76:79], v[244:247], v[182:185], v[76:79]
	ds_read_b128 v[252:255], v162 offset:15360
	buffer_load_dwordx4 v[4:7], v160, s[16:19], s74 offen
	s_waitcnt vmcnt(11)
	v_cvt_pk_bf16_f32 v11, v10, v11
	v_cvt_pk_bf16_f32 v10, v8, v9
	v_mfma_f32_16x16x32_bf16 v[72:75], v[248:251], v[182:185], v[72:75]
	ds_write_b64 v161, v[10:11] offset:52480
	v_mfma_f32_16x16x32_bf16 v[68:71], v[202:205], v[182:185], v[68:71]
	v_mfma_f32_16x16x32_bf16 v[64:67], v[206:209], v[182:185], v[64:67]
	s_waitcnt lgkmcnt(2)
	v_mfma_f32_16x16x32_bf16 v[60:63], v[244:247], v[186:189], v[60:63]
	buffer_load_dwordx4 v[8:11], v160, s[16:19], s75 offen
	s_waitcnt vmcnt(11)
	v_cvt_pk_bf16_f32 v19, v18, v19
	v_cvt_pk_bf16_f32 v18, v16, v17
	v_mfma_f32_16x16x32_bf16 v[56:59], v[248:251], v[186:189], v[56:59]
	ds_write_b64 v161, v[18:19] offset:61184
	v_mfma_f32_16x16x32_bf16 v[52:55], v[202:205], v[186:189], v[52:55]
	buffer_load_dwordx4 v[16:19], v160, s[16:19], s76 offen
	v_mfma_f32_16x16x32_bf16 v[48:51], v[206:209], v[186:189], v[48:51]
	s_waitcnt vmcnt(8)
	s_mov_b32 m0, s56
	s_waitcnt lgkmcnt(0)
	s_barrier
	ds_read_b64_tr_b16 v[170:171], v166 offset:34816
	ds_read_b64_tr_b16 v[172:173], v167 offset:34816
	ds_read_b64_tr_b16 v[176:177], v167 offset:34848
	ds_read_b128 v[178:181], v162 offset:32768
	ds_read_b64_tr_b16 v[174:175], v166 offset:34848
	ds_read_b64_tr_b16 v[182:183], v166 offset:34880
	ds_read_b64_tr_b16 v[186:187], v166 offset:34912
	ds_read_b64_tr_b16 v[184:185], v167 offset:34880
	ds_read_b64_tr_b16 v[188:189], v167 offset:34912
	ds_read_b128 v[190:193], v162 offset:34816
	ds_read_b128 v[198:201], v162 offset:36864
	buffer_load_dwordx4 v163, s[20:23], s45 offen lds
	s_mov_b32 m0, s57
	v_mfma_f32_16x16x32_bf16 v[44:47], v[244:247], v[252:255], v[44:47]
	v_mfma_f32_16x16x32_bf16 v[40:43], v[248:251], v[252:255], v[40:43]
	v_mfma_f32_16x16x32_bf16 v[36:39], v[202:205], v[252:255], v[36:39]
	v_mfma_f32_16x16x32_bf16 v[32:35], v[206:209], v[252:255], v[32:35]
	s_waitcnt lgkmcnt(7)
	v_mfma_f32_16x16x32_bf16 v[156:159], v[170:173], v[178:181], v[156:159]
	buffer_load_dwordx4 v165, s[20:23], s45 offen lds
	s_add_i32 s69, s13, 0xfffa0000
	s_waitcnt lgkmcnt(6)
	v_mfma_f32_16x16x32_bf16 v[152:155], v[174:177], v[178:181], v[152:155]
	s_waitcnt lgkmcnt(3)
	v_mfma_f32_16x16x32_bf16 v[148:151], v[182:185], v[178:181], v[148:151]
	s_waitcnt lgkmcnt(2)
	v_mfma_f32_16x16x32_bf16 v[144:147], v[186:189], v[178:181], v[144:147]
	s_waitcnt lgkmcnt(1)
	v_mfma_f32_16x16x32_bf16 v[140:143], v[170:173], v[190:193], v[140:143]
	s_mov_b32 m0, s58
	s_nop 0
	buffer_load_dwordx4 v164, s[20:23], s45 offen lds
	ds_read_b128 v[178:181], v162 offset:38912
	s_waitcnt vmcnt(10)
	v_cvt_pk_bf16_f32 v15, v14, v15
	v_cvt_pk_bf16_f32 v14, v12, v13
	v_mfma_f32_16x16x32_bf16 v[136:139], v[174:177], v[190:193], v[136:139]
	ds_write_b64 v161, v[14:15]
	v_mfma_f32_16x16x32_bf16 v[132:135], v[182:185], v[190:193], v[132:135]
	s_mov_b32 m0, s59
	s_nop 0
	buffer_load_dwordx4 v168, s[20:23], s45 offen lds
	v_mfma_f32_16x16x32_bf16 v[128:131], v[186:189], v[190:193], v[128:131]
	s_waitcnt lgkmcnt(2)
	v_mfma_f32_16x16x32_bf16 v[124:127], v[170:173], v[198:201], v[124:127]
	ds_read_b128 v[190:193], v162 offset:40960
	v_mfma_f32_16x16x32_bf16 v[120:123], v[174:177], v[198:201], v[120:123]
	v_mfma_f32_16x16x32_bf16 v[116:119], v[182:185], v[198:201], v[116:119]
	v_mfma_f32_16x16x32_bf16 v[112:115], v[186:189], v[198:201], v[112:115]
	s_waitcnt lgkmcnt(2)
	v_mfma_f32_16x16x32_bf16 v[108:111], v[170:173], v[178:181], v[108:111]
	ds_read_b128 v[198:201], v162 offset:43008
	buffer_load_dwordx4 v[12:15], v160, s[24:27], s69 offen
	s_waitcnt vmcnt(11)
	v_cvt_pk_bf16_f32 v3, v2, v3
	v_cvt_pk_bf16_f32 v2, v0, v1
	v_mfma_f32_16x16x32_bf16 v[104:107], v[174:177], v[178:181], v[104:107]
	ds_write_b64 v161, v[2:3] offset:8704
	v_mfma_f32_16x16x32_bf16 v[100:103], v[182:185], v[178:181], v[100:103]
	v_mfma_f32_16x16x32_bf16 v[96:99], v[186:189], v[178:181], v[96:99]
	s_add_i32 s74, s13, 0xfffc0000
	s_waitcnt lgkmcnt(2)
	v_mfma_f32_16x16x32_bf16 v[92:95], v[170:173], v[190:193], v[92:95]
	ds_read_b128 v[178:181], v162 offset:45056
	v_mfma_f32_16x16x32_bf16 v[88:91], v[174:177], v[190:193], v[88:91]
	v_mfma_f32_16x16x32_bf16 v[84:87], v[182:185], v[190:193], v[84:87]
	v_mfma_f32_16x16x32_bf16 v[80:83], v[186:189], v[190:193], v[80:83]
	s_waitcnt lgkmcnt(2)
; #define G_DMA_A(kt, AO) do { G_DMA1(kt, AO, 0); G_DMA1(kt, AO, 1); G_DMA1(kt, AO, 2); G_DMA1(kt, AO, 3); if (MF == 9) G_DMA5(kt, AO); } while (0)
; #define G_ISSUE_B(kt) do { const unsigned _sb = (unsigned)(kt) * 4u * kstepB; \
;         _Pragma("unroll") for (int _i = 0; _i < 8; ++_i) sb[_i] = bload16(_i < 4 ? rsB0 : rsB1, vob, _sb + (_i & 3) * kstepB); } while (0)
; #define G_WRITE_B(BO) do { \
;         _Pragma("unroll") for (int _i = 0; _i < 8; ++_i) *(LAS u32x2*)(b_wr + (BO) + (_i & 3) * (16 * G_BSTRIDE) + (_i >> 2) * SLAB1) = pack4(__builtin_bit_cast(f32x4, sb[_i])); } while (0)
; #define G_ENDTILE(VM) do { asm volatile("s_waitcnt vmcnt(" #VM ")" ::: "memory"); \
;         asm volatile("s_waitcnt lgkmcnt(0)" ::: "memory"); __builtin_amdgcn_s_barrier(); asm volatile("" ::: "memory"); } while (0)
;     ...
;     __builtin_amdgcn_s_barrier();
;     G_DMA_A(0, G_A0); G_ISSUE_B(0); G_WRITE_B(G_B0);
;     __builtin_amdgcn_sched_barrier(0);
;     G_ISSUE_B(1);
;     __builtin_amdgcn_sched_barrier(0);
;     G_ENDTILE(8);
;     for (int ui = 0;; ++ui) {
; #pragma unroll
;         for (int m = 0; m < MF; ++m)
; #pragma unroll
;             for (int n = 0; n < 4; ++n) acc[m][n] = (f32x4){0.f, 0.f, 0.f, 0.f};
;         for (int t = 0; t < nt - 2; t += 2) {
;             G_TILE(G_A0, G_B0, true, G_B1, G_A1, t + 1, true, t + 2, (void)0);
;             G_ENDTILE(8);
;             G_TILE(G_A1, G_B1, true, G_B0, G_A0, t + 2, true, t + 3, (void)0);
;             G_ENDTILE(8);
;         }
	v_mfma_f32_16x16x32_bf16 v[76:79], v[170:173], v[198:201], v[76:79]
	ds_read_b128 v[190:193], v162 offset:47104
	buffer_load_dwordx4 v[0:3], v160, s[24:27], s74 offen
	s_waitcnt vmcnt(11)
	v_cvt_pk_bf16_f32 v31, v30, v31
	v_cvt_pk_bf16_f32 v30, v28, v29
	v_mfma_f32_16x16x32_bf16 v[72:75], v[174:177], v[198:201], v[72:75]
	ds_write_b64 v161, v[30:31] offset:17408
	v_mfma_f32_16x16x32_bf16 v[68:71], v[182:185], v[198:201], v[68:71]
	v_mfma_f32_16x16x32_bf16 v[64:67], v[186:189], v[198:201], v[64:67]
	s_add_i32 s75, s13, 0xfffe0000
	s_waitcnt lgkmcnt(2)
	v_mfma_f32_16x16x32_bf16 v[60:63], v[170:173], v[178:181], v[60:63]
	ds_read_b128 v[198:201], v162 offset:33792
	v_mfma_f32_16x16x32_bf16 v[56:59], v[174:177], v[178:181], v[56:59]
	v_mfma_f32_16x16x32_bf16 v[52:55], v[182:185], v[178:181], v[52:55]
	v_mfma_f32_16x16x32_bf16 v[48:51], v[186:189], v[178:181], v[48:51]
	s_waitcnt lgkmcnt(2)
	v_mfma_f32_16x16x32_bf16 v[44:47], v[170:173], v[190:193], v[44:47]
	ds_read_b128 v[170:173], v162 offset:35840
	buffer_load_dwordx4 v[28:31], v160, s[24:27], s75 offen
	s_waitcnt vmcnt(11)
	v_cvt_pk_bf16_f32 v27, v26, v27
	v_cvt_pk_bf16_f32 v26, v24, v25
	v_mfma_f32_16x16x32_bf16 v[40:43], v[174:177], v[190:193], v[40:43]
	ds_read_b64_tr_b16 v[244:245], v166 offset:52224
	ds_read_b64_tr_b16 v[248:249], v166 offset:52256
	ds_read_b64_tr_b16 v[202:203], v166 offset:52288
	ds_read_b64_tr_b16 v[206:207], v166 offset:52320
	ds_read_b64_tr_b16 v[246:247], v167 offset:52224
	ds_read_b64_tr_b16 v[250:251], v167 offset:52256
	ds_read_b64_tr_b16 v[204:205], v167 offset:52288
	ds_read_b64_tr_b16 v[208:209], v167 offset:52320
	ds_write_b64 v161, v[26:27] offset:26112
	v_mfma_f32_16x16x32_bf16 v[36:39], v[182:185], v[190:193], v[36:39]
	v_mfma_f32_16x16x32_bf16 v[32:35], v[186:189], v[190:193], v[32:35]
	s_waitcnt lgkmcnt(4)
	v_mfma_f32_16x16x32_bf16 v[156:159], v[244:247], v[198:201], v[156:159]
	ds_read_b128 v[182:185], v162 offset:37888
	s_waitcnt lgkmcnt(4)
	v_mfma_f32_16x16x32_bf16 v[152:155], v[248:251], v[198:201], v[152:155]
	s_waitcnt lgkmcnt(3)
	v_mfma_f32_16x16x32_bf16 v[148:151], v[202:205], v[198:201], v[148:151]
	s_waitcnt lgkmcnt(2)
	v_mfma_f32_16x16x32_bf16 v[144:147], v[206:209], v[198:201], v[144:147]
	v_mfma_f32_16x16x32_bf16 v[140:143], v[244:247], v[170:173], v[140:143]
	ds_read_b128 v[186:189], v162 offset:39936
	buffer_load_dwordx4 v[24:27], v160, s[24:27], s13 offen
	s_waitcnt vmcnt(11)
	v_cvt_pk_bf16_f32 v23, v22, v23
	v_cvt_pk_bf16_f32 v22, v20, v21
	v_mfma_f32_16x16x32_bf16 v[136:139], v[248:251], v[170:173], v[136:139]
	ds_write_b64 v161, v[22:23] offset:256
	v_mfma_f32_16x16x32_bf16 v[132:135], v[202:205], v[170:173], v[132:135]
	v_mfma_f32_16x16x32_bf16 v[128:131], v[206:209], v[170:173], v[128:131]
	s_waitcnt lgkmcnt(2)
	v_mfma_f32_16x16x32_bf16 v[124:127], v[244:247], v[182:185], v[124:127]
	ds_read_b128 v[170:173], v162 offset:41984
	v_mfma_f32_16x16x32_bf16 v[120:123], v[248:251], v[182:185], v[120:123]
	v_mfma_f32_16x16x32_bf16 v[116:119], v[202:205], v[182:185], v[116:119]
	v_mfma_f32_16x16x32_bf16 v[112:115], v[206:209], v[182:185], v[112:115]
	s_waitcnt lgkmcnt(2)
	v_mfma_f32_16x16x32_bf16 v[108:111], v[244:247], v[186:189], v[108:111]
	ds_read_b128 v[182:185], v162 offset:44032
	buffer_load_dwordx4 v[20:23], v160, s[16:19], s69 offen
	s_waitcnt vmcnt(11)
	v_cvt_pk_bf16_f32 v7, v6, v7
	v_cvt_pk_bf16_f32 v6, v4, v5
	v_mfma_f32_16x16x32_bf16 v[104:107], v[248:251], v[186:189], v[104:107]
	ds_write_b64 v161, v[6:7] offset:8960
	v_mfma_f32_16x16x32_bf16 v[100:103], v[202:205], v[186:189], v[100:103]
	v_mfma_f32_16x16x32_bf16 v[96:99], v[206:209], v[186:189], v[96:99]
	s_waitcnt lgkmcnt(2)
	v_mfma_f32_16x16x32_bf16 v[92:95], v[244:247], v[170:173], v[92:95]
	ds_read_b128 v[186:189], v162 offset:46080
	v_mfma_f32_16x16x32_bf16 v[88:91], v[248:251], v[170:173], v[88:91]
	v_mfma_f32_16x16x32_bf16 v[84:87], v[202:205], v[170:173], v[84:87]
	v_mfma_f32_16x16x32_bf16 v[80:83], v[206:209], v[170:173], v[80:83]
	s_waitcnt lgkmcnt(2)
	v_mfma_f32_16x16x32_bf16 v[76:79], v[244:247], v[182:185], v[76:79]
	ds_read_b128 v[252:255], v162 offset:48128
	buffer_load_dwordx4 v[4:7], v160, s[16:19], s74 offen
	s_waitcnt vmcnt(11)
	v_cvt_pk_bf16_f32 v11, v10, v11
	v_cvt_pk_bf16_f32 v10, v8, v9
	v_mfma_f32_16x16x32_bf16 v[72:75], v[248:251], v[182:185], v[72:75]
	ds_write_b64 v161, v[10:11] offset:17664
	v_mfma_f32_16x16x32_bf16 v[68:71], v[202:205], v[182:185], v[68:71]
	v_mfma_f32_16x16x32_bf16 v[64:67], v[206:209], v[182:185], v[64:67]
	s_waitcnt lgkmcnt(2)
	v_mfma_f32_16x16x32_bf16 v[60:63], v[244:247], v[186:189], v[60:63]
	buffer_load_dwordx4 v[8:11], v160, s[16:19], s75 offen
	s_waitcnt vmcnt(11)
	v_cvt_pk_bf16_f32 v19, v18, v19
	v_cvt_pk_bf16_f32 v18, v16, v17
	v_mfma_f32_16x16x32_bf16 v[56:59], v[248:251], v[186:189], v[56:59]
	ds_write_b64 v161, v[18:19] offset:26368
	v_mfma_f32_16x16x32_bf16 v[52:55], v[202:205], v[186:189], v[52:55]
	buffer_load_dwordx4 v[16:19], v160, s[16:19], s13 offen
	v_mfma_f32_16x16x32_bf16 v[48:51], v[206:209], v[186:189], v[48:51]
	s_add_i32 s12, s12, 2
	s_add_i32 s13, s13, 0x100000
	s_addk_i32 s45, 0x100
	s_cmp_ge_i32 s12, s30
	s_waitcnt vmcnt(8)
	s_waitcnt lgkmcnt(0)
	s_barrier
	s_cbranch_scc1 .Lflush_PLE
; #define G_DMA_A(kt, AO) do { G_DMA1(kt, AO, 0); G_DMA1(kt, AO, 1); G_DMA1(kt, AO, 2); G_DMA1(kt, AO, 3); if (MF == 9) G_DMA5(kt, AO); } while (0)
; #define G_ISSUE_B(kt) do { const unsigned _sb = (unsigned)(kt) * 4u * kstepB; \
;         _Pragma("unroll") for (int _i = 0; _i < 8; ++_i) sb[_i] = bload16(_i < 4 ? rsB0 : rsB1, vob, _sb + (_i & 3) * kstepB); } while (0)
; #define G_WRITE_B(BO) do { \
;         _Pragma("unroll") for (int _i = 0; _i < 8; ++_i) *(LAS u32x2*)(b_wr + (BO) + (_i & 3) * (16 * G_BSTRIDE) + (_i >> 2) * SLAB1) = pack4(__builtin_bit_cast(f32x4, sb[_i])); } while (0)
; #define G_ENDTILE(VM) do { asm volatile("s_waitcnt vmcnt(" #VM ")" ::: "memory"); \
;         asm volatile("s_waitcnt lgkmcnt(0)" ::: "memory"); __builtin_amdgcn_s_barrier(); asm volatile("" ::: "memory"); } while (0)
;     ...
;     __builtin_amdgcn_s_barrier();
;     G_DMA_A(0, G_A0); G_ISSUE_B(0); G_WRITE_B(G_B0);
;     __builtin_amdgcn_sched_barrier(0);
;     G_ISSUE_B(1);
;     __builtin_amdgcn_sched_barrier(0);
;     G_ENDTILE(8);
;     for (int ui = 0;; ++ui) {
; #pragma unroll
;         for (int m = 0; m < MF; ++m)
; #pragma unroll
;             for (int n = 0; n < 4; ++n) acc[m][n] = (f32x4){0.f, 0.f, 0.f, 0.f};
;         for (int t = 0; t < nt - 2; t += 2) {
;             G_TILE(G_A0, G_B0, true, G_B1, G_A1, t + 1, true, t + 2, (void)0);
.LBB0_899:
	s_mov_b32 m0, s64
	s_add_i32 s69, s45, 0xffffff80
	ds_read_b64_tr_b16 v[170:171], v166
	ds_read_b64_tr_b16 v[172:173], v167
	ds_read_b64_tr_b16 v[176:177], v167 offset:32
	ds_read_b128 v[178:181], v162
	ds_read_b64_tr_b16 v[174:175], v166 offset:32
	ds_read_b64_tr_b16 v[182:183], v166 offset:64
	ds_read_b64_tr_b16 v[186:187], v166 offset:96
	ds_read_b64_tr_b16 v[184:185], v167 offset:64
	ds_read_b64_tr_b16 v[188:189], v167 offset:96
	ds_read_b128 v[190:193], v162 offset:2048
	ds_read_b128 v[198:201], v162 offset:4096
	buffer_load_dwordx4 v163, s[20:23], s69 offen lds
	s_mov_b32 m0, s63
	v_mfma_f32_16x16x32_bf16 v[44:47], v[244:247], v[252:255], v[44:47]
	v_mfma_f32_16x16x32_bf16 v[40:43], v[248:251], v[252:255], v[40:43]
	v_mfma_f32_16x16x32_bf16 v[36:39], v[202:205], v[252:255], v[36:39]
	v_mfma_f32_16x16x32_bf16 v[32:35], v[206:209], v[252:255], v[32:35]
	s_waitcnt lgkmcnt(7)
	v_mfma_f32_16x16x32_bf16 v[156:159], v[170:173], v[178:181], v[156:159]
	buffer_load_dwordx4 v165, s[20:23], s69 offen lds
	s_waitcnt lgkmcnt(6)
	v_mfma_f32_16x16x32_bf16 v[152:155], v[174:177], v[178:181], v[152:155]
	s_waitcnt lgkmcnt(3)
	v_mfma_f32_16x16x32_bf16 v[148:151], v[182:185], v[178:181], v[148:151]
	s_waitcnt lgkmcnt(2)
	v_mfma_f32_16x16x32_bf16 v[144:147], v[186:189], v[178:181], v[144:147]
	s_waitcnt lgkmcnt(1)
	v_mfma_f32_16x16x32_bf16 v[140:143], v[170:173], v[190:193], v[140:143]
	s_mov_b32 m0, s62
	s_nop 0
	buffer_load_dwordx4 v164, s[20:23], s69 offen lds
	ds_read_b128 v[178:181], v162 offset:6144
	s_waitcnt vmcnt(10)
	v_cvt_pk_bf16_f32 v15, v14, v15
	v_cvt_pk_bf16_f32 v14, v12, v13
	v_mfma_f32_16x16x32_bf16 v[136:139], v[174:177], v[190:193], v[136:139]
	ds_write_b64 v161, v[14:15] offset:34816
	v_mfma_f32_16x16x32_bf16 v[132:135], v[182:185], v[190:193], v[132:135]
	s_mov_b32 m0, s31
	s_nop 0
	buffer_load_dwordx4 v168, s[20:23], s69 offen lds
	s_add_i32 s69, s13, 0xfff20000
	v_mfma_f32_16x16x32_bf16 v[128:131], v[186:189], v[190:193], v[128:131]
	s_waitcnt lgkmcnt(2)
	v_mfma_f32_16x16x32_bf16 v[124:127], v[170:173], v[198:201], v[124:127]
	ds_read_b128 v[190:193], v162 offset:8192
	v_mfma_f32_16x16x32_bf16 v[120:123], v[174:177], v[198:201], v[120:123]
	v_mfma_f32_16x16x32_bf16 v[116:119], v[182:185], v[198:201], v[116:119]
	v_mfma_f32_16x16x32_bf16 v[112:115], v[186:189], v[198:201], v[112:115]
	s_waitcnt lgkmcnt(2)
	v_mfma_f32_16x16x32_bf16 v[108:111], v[170:173], v[178:181], v[108:111]
	ds_read_b128 v[198:201], v162 offset:10240
	buffer_load_dwordx4 v[12:15], v160, s[24:27], s69 offen
	s_waitcnt vmcnt(11)
	v_cvt_pk_bf16_f32 v3, v2, v3
	v_cvt_pk_bf16_f32 v2, v0, v1
	v_mfma_f32_16x16x32_bf16 v[104:107], v[174:177], v[178:181], v[104:107]
	ds_write_b64 v161, v[2:3] offset:43520
	v_mfma_f32_16x16x32_bf16 v[100:103], v[182:185], v[178:181], v[100:103]
	v_mfma_f32_16x16x32_bf16 v[96:99], v[186:189], v[178:181], v[96:99]
	s_add_i32 s74, s13, 0xfff40000
	s_waitcnt lgkmcnt(2)
	v_mfma_f32_16x16x32_bf16 v[92:95], v[170:173], v[190:193], v[92:95]
	ds_read_b128 v[178:181], v162 offset:12288
	v_mfma_f32_16x16x32_bf16 v[88:91], v[174:177], v[190:193], v[88:91]
	v_mfma_f32_16x16x32_bf16 v[84:87], v[182:185], v[190:193], v[84:87]
	v_mfma_f32_16x16x32_bf16 v[80:83], v[186:189], v[190:193], v[80:83]
	s_waitcnt lgkmcnt(2)
	v_mfma_f32_16x16x32_bf16 v[76:79], v[170:173], v[198:201], v[76:79]
	ds_read_b128 v[190:193], v162 offset:14336
	buffer_load_dwordx4 v[0:3], v160, s[24:27], s74 offen
	s_waitcnt vmcnt(11)
	v_cvt_pk_bf16_f32 v31, v30, v31
	v_cvt_pk_bf16_f32 v30, v28, v29
	v_mfma_f32_16x16x32_bf16 v[72:75], v[174:177], v[198:201], v[72:75]
	ds_write_b64 v161, v[30:31] offset:52224
	v_mfma_f32_16x16x32_bf16 v[68:71], v[182:185], v[198:201], v[68:71]
	v_mfma_f32_16x16x32_bf16 v[64:67], v[186:189], v[198:201], v[64:67]
	s_add_i32 s75, s13, 0xfff60000
	s_waitcnt lgkmcnt(2)
	v_mfma_f32_16x16x32_bf16 v[60:63], v[170:173], v[178:181], v[60:63]
	ds_read_b128 v[198:201], v162 offset:1024
	v_mfma_f32_16x16x32_bf16 v[56:59], v[174:177], v[178:181], v[56:59]
	v_mfma_f32_16x16x32_bf16 v[52:55], v[182:185], v[178:181], v[52:55]
	v_mfma_f32_16x16x32_bf16 v[48:51], v[186:189], v[178:181], v[48:51]
	s_waitcnt lgkmcnt(2)
	v_mfma_f32_16x16x32_bf16 v[44:47], v[170:173], v[190:193], v[44:47]
	ds_read_b128 v[170:173], v162 offset:3072
	buffer_load_dwordx4 v[28:31], v160, s[24:27], s75 offen
	s_waitcnt vmcnt(11)
	v_cvt_pk_bf16_f32 v27, v26, v27
	v_cvt_pk_bf16_f32 v26, v24, v25
	v_mfma_f32_16x16x32_bf16 v[40:43], v[174:177], v[190:193], v[40:43]
	ds_read_b64_tr_b16 v[244:245], v166 offset:17408
	ds_read_b64_tr_b16 v[248:249], v166 offset:17440
	ds_read_b64_tr_b16 v[202:203], v166 offset:17472
	ds_read_b64_tr_b16 v[206:207], v166 offset:17504
	ds_read_b64_tr_b16 v[246:247], v167 offset:17408
	ds_read_b64_tr_b16 v[250:251], v167 offset:17440
	ds_read_b64_tr_b16 v[204:205], v167 offset:17472
	ds_read_b64_tr_b16 v[208:209], v167 offset:17504
	ds_write_b64 v161, v[26:27] offset:60928
	v_mfma_f32_16x16x32_bf16 v[36:39], v[182:185], v[190:193], v[36:39]
	v_mfma_f32_16x16x32_bf16 v[32:35], v[186:189], v[190:193], v[32:35]
	s_add_i32 s76, s13, 0xfff80000
	s_waitcnt lgkmcnt(4)
	v_mfma_f32_16x16x32_bf16 v[156:159], v[244:247], v[198:201], v[156:159]
	ds_read_b128 v[182:185], v162 offset:5120
	s_waitcnt lgkmcnt(4)
	v_mfma_f32_16x16x32_bf16 v[152:155], v[248:251], v[198:201], v[152:155]
	s_waitcnt lgkmcnt(3)
	v_mfma_f32_16x16x32_bf16 v[148:151], v[202:205], v[198:201], v[148:151]
	s_waitcnt lgkmcnt(2)
	v_mfma_f32_16x16x32_bf16 v[144:147], v[206:209], v[198:201], v[144:147]
	v_mfma_f32_16x16x32_bf16 v[140:143], v[244:247], v[170:173], v[140:143]
	ds_read_b128 v[186:189], v162 offset:7168
	buffer_load_dwordx4 v[24:27], v160, s[24:27], s76 offen
	s_waitcnt vmcnt(11)
; #define G_DMA_A(kt, AO) do { G_DMA1(kt, AO, 0); G_DMA1(kt, AO, 1); G_DMA1(kt, AO, 2); G_DMA1(kt, AO, 3); if (MF == 9) G_DMA5(kt, AO); } while (0)
; #define G_ISSUE_B(kt) do { const unsigned _sb = (unsigned)(kt) * 4u * kstepB; \
;         _Pragma("unroll") for (int _i = 0; _i < 8; ++_i) sb[_i] = bload16(_i < 4 ? rsB0 : rsB1, vob, _sb + (_i & 3) * kstepB); } while (0)
; #define G_WRITE_B(BO) do { \
;         _Pragma("unroll") for (int _i = 0; _i < 8; ++_i) *(LAS u32x2*)(b_wr + (BO) + (_i & 3) * (16 * G_BSTRIDE) + (_i >> 2) * SLAB1) = pack4(__builtin_bit_cast(f32x4, sb[_i])); } while (0)
; #define G_ENDTILE(VM) do { asm volatile("s_waitcnt vmcnt(" #VM ")" ::: "memory"); \
;         asm volatile("s_waitcnt lgkmcnt(0)" ::: "memory"); __builtin_amdgcn_s_barrier(); asm volatile("" ::: "memory"); } while (0)
;     ...
;     __builtin_amdgcn_s_barrier();
;     G_DMA_A(0, G_A0); G_ISSUE_B(0); G_WRITE_B(G_B0);
;     __builtin_amdgcn_sched_barrier(0);
;     G_ISSUE_B(1);
;     __builtin_amdgcn_sched_barrier(0);
;     G_ENDTILE(8);
;     for (int ui = 0;; ++ui) {
; #pragma unroll
;         for (int m = 0; m < MF; ++m)
; #pragma unroll
;             for (int n = 0; n < 4; ++n) acc[m][n] = (f32x4){0.f, 0.f, 0.f, 0.f};
;         for (int t = 0; t < nt - 2; t += 2) {
;             G_TILE(G_A0, G_B0, true, G_B1, G_A1, t + 1, true, t + 2, (void)0);
;             G_ENDTILE(8);
;             G_TILE(G_A1, G_B1, true, G_B0, G_A0, t + 2, true, t + 3, (void)0);
;             G_ENDTILE(8);
	v_cvt_pk_bf16_f32 v23, v22, v23
	v_cvt_pk_bf16_f32 v22, v20, v21
	v_mfma_f32_16x16x32_bf16 v[136:139], v[248:251], v[170:173], v[136:139]
	ds_write_b64 v161, v[22:23] offset:35072
	v_mfma_f32_16x16x32_bf16 v[132:135], v[202:205], v[170:173], v[132:135]
	v_mfma_f32_16x16x32_bf16 v[128:131], v[206:209], v[170:173], v[128:131]
	s_waitcnt lgkmcnt(2)
	v_mfma_f32_16x16x32_bf16 v[124:127], v[244:247], v[182:185], v[124:127]
	ds_read_b128 v[170:173], v162 offset:9216
	v_mfma_f32_16x16x32_bf16 v[120:123], v[248:251], v[182:185], v[120:123]
	v_mfma_f32_16x16x32_bf16 v[116:119], v[202:205], v[182:185], v[116:119]
	v_mfma_f32_16x16x32_bf16 v[112:115], v[206:209], v[182:185], v[112:115]
	s_waitcnt lgkmcnt(2)
	v_mfma_f32_16x16x32_bf16 v[108:111], v[244:247], v[186:189], v[108:111]
	ds_read_b128 v[182:185], v162 offset:11264
	buffer_load_dwordx4 v[20:23], v160, s[16:19], s69 offen
	s_waitcnt vmcnt(11)
	v_cvt_pk_bf16_f32 v7, v6, v7
	v_cvt_pk_bf16_f32 v6, v4, v5
	v_mfma_f32_16x16x32_bf16 v[104:107], v[248:251], v[186:189], v[104:107]
	ds_write_b64 v161, v[6:7] offset:43776
	v_mfma_f32_16x16x32_bf16 v[100:103], v[202:205], v[186:189], v[100:103]
	v_mfma_f32_16x16x32_bf16 v[96:99], v[206:209], v[186:189], v[96:99]
	s_waitcnt lgkmcnt(2)
	v_mfma_f32_16x16x32_bf16 v[92:95], v[244:247], v[170:173], v[92:95]
	ds_read_b128 v[186:189], v162 offset:13312
	v_mfma_f32_16x16x32_bf16 v[88:91], v[248:251], v[170:173], v[88:91]
	v_mfma_f32_16x16x32_bf16 v[84:87], v[202:205], v[170:173], v[84:87]
	v_mfma_f32_16x16x32_bf16 v[80:83], v[206:209], v[170:173], v[80:83]
	s_waitcnt lgkmcnt(2)
	v_mfma_f32_16x16x32_bf16 v[76:79], v[244:247], v[182:185], v[76:79]
	ds_read_b128 v[252:255], v162 offset:15360
	buffer_load_dwordx4 v[4:7], v160, s[16:19], s74 offen
	s_waitcnt vmcnt(11)
	v_cvt_pk_bf16_f32 v11, v10, v11
	v_cvt_pk_bf16_f32 v10, v8, v9
	v_mfma_f32_16x16x32_bf16 v[72:75], v[248:251], v[182:185], v[72:75]
	ds_write_b64 v161, v[10:11] offset:52480
	v_mfma_f32_16x16x32_bf16 v[68:71], v[202:205], v[182:185], v[68:71]
	v_mfma_f32_16x16x32_bf16 v[64:67], v[206:209], v[182:185], v[64:67]
	s_waitcnt lgkmcnt(2)
	v_mfma_f32_16x16x32_bf16 v[60:63], v[244:247], v[186:189], v[60:63]
	buffer_load_dwordx4 v[8:11], v160, s[16:19], s75 offen
	s_waitcnt vmcnt(11)
	v_cvt_pk_bf16_f32 v19, v18, v19
	v_cvt_pk_bf16_f32 v18, v16, v17
	v_mfma_f32_16x16x32_bf16 v[56:59], v[248:251], v[186:189], v[56:59]
	ds_write_b64 v161, v[18:19] offset:61184
	v_mfma_f32_16x16x32_bf16 v[52:55], v[202:205], v[186:189], v[52:55]
	buffer_load_dwordx4 v[16:19], v160, s[16:19], s76 offen
	v_mfma_f32_16x16x32_bf16 v[48:51], v[206:209], v[186:189], v[48:51]
	s_waitcnt vmcnt(8)
	s_mov_b32 m0, s56
	s_waitcnt lgkmcnt(0)
	s_barrier
	ds_read_b64_tr_b16 v[170:171], v166 offset:34816
	ds_read_b64_tr_b16 v[172:173], v167 offset:34816
	ds_read_b64_tr_b16 v[176:177], v167 offset:34848
	ds_read_b128 v[178:181], v162 offset:32768
	ds_read_b64_tr_b16 v[174:175], v166 offset:34848
	ds_read_b64_tr_b16 v[182:183], v166 offset:34880
	ds_read_b64_tr_b16 v[186:187], v166 offset:34912
	ds_read_b64_tr_b16 v[184:185], v167 offset:34880
	ds_read_b64_tr_b16 v[188:189], v167 offset:34912
	ds_read_b128 v[190:193], v162 offset:34816
	ds_read_b128 v[198:201], v162 offset:36864
	buffer_load_dwordx4 v163, s[20:23], s45 offen lds
	s_mov_b32 m0, s57
	v_mfma_f32_16x16x32_bf16 v[44:47], v[244:247], v[252:255], v[44:47]
	v_mfma_f32_16x16x32_bf16 v[40:43], v[248:251], v[252:255], v[40:43]
	v_mfma_f32_16x16x32_bf16 v[36:39], v[202:205], v[252:255], v[36:39]
	v_mfma_f32_16x16x32_bf16 v[32:35], v[206:209], v[252:255], v[32:35]
	s_waitcnt lgkmcnt(7)
	v_mfma_f32_16x16x32_bf16 v[156:159], v[170:173], v[178:181], v[156:159]
	buffer_load_dwordx4 v165, s[20:23], s45 offen lds
	s_add_i32 s69, s13, 0xfffa0000
	s_waitcnt lgkmcnt(6)
	v_mfma_f32_16x16x32_bf16 v[152:155], v[174:177], v[178:181], v[152:155]
	s_waitcnt lgkmcnt(3)
	v_mfma_f32_16x16x32_bf16 v[148:151], v[182:185], v[178:181], v[148:151]
	s_waitcnt lgkmcnt(2)
	v_mfma_f32_16x16x32_bf16 v[144:147], v[186:189], v[178:181], v[144:147]
	s_waitcnt lgkmcnt(1)
	v_mfma_f32_16x16x32_bf16 v[140:143], v[170:173], v[190:193], v[140:143]
	s_mov_b32 m0, s58
	s_nop 0
	buffer_load_dwordx4 v164, s[20:23], s45 offen lds
	ds_read_b128 v[178:181], v162 offset:38912
	s_waitcnt vmcnt(10)
	v_cvt_pk_bf16_f32 v15, v14, v15
	v_cvt_pk_bf16_f32 v14, v12, v13
	v_mfma_f32_16x16x32_bf16 v[136:139], v[174:177], v[190:193], v[136:139]
	ds_write_b64 v161, v[14:15]
	v_mfma_f32_16x16x32_bf16 v[132:135], v[182:185], v[190:193], v[132:135]
	s_mov_b32 m0, s59
	s_nop 0
	buffer_load_dwordx4 v168, s[20:23], s45 offen lds
	v_mfma_f32_16x16x32_bf16 v[128:131], v[186:189], v[190:193], v[128:131]
	s_waitcnt lgkmcnt(2)
	v_mfma_f32_16x16x32_bf16 v[124:127], v[170:173], v[198:201], v[124:127]
	ds_read_b128 v[190:193], v162 offset:40960
	v_mfma_f32_16x16x32_bf16 v[120:123], v[174:177], v[198:201], v[120:123]
	v_mfma_f32_16x16x32_bf16 v[116:119], v[182:185], v[198:201], v[116:119]
	v_mfma_f32_16x16x32_bf16 v[112:115], v[186:189], v[198:201], v[112:115]
	s_waitcnt lgkmcnt(2)
	v_mfma_f32_16x16x32_bf16 v[108:111], v[170:173], v[178:181], v[108:111]
	ds_read_b128 v[198:201], v162 offset:43008
	buffer_load_dwordx4 v[12:15], v160, s[24:27], s69 offen
	s_waitcnt vmcnt(11)
	v_cvt_pk_bf16_f32 v3, v2, v3
	v_cvt_pk_bf16_f32 v2, v0, v1
	v_mfma_f32_16x16x32_bf16 v[104:107], v[174:177], v[178:181], v[104:107]
	ds_write_b64 v161, v[2:3] offset:8704
	v_mfma_f32_16x16x32_bf16 v[100:103], v[182:185], v[178:181], v[100:103]
	v_mfma_f32_16x16x32_bf16 v[96:99], v[186:189], v[178:181], v[96:99]
	s_add_i32 s74, s13, 0xfffc0000
	s_waitcnt lgkmcnt(2)
; #define G_DMA_A(kt, AO) do { G_DMA1(kt, AO, 0); G_DMA1(kt, AO, 1); G_DMA1(kt, AO, 2); G_DMA1(kt, AO, 3); if (MF == 9) G_DMA5(kt, AO); } while (0)
; #define G_ISSUE_B(kt) do { const unsigned _sb = (unsigned)(kt) * 4u * kstepB; \
;         _Pragma("unroll") for (int _i = 0; _i < 8; ++_i) sb[_i] = bload16(_i < 4 ? rsB0 : rsB1, vob, _sb + (_i & 3) * kstepB); } while (0)
; #define G_WRITE_B(BO) do { \
;         _Pragma("unroll") for (int _i = 0; _i < 8; ++_i) *(LAS u32x2*)(b_wr + (BO) + (_i & 3) * (16 * G_BSTRIDE) + (_i >> 2) * SLAB1) = pack4(__builtin_bit_cast(f32x4, sb[_i])); } while (0)
; #define G_ENDTILE(VM) do { asm volatile("s_waitcnt vmcnt(" #VM ")" ::: "memory"); \
;         asm volatile("s_waitcnt lgkmcnt(0)" ::: "memory"); __builtin_amdgcn_s_barrier(); asm volatile("" ::: "memory"); } while (0)
;     ...
;     __builtin_amdgcn_s_barrier();
;     G_DMA_A(0, G_A0); G_ISSUE_B(0); G_WRITE_B(G_B0);
;     __builtin_amdgcn_sched_barrier(0);
;     G_ISSUE_B(1);
;     __builtin_amdgcn_sched_barrier(0);
;     G_ENDTILE(8);
;     for (int ui = 0;; ++ui) {
; #pragma unroll
;         for (int m = 0; m < MF; ++m)
; #pragma unroll
;             for (int n = 0; n < 4; ++n) acc[m][n] = (f32x4){0.f, 0.f, 0.f, 0.f};
;         for (int t = 0; t < nt - 2; t += 2) {
;             G_TILE(G_A0, G_B0, true, G_B1, G_A1, t + 1, true, t + 2, (void)0);
;             G_ENDTILE(8);
;             G_TILE(G_A1, G_B1, true, G_B0, G_A0, t + 2, true, t + 3, (void)0);
;             G_ENDTILE(8);
;         }
	v_mfma_f32_16x16x32_bf16 v[92:95], v[170:173], v[190:193], v[92:95]
	ds_read_b128 v[178:181], v162 offset:45056
	v_mfma_f32_16x16x32_bf16 v[88:91], v[174:177], v[190:193], v[88:91]
	v_mfma_f32_16x16x32_bf16 v[84:87], v[182:185], v[190:193], v[84:87]
	v_mfma_f32_16x16x32_bf16 v[80:83], v[186:189], v[190:193], v[80:83]
	s_waitcnt lgkmcnt(2)
	v_mfma_f32_16x16x32_bf16 v[76:79], v[170:173], v[198:201], v[76:79]
	ds_read_b128 v[190:193], v162 offset:47104
	buffer_load_dwordx4 v[0:3], v160, s[24:27], s74 offen
	s_waitcnt vmcnt(11)
	v_cvt_pk_bf16_f32 v31, v30, v31
	v_cvt_pk_bf16_f32 v30, v28, v29
	v_mfma_f32_16x16x32_bf16 v[72:75], v[174:177], v[198:201], v[72:75]
	ds_write_b64 v161, v[30:31] offset:17408
	v_mfma_f32_16x16x32_bf16 v[68:71], v[182:185], v[198:201], v[68:71]
	v_mfma_f32_16x16x32_bf16 v[64:67], v[186:189], v[198:201], v[64:67]
	s_add_i32 s75, s13, 0xfffe0000
	s_waitcnt lgkmcnt(2)
	v_mfma_f32_16x16x32_bf16 v[60:63], v[170:173], v[178:181], v[60:63]
	ds_read_b128 v[198:201], v162 offset:33792
	v_mfma_f32_16x16x32_bf16 v[56:59], v[174:177], v[178:181], v[56:59]
	v_mfma_f32_16x16x32_bf16 v[52:55], v[182:185], v[178:181], v[52:55]
	v_mfma_f32_16x16x32_bf16 v[48:51], v[186:189], v[178:181], v[48:51]
	s_waitcnt lgkmcnt(2)
	v_mfma_f32_16x16x32_bf16 v[44:47], v[170:173], v[190:193], v[44:47]
	ds_read_b128 v[170:173], v162 offset:35840
	buffer_load_dwordx4 v[28:31], v160, s[24:27], s75 offen
	s_waitcnt vmcnt(11)
	v_cvt_pk_bf16_f32 v27, v26, v27
	v_cvt_pk_bf16_f32 v26, v24, v25
	v_mfma_f32_16x16x32_bf16 v[40:43], v[174:177], v[190:193], v[40:43]
	ds_read_b64_tr_b16 v[244:245], v166 offset:52224
	ds_read_b64_tr_b16 v[248:249], v166 offset:52256
	ds_read_b64_tr_b16 v[202:203], v166 offset:52288
	ds_read_b64_tr_b16 v[206:207], v166 offset:52320
	ds_read_b64_tr_b16 v[246:247], v167 offset:52224
	ds_read_b64_tr_b16 v[250:251], v167 offset:52256
	ds_read_b64_tr_b16 v[204:205], v167 offset:52288
	ds_read_b64_tr_b16 v[208:209], v167 offset:52320
	ds_write_b64 v161, v[26:27] offset:26112
	v_mfma_f32_16x16x32_bf16 v[36:39], v[182:185], v[190:193], v[36:39]
	v_mfma_f32_16x16x32_bf16 v[32:35], v[186:189], v[190:193], v[32:35]
	s_waitcnt lgkmcnt(4)
	v_mfma_f32_16x16x32_bf16 v[156:159], v[244:247], v[198:201], v[156:159]
	ds_read_b128 v[182:185], v162 offset:37888
	s_waitcnt lgkmcnt(4)
	v_mfma_f32_16x16x32_bf16 v[152:155], v[248:251], v[198:201], v[152:155]
	s_waitcnt lgkmcnt(3)
	v_mfma_f32_16x16x32_bf16 v[148:151], v[202:205], v[198:201], v[148:151]
	s_waitcnt lgkmcnt(2)
	v_mfma_f32_16x16x32_bf16 v[144:147], v[206:209], v[198:201], v[144:147]
	v_mfma_f32_16x16x32_bf16 v[140:143], v[244:247], v[170:173], v[140:143]
	ds_read_b128 v[186:189], v162 offset:39936
	buffer_load_dwordx4 v[24:27], v160, s[24:27], s13 offen
	s_waitcnt vmcnt(11)
	v_cvt_pk_bf16_f32 v23, v22, v23
	v_cvt_pk_bf16_f32 v22, v20, v21
	v_mfma_f32_16x16x32_bf16 v[136:139], v[248:251], v[170:173], v[136:139]
	ds_write_b64 v161, v[22:23] offset:256
	v_mfma_f32_16x16x32_bf16 v[132:135], v[202:205], v[170:173], v[132:135]
	v_mfma_f32_16x16x32_bf16 v[128:131], v[206:209], v[170:173], v[128:131]
	s_waitcnt lgkmcnt(2)
	v_mfma_f32_16x16x32_bf16 v[124:127], v[244:247], v[182:185], v[124:127]
	ds_read_b128 v[170:173], v162 offset:41984
	v_mfma_f32_16x16x32_bf16 v[120:123], v[248:251], v[182:185], v[120:123]
	v_mfma_f32_16x16x32_bf16 v[116:119], v[202:205], v[182:185], v[116:119]
	v_mfma_f32_16x16x32_bf16 v[112:115], v[206:209], v[182:185], v[112:115]
	s_waitcnt lgkmcnt(2)
	v_mfma_f32_16x16x32_bf16 v[108:111], v[244:247], v[186:189], v[108:111]
	ds_read_b128 v[182:185], v162 offset:44032
	buffer_load_dwordx4 v[20:23], v160, s[16:19], s69 offen
	s_waitcnt vmcnt(11)
	v_cvt_pk_bf16_f32 v7, v6, v7
	v_cvt_pk_bf16_f32 v6, v4, v5
	v_mfma_f32_16x16x32_bf16 v[104:107], v[248:251], v[186:189], v[104:107]
	ds_write_b64 v161, v[6:7] offset:8960
	v_mfma_f32_16x16x32_bf16 v[100:103], v[202:205], v[186:189], v[100:103]
	v_mfma_f32_16x16x32_bf16 v[96:99], v[206:209], v[186:189], v[96:99]
	s_waitcnt lgkmcnt(2)
	v_mfma_f32_16x16x32_bf16 v[92:95], v[244:247], v[170:173], v[92:95]
	ds_read_b128 v[186:189], v162 offset:46080
	v_mfma_f32_16x16x32_bf16 v[88:91], v[248:251], v[170:173], v[88:91]
	v_mfma_f32_16x16x32_bf16 v[84:87], v[202:205], v[170:173], v[84:87]
	v_mfma_f32_16x16x32_bf16 v[80:83], v[206:209], v[170:173], v[80:83]
	s_waitcnt lgkmcnt(2)
	v_mfma_f32_16x16x32_bf16 v[76:79], v[244:247], v[182:185], v[76:79]
	ds_read_b128 v[252:255], v162 offset:48128
	buffer_load_dwordx4 v[4:7], v160, s[16:19], s74 offen
	s_waitcnt vmcnt(11)
	v_cvt_pk_bf16_f32 v11, v10, v11
	v_cvt_pk_bf16_f32 v10, v8, v9
	v_mfma_f32_16x16x32_bf16 v[72:75], v[248:251], v[182:185], v[72:75]
	ds_write_b64 v161, v[10:11] offset:17664
	v_mfma_f32_16x16x32_bf16 v[68:71], v[202:205], v[182:185], v[68:71]
	v_mfma_f32_16x16x32_bf16 v[64:67], v[206:209], v[182:185], v[64:67]
	s_waitcnt lgkmcnt(2)
	v_mfma_f32_16x16x32_bf16 v[60:63], v[244:247], v[186:189], v[60:63]
	buffer_load_dwordx4 v[8:11], v160, s[16:19], s75 offen
	s_waitcnt vmcnt(11)
	v_cvt_pk_bf16_f32 v19, v18, v19
	v_cvt_pk_bf16_f32 v18, v16, v17
	v_mfma_f32_16x16x32_bf16 v[56:59], v[248:251], v[186:189], v[56:59]
	ds_write_b64 v161, v[18:19] offset:26368
	v_mfma_f32_16x16x32_bf16 v[52:55], v[202:205], v[186:189], v[52:55]
	buffer_load_dwordx4 v[16:19], v160, s[16:19], s13 offen
	v_mfma_f32_16x16x32_bf16 v[48:51], v[206:209], v[186:189], v[48:51]
	s_add_i32 s12, s12, 2
	s_add_i32 s13, s13, 0x100000
	s_addk_i32 s45, 0x100
	s_cmp_ge_i32 s12, s30
	s_waitcnt vmcnt(8)
	s_waitcnt lgkmcnt(0)
	s_barrier
	s_cbranch_scc0 .LBB0_899

; #define G_DMA_A(kt, AO) do { G_DMA1(kt, AO, 0); G_DMA1(kt, AO, 1); G_DMA1(kt, AO, 2); G_DMA1(kt, AO, 3); if (MF == 9) G_DMA5(kt, AO); } while (0)
; #define G_ISSUE_B(kt) do { const unsigned _sb = (unsigned)(kt) * 4u * kstepB; \
;         _Pragma("unroll") for (int _i = 0; _i < 8; ++_i) sb[_i] = bload16(_i < 4 ? rsB0 : rsB1, vob, _sb + (_i & 3) * kstepB); } while (0)
; #define G_WRITE_B(BO) do { \
;         _Pragma("unroll") for (int _i = 0; _i < 8; ++_i) *(LAS u32x2*)(b_wr + (BO) + (_i & 3) * (16 * G_BSTRIDE) + (_i >> 2) * SLAB1) = pack4(__builtin_bit_cast(f32x4, sb[_i])); } while (0)
; #define G_ENDTILE(VM) do { asm volatile("s_waitcnt vmcnt(" #VM ")" ::: "memory"); \
;         asm volatile("s_waitcnt lgkmcnt(0)" ::: "memory"); __builtin_amdgcn_s_barrier(); asm volatile("" ::: "memory"); } while (0)
;     ...
;     __builtin_amdgcn_s_barrier();
;     G_DMA_A(0, G_A0); G_ISSUE_B(0); G_WRITE_B(G_B0);
;     __builtin_amdgcn_sched_barrier(0);
;     G_ISSUE_B(1);
;     __builtin_amdgcn_sched_barrier(0);
;     G_ENDTILE(8);
;     for (int ui = 0;; ++ui) {
; #pragma unroll
;         for (int m = 0; m < MF; ++m)
; #pragma unroll
;             for (int n = 0; n < 4; ++n) acc[m][n] = (f32x4){0.f, 0.f, 0.f, 0.f};
;         for (int t = 0; t < nt - 2; t += 2) {
;             G_TILE(G_A0, G_B0, true, G_B1, G_A1, t + 1, true, t + 2, (void)0);
.LBB0_1036:
	s_andn2_b64 vcc, exec, s[26:27]
	v_mov_b32_e32 v159, 0
	s_cbranch_vccnz .LBB0_1039
	s_mov_b32 s0, 0
	s_mov_b32 s1, 0x1e0000
	s_movk_i32 s4, 0x100
	s_mov_b32 m0, s64
	s_add_i32 s5, s4, 0xffffff80
	ds_read_b64_tr_b16 v[160:161], v178
	ds_read_b64_tr_b16 v[162:163], v179
	ds_read_b64_tr_b16 v[166:167], v179 offset:32
	ds_read_b128 v[168:171], v175
	ds_read_b64_tr_b16 v[164:165], v178 offset:32
	ds_read_b64_tr_b16 v[182:183], v178 offset:64
	ds_read_b64_tr_b16 v[186:187], v178 offset:96
	ds_read_b64_tr_b16 v[184:185], v179 offset:64
	ds_read_b64_tr_b16 v[188:189], v179 offset:96
	ds_read_b128 v[190:193], v175 offset:2048
	ds_read_b128 v[194:197], v175 offset:4096
	buffer_load_dwordx4 v176, s[16:19], s5 offen lds
	s_mov_b32 m0, s63
	s_waitcnt lgkmcnt(7)
	v_mfma_f32_16x16x32_bf16 v[156:159], v[160:163], v[168:171], 0
	buffer_load_dwordx4 v177, s[16:19], s5 offen lds
	s_waitcnt lgkmcnt(6)
	v_mfma_f32_16x16x32_bf16 v[152:155], v[164:167], v[168:171], 0
	s_waitcnt lgkmcnt(3)
	v_mfma_f32_16x16x32_bf16 v[148:151], v[182:185], v[168:171], 0
	s_waitcnt lgkmcnt(2)
	v_mfma_f32_16x16x32_bf16 v[144:147], v[186:189], v[168:171], 0
	s_waitcnt lgkmcnt(1)
	v_mfma_f32_16x16x32_bf16 v[140:143], v[160:163], v[190:193], 0
	s_mov_b32 m0, s62
	s_nop 0
	buffer_load_dwordx4 v180, s[16:19], s5 offen lds
	ds_read_b128 v[168:171], v175 offset:6144
	s_waitcnt vmcnt(10)
	v_cvt_pk_bf16_f32 v15, v14, v15
	v_cvt_pk_bf16_f32 v14, v12, v13
	v_mfma_f32_16x16x32_bf16 v[136:139], v[164:167], v[190:193], 0
	ds_write_b64 v174, v[14:15] offset:34816
	v_mfma_f32_16x16x32_bf16 v[132:135], v[182:185], v[190:193], 0
	s_mov_b32 m0, s61
	s_nop 0
	buffer_load_dwordx4 v181, s[16:19], s5 offen lds
	s_add_i32 s5, s1, 0xfff20000
	v_mfma_f32_16x16x32_bf16 v[128:131], v[186:189], v[190:193], 0
	s_waitcnt lgkmcnt(2)
	v_mfma_f32_16x16x32_bf16 v[124:127], v[160:163], v[194:197], 0
	ds_read_b128 v[190:193], v175 offset:8192
	v_mfma_f32_16x16x32_bf16 v[120:123], v[164:167], v[194:197], 0
	v_mfma_f32_16x16x32_bf16 v[116:119], v[182:185], v[194:197], 0
	v_mfma_f32_16x16x32_bf16 v[112:115], v[186:189], v[194:197], 0
	s_waitcnt lgkmcnt(2)
	v_mfma_f32_16x16x32_bf16 v[108:111], v[160:163], v[168:171], 0
	ds_read_b128 v[194:197], v175 offset:10240
	buffer_load_dwordx4 v[12:15], v173, s[8:11], s5 offen
	s_waitcnt vmcnt(10)
	v_cvt_pk_bf16_f32 v31, v30, v31
	v_cvt_pk_bf16_f32 v30, v28, v29
	v_mfma_f32_16x16x32_bf16 v[104:107], v[164:167], v[168:171], 0
	ds_write_b64 v174, v[30:31] offset:43520
	v_mfma_f32_16x16x32_bf16 v[100:103], v[182:185], v[168:171], 0
	v_mfma_f32_16x16x32_bf16 v[96:99], v[186:189], v[168:171], 0
	s_add_i32 s20, s1, 0xfff40000
	s_waitcnt lgkmcnt(2)
	v_mfma_f32_16x16x32_bf16 v[92:95], v[160:163], v[190:193], 0
	ds_read_b128 v[168:171], v175 offset:12288
	v_mfma_f32_16x16x32_bf16 v[88:91], v[164:167], v[190:193], 0
	v_mfma_f32_16x16x32_bf16 v[84:87], v[182:185], v[190:193], 0
	v_mfma_f32_16x16x32_bf16 v[80:83], v[186:189], v[190:193], 0
	s_waitcnt lgkmcnt(2)
	v_mfma_f32_16x16x32_bf16 v[76:79], v[160:163], v[194:197], 0
	ds_read_b128 v[190:193], v175 offset:14336
	v_cvt_pk_bf16_f32 v7, v6, v7
	v_cvt_pk_bf16_f32 v6, v4, v5
	v_mfma_f32_16x16x32_bf16 v[72:75], v[164:167], v[194:197], 0
	ds_write_b64 v174, v[6:7] offset:52224
	v_mfma_f32_16x16x32_bf16 v[68:71], v[182:185], v[194:197], 0
	v_mfma_f32_16x16x32_bf16 v[64:67], v[186:189], v[194:197], 0
	s_add_i32 s21, s1, 0xfff60000
	buffer_load_dwordx4 v[28:31], v173, s[8:11], s20 offen
	s_waitcnt lgkmcnt(2)
	v_mfma_f32_16x16x32_bf16 v[60:63], v[160:163], v[168:171], 0
	ds_read_b128 v[194:197], v175 offset:1024
	v_mfma_f32_16x16x32_bf16 v[56:59], v[164:167], v[168:171], 0
	v_mfma_f32_16x16x32_bf16 v[52:55], v[182:185], v[168:171], 0
	v_mfma_f32_16x16x32_bf16 v[48:51], v[186:189], v[168:171], 0
	s_waitcnt lgkmcnt(2)
	v_mfma_f32_16x16x32_bf16 v[44:47], v[160:163], v[190:193], 0
	ds_read_b128 v[160:163], v175 offset:3072
	buffer_load_dwordx4 v[4:7], v173, s[8:11], s21 offen
	s_waitcnt vmcnt(11)
	v_cvt_pk_bf16_f32 v27, v26, v27
	v_cvt_pk_bf16_f32 v26, v24, v25
	v_mfma_f32_16x16x32_bf16 v[40:43], v[164:167], v[190:193], 0
	ds_read_b64_tr_b16 v[244:245], v178 offset:17408
	ds_read_b64_tr_b16 v[248:249], v178 offset:17440
	ds_read_b64_tr_b16 v[198:199], v178 offset:17472
	ds_read_b64_tr_b16 v[202:203], v178 offset:17504
	ds_read_b64_tr_b16 v[246:247], v179 offset:17408
	ds_read_b64_tr_b16 v[250:251], v179 offset:17440
	ds_read_b64_tr_b16 v[200:201], v179 offset:17472
	ds_read_b64_tr_b16 v[204:205], v179 offset:17504
	ds_write_b64 v174, v[26:27] offset:60928
	v_mfma_f32_16x16x32_bf16 v[36:39], v[182:185], v[190:193], 0
	v_mfma_f32_16x16x32_bf16 v[32:35], v[186:189], v[190:193], 0
	s_add_i32 s22, s1, 0xfff80000
	s_waitcnt lgkmcnt(4)
	v_mfma_f32_16x16x32_bf16 v[156:159], v[244:247], v[194:197], v[156:159]
	ds_read_b128 v[182:185], v175 offset:5120
	s_waitcnt lgkmcnt(4)
	v_mfma_f32_16x16x32_bf16 v[152:155], v[248:251], v[194:197], v[152:155]
	s_waitcnt lgkmcnt(3)
	v_mfma_f32_16x16x32_bf16 v[148:151], v[198:201], v[194:197], v[148:151]
	s_waitcnt lgkmcnt(2)
	v_mfma_f32_16x16x32_bf16 v[144:147], v[202:205], v[194:197], v[144:147]
	v_mfma_f32_16x16x32_bf16 v[140:143], v[244:247], v[160:163], v[140:143]
	ds_read_b128 v[186:189], v175 offset:7168
	buffer_load_dwordx4 v[24:27], v173, s[8:11], s22 offen
	s_waitcnt vmcnt(11)
	v_cvt_pk_bf16_f32 v23, v22, v23
	v_cvt_pk_bf16_f32 v22, v20, v21
	v_mfma_f32_16x16x32_bf16 v[136:139], v[248:251], v[160:163], v[136:139]
	ds_write_b64 v174, v[22:23] offset:35072
	v_mfma_f32_16x16x32_bf16 v[132:135], v[198:201], v[160:163], v[132:135]
	v_mfma_f32_16x16x32_bf16 v[128:131], v[202:205], v[160:163], v[128:131]
	s_waitcnt lgkmcnt(2)
	v_mfma_f32_16x16x32_bf16 v[124:127], v[244:247], v[182:185], v[124:127]
	ds_read_b128 v[160:163], v175 offset:9216
	v_mfma_f32_16x16x32_bf16 v[120:123], v[248:251], v[182:185], v[120:123]
	v_mfma_f32_16x16x32_bf16 v[116:119], v[198:201], v[182:185], v[116:119]
	v_mfma_f32_16x16x32_bf16 v[112:115], v[202:205], v[182:185], v[112:115]
	s_waitcnt lgkmcnt(2)
	v_mfma_f32_16x16x32_bf16 v[108:111], v[244:247], v[186:189], v[108:111]
	ds_read_b128 v[182:185], v175 offset:11264
	buffer_load_dwordx4 v[20:23], v173, s[12:15], s5 offen
	s_waitcnt vmcnt(10)
	v_cvt_pk_bf16_f32 v11, v10, v11
	v_cvt_pk_bf16_f32 v10, v8, v9
	v_mfma_f32_16x16x32_bf16 v[104:107], v[248:251], v[186:189], v[104:107]
	ds_write_b64 v174, v[10:11] offset:43776
	v_mfma_f32_16x16x32_bf16 v[100:103], v[198:201], v[186:189], v[100:103]
	v_mfma_f32_16x16x32_bf16 v[96:99], v[202:205], v[186:189], v[96:99]
	s_waitcnt lgkmcnt(2)
	v_mfma_f32_16x16x32_bf16 v[92:95], v[244:247], v[160:163], v[92:95]
	ds_read_b128 v[186:189], v175 offset:13312
	v_mfma_f32_16x16x32_bf16 v[88:91], v[248:251], v[160:163], v[88:91]
	v_mfma_f32_16x16x32_bf16 v[84:87], v[198:201], v[160:163], v[84:87]
	v_mfma_f32_16x16x32_bf16 v[80:83], v[202:205], v[160:163], v[80:83]
	s_waitcnt lgkmcnt(2)
	v_mfma_f32_16x16x32_bf16 v[76:79], v[244:247], v[182:185], v[76:79]
	ds_read_b128 v[252:255], v175 offset:15360
	v_cvt_pk_bf16_f32 v3, v2, v3
	v_cvt_pk_bf16_f32 v2, v0, v1
	v_mfma_f32_16x16x32_bf16 v[72:75], v[248:251], v[182:185], v[72:75]
	ds_write_b64 v174, v[2:3] offset:52480
	v_mfma_f32_16x16x32_bf16 v[68:71], v[198:201], v[182:185], v[68:71]
	v_mfma_f32_16x16x32_bf16 v[64:67], v[202:205], v[182:185], v[64:67]
	buffer_load_dwordx4 v[8:11], v173, s[12:15], s20 offen
	s_waitcnt lgkmcnt(2)
	v_mfma_f32_16x16x32_bf16 v[60:63], v[244:247], v[186:189], v[60:63]
	buffer_load_dwordx4 v[0:3], v173, s[12:15], s21 offen
	s_waitcnt vmcnt(11)
	v_cvt_pk_bf16_f32 v19, v18, v19
	v_cvt_pk_bf16_f32 v18, v16, v17
	v_mfma_f32_16x16x32_bf16 v[56:59], v[248:251], v[186:189], v[56:59]
	ds_write_b64 v174, v[18:19] offset:61184
	v_mfma_f32_16x16x32_bf16 v[52:55], v[198:201], v[186:189], v[52:55]
	buffer_load_dwordx4 v[16:19], v173, s[12:15], s22 offen
	v_mfma_f32_16x16x32_bf16 v[48:51], v[202:205], v[186:189], v[48:51]
	s_waitcnt vmcnt(8)
	s_mov_b32 m0, s45
	s_waitcnt lgkmcnt(0)
	s_barrier
	ds_read_b64_tr_b16 v[160:161], v178 offset:34816
	ds_read_b64_tr_b16 v[162:163], v179 offset:34816
	ds_read_b64_tr_b16 v[166:167], v179 offset:34848
	ds_read_b128 v[168:171], v175 offset:32768
	ds_read_b64_tr_b16 v[164:165], v178 offset:34848
	ds_read_b64_tr_b16 v[182:183], v178 offset:34880
	ds_read_b64_tr_b16 v[186:187], v178 offset:34912
	ds_read_b64_tr_b16 v[184:185], v179 offset:34880
	ds_read_b64_tr_b16 v[188:189], v179 offset:34912
	ds_read_b128 v[190:193], v175 offset:34816
	ds_read_b128 v[194:197], v175 offset:36864
	buffer_load_dwordx4 v176, s[16:19], s4 offen lds
	s_mov_b32 m0, s53
	v_mfma_f32_16x16x32_bf16 v[44:47], v[244:247], v[252:255], v[44:47]
	v_mfma_f32_16x16x32_bf16 v[40:43], v[248:251], v[252:255], v[40:43]
	v_mfma_f32_16x16x32_bf16 v[36:39], v[198:201], v[252:255], v[36:39]
	v_mfma_f32_16x16x32_bf16 v[32:35], v[202:205], v[252:255], v[32:35]
	s_waitcnt lgkmcnt(7)
	v_mfma_f32_16x16x32_bf16 v[156:159], v[160:163], v[168:171], v[156:159]
	buffer_load_dwordx4 v177, s[16:19], s4 offen lds
	s_add_i32 s5, s1, 0xfffa0000
	s_waitcnt lgkmcnt(6)
	v_mfma_f32_16x16x32_bf16 v[152:155], v[164:167], v[168:171], v[152:155]
	s_waitcnt lgkmcnt(3)
	v_mfma_f32_16x16x32_bf16 v[148:151], v[182:185], v[168:171], v[148:151]
	s_waitcnt lgkmcnt(2)
	v_mfma_f32_16x16x32_bf16 v[144:147], v[186:189], v[168:171], v[144:147]
	s_waitcnt lgkmcnt(1)
	v_mfma_f32_16x16x32_bf16 v[140:143], v[160:163], v[190:193], v[140:143]
	s_mov_b32 m0, s54
	s_nop 0
	buffer_load_dwordx4 v180, s[16:19], s4 offen lds
	ds_read_b128 v[168:171], v175 offset:38912
	s_waitcnt vmcnt(10)
	v_cvt_pk_bf16_f32 v15, v14, v15
	v_cvt_pk_bf16_f32 v14, v12, v13
	v_mfma_f32_16x16x32_bf16 v[136:139], v[164:167], v[190:193], v[136:139]
	ds_write_b64 v174, v[14:15]
	v_mfma_f32_16x16x32_bf16 v[132:135], v[182:185], v[190:193], v[132:135]
	s_mov_b32 m0, s55
	s_nop 0
	buffer_load_dwordx4 v181, s[16:19], s4 offen lds
	v_mfma_f32_16x16x32_bf16 v[128:131], v[186:189], v[190:193], v[128:131]
	s_waitcnt lgkmcnt(2)
	v_mfma_f32_16x16x32_bf16 v[124:127], v[160:163], v[194:197], v[124:127]
	ds_read_b128 v[190:193], v175 offset:40960
	v_mfma_f32_16x16x32_bf16 v[120:123], v[164:167], v[194:197], v[120:123]
	v_mfma_f32_16x16x32_bf16 v[116:119], v[182:185], v[194:197], v[116:119]
	v_mfma_f32_16x16x32_bf16 v[112:115], v[186:189], v[194:197], v[112:115]
	s_waitcnt lgkmcnt(2)
	v_mfma_f32_16x16x32_bf16 v[108:111], v[160:163], v[168:171], v[108:111]
	ds_read_b128 v[194:197], v175 offset:43008
	buffer_load_dwordx4 v[12:15], v173, s[8:11], s5 offen
	s_waitcnt vmcnt(11)
	v_cvt_pk_bf16_f32 v31, v30, v31
	v_cvt_pk_bf16_f32 v30, v28, v29
	v_mfma_f32_16x16x32_bf16 v[104:107], v[164:167], v[168:171], v[104:107]
	ds_write_b64 v174, v[30:31] offset:8704
	v_mfma_f32_16x16x32_bf16 v[100:103], v[182:185], v[168:171], v[100:103]
	v_mfma_f32_16x16x32_bf16 v[96:99], v[186:189], v[168:171], v[96:99]
	s_add_i32 s20, s1, 0xfffc0000
	s_waitcnt lgkmcnt(2)
	v_mfma_f32_16x16x32_bf16 v[92:95], v[160:163], v[190:193], v[92:95]
	ds_read_b128 v[168:171], v175 offset:45056
	v_mfma_f32_16x16x32_bf16 v[88:91], v[164:167], v[190:193], v[88:91]
	v_mfma_f32_16x16x32_bf16 v[84:87], v[182:185], v[190:193], v[84:87]
	v_mfma_f32_16x16x32_bf16 v[80:83], v[186:189], v[190:193], v[80:83]
	s_waitcnt lgkmcnt(2)
; #define G_ENDTILE(VM) do { asm volatile("s_waitcnt vmcnt(" #VM ")" ::: "memory"); \
;         asm volatile("s_waitcnt lgkmcnt(0)" ::: "memory"); __builtin_amdgcn_s_barrier(); asm volatile("" ::: "memory"); } while (0)
;     ...
;         for (int t = 0; t < nt - 2; t += 2) {
;             G_TILE(G_A0, G_B0, true, G_B1, G_A1, t + 1, true, t + 2, (void)0);
;             G_ENDTILE(8);
;             G_TILE(G_A1, G_B1, true, G_B0, G_A0, t + 2, true, t + 3, (void)0);
;             G_ENDTILE(8);
;         }
	v_mfma_f32_16x16x32_bf16 v[76:79], v[160:163], v[194:197], v[76:79]
	ds_read_b128 v[190:193], v175 offset:47104
	buffer_load_dwordx4 v[28:31], v173, s[8:11], s20 offen
	s_waitcnt vmcnt(11)
	v_cvt_pk_bf16_f32 v7, v6, v7
	v_cvt_pk_bf16_f32 v6, v4, v5
	v_mfma_f32_16x16x32_bf16 v[72:75], v[164:167], v[194:197], v[72:75]
	ds_write_b64 v174, v[6:7] offset:17408
	v_mfma_f32_16x16x32_bf16 v[68:71], v[182:185], v[194:197], v[68:71]
	v_mfma_f32_16x16x32_bf16 v[64:67], v[186:189], v[194:197], v[64:67]
	s_add_i32 s21, s1, 0xfffe0000
	s_waitcnt lgkmcnt(2)
	v_mfma_f32_16x16x32_bf16 v[60:63], v[160:163], v[168:171], v[60:63]
	ds_read_b128 v[194:197], v175 offset:33792
	v_mfma_f32_16x16x32_bf16 v[56:59], v[164:167], v[168:171], v[56:59]
	v_mfma_f32_16x16x32_bf16 v[52:55], v[182:185], v[168:171], v[52:55]
	v_mfma_f32_16x16x32_bf16 v[48:51], v[186:189], v[168:171], v[48:51]
	s_waitcnt lgkmcnt(2)
	v_mfma_f32_16x16x32_bf16 v[44:47], v[160:163], v[190:193], v[44:47]
	ds_read_b128 v[160:163], v175 offset:35840
	buffer_load_dwordx4 v[4:7], v173, s[8:11], s21 offen
	s_waitcnt vmcnt(11)
	v_cvt_pk_bf16_f32 v27, v26, v27
	v_cvt_pk_bf16_f32 v26, v24, v25
	v_mfma_f32_16x16x32_bf16 v[40:43], v[164:167], v[190:193], v[40:43]
	ds_read_b64_tr_b16 v[244:245], v178 offset:52224
	ds_read_b64_tr_b16 v[248:249], v178 offset:52256
	ds_read_b64_tr_b16 v[198:199], v178 offset:52288
	ds_read_b64_tr_b16 v[202:203], v178 offset:52320
	ds_read_b64_tr_b16 v[246:247], v179 offset:52224
	ds_read_b64_tr_b16 v[250:251], v179 offset:52256
	ds_read_b64_tr_b16 v[200:201], v179 offset:52288
	ds_read_b64_tr_b16 v[204:205], v179 offset:52320
	ds_write_b64 v174, v[26:27] offset:26112
	v_mfma_f32_16x16x32_bf16 v[36:39], v[182:185], v[190:193], v[36:39]
	v_mfma_f32_16x16x32_bf16 v[32:35], v[186:189], v[190:193], v[32:35]
	s_waitcnt lgkmcnt(4)
	v_mfma_f32_16x16x32_bf16 v[156:159], v[244:247], v[194:197], v[156:159]
	ds_read_b128 v[182:185], v175 offset:37888
	s_waitcnt lgkmcnt(4)
	v_mfma_f32_16x16x32_bf16 v[152:155], v[248:251], v[194:197], v[152:155]
	s_waitcnt lgkmcnt(3)
	v_mfma_f32_16x16x32_bf16 v[148:151], v[198:201], v[194:197], v[148:151]
	s_waitcnt lgkmcnt(2)
	v_mfma_f32_16x16x32_bf16 v[144:147], v[202:205], v[194:197], v[144:147]
	v_mfma_f32_16x16x32_bf16 v[140:143], v[244:247], v[160:163], v[140:143]
	ds_read_b128 v[186:189], v175 offset:39936
	buffer_load_dwordx4 v[24:27], v173, s[8:11], s1 offen
	s_waitcnt vmcnt(11)
	v_cvt_pk_bf16_f32 v23, v22, v23
	v_cvt_pk_bf16_f32 v22, v20, v21
	v_mfma_f32_16x16x32_bf16 v[136:139], v[248:251], v[160:163], v[136:139]
	ds_write_b64 v174, v[22:23] offset:256
	v_mfma_f32_16x16x32_bf16 v[132:135], v[198:201], v[160:163], v[132:135]
	v_mfma_f32_16x16x32_bf16 v[128:131], v[202:205], v[160:163], v[128:131]
	s_waitcnt lgkmcnt(2)
	v_mfma_f32_16x16x32_bf16 v[124:127], v[244:247], v[182:185], v[124:127]
	ds_read_b128 v[160:163], v175 offset:41984
	v_mfma_f32_16x16x32_bf16 v[120:123], v[248:251], v[182:185], v[120:123]
	v_mfma_f32_16x16x32_bf16 v[116:119], v[198:201], v[182:185], v[116:119]
	v_mfma_f32_16x16x32_bf16 v[112:115], v[202:205], v[182:185], v[112:115]
	s_waitcnt lgkmcnt(2)
	v_mfma_f32_16x16x32_bf16 v[108:111], v[244:247], v[186:189], v[108:111]
	ds_read_b128 v[182:185], v175 offset:44032
	buffer_load_dwordx4 v[20:23], v173, s[12:15], s5 offen
	s_waitcnt vmcnt(11)
	v_cvt_pk_bf16_f32 v11, v10, v11
	v_cvt_pk_bf16_f32 v10, v8, v9
	v_mfma_f32_16x16x32_bf16 v[104:107], v[248:251], v[186:189], v[104:107]
	ds_write_b64 v174, v[10:11] offset:8960
	v_mfma_f32_16x16x32_bf16 v[100:103], v[198:201], v[186:189], v[100:103]
	v_mfma_f32_16x16x32_bf16 v[96:99], v[202:205], v[186:189], v[96:99]
	s_waitcnt lgkmcnt(2)
	v_mfma_f32_16x16x32_bf16 v[92:95], v[244:247], v[160:163], v[92:95]
	ds_read_b128 v[186:189], v175 offset:46080
	v_mfma_f32_16x16x32_bf16 v[88:91], v[248:251], v[160:163], v[88:91]
	v_mfma_f32_16x16x32_bf16 v[84:87], v[198:201], v[160:163], v[84:87]
	v_mfma_f32_16x16x32_bf16 v[80:83], v[202:205], v[160:163], v[80:83]
	s_waitcnt lgkmcnt(2)
	v_mfma_f32_16x16x32_bf16 v[76:79], v[244:247], v[182:185], v[76:79]
	ds_read_b128 v[252:255], v175 offset:48128
	buffer_load_dwordx4 v[8:11], v173, s[12:15], s20 offen
	s_waitcnt vmcnt(11)
	v_cvt_pk_bf16_f32 v3, v2, v3
	v_cvt_pk_bf16_f32 v2, v0, v1
	v_mfma_f32_16x16x32_bf16 v[72:75], v[248:251], v[182:185], v[72:75]
	ds_write_b64 v174, v[2:3] offset:17664
	v_mfma_f32_16x16x32_bf16 v[68:71], v[198:201], v[182:185], v[68:71]
	v_mfma_f32_16x16x32_bf16 v[64:67], v[202:205], v[182:185], v[64:67]
	s_waitcnt lgkmcnt(2)
	v_mfma_f32_16x16x32_bf16 v[60:63], v[244:247], v[186:189], v[60:63]
	buffer_load_dwordx4 v[0:3], v173, s[12:15], s21 offen
	s_waitcnt vmcnt(11)
	v_cvt_pk_bf16_f32 v19, v18, v19
	v_cvt_pk_bf16_f32 v18, v16, v17
	v_mfma_f32_16x16x32_bf16 v[56:59], v[248:251], v[186:189], v[56:59]
	ds_write_b64 v174, v[18:19] offset:26368
	v_mfma_f32_16x16x32_bf16 v[52:55], v[198:201], v[186:189], v[52:55]
	buffer_load_dwordx4 v[16:19], v173, s[12:15], s1 offen
	v_mfma_f32_16x16x32_bf16 v[48:51], v[202:205], v[186:189], v[48:51]
	s_add_i32 s0, s0, 2
	s_add_i32 s1, s1, 0x100000
	s_addk_i32 s4, 0x100
	s_cmp_ge_i32 s0, s60
	s_waitcnt vmcnt(8)
	s_waitcnt lgkmcnt(0)
	s_barrier
	s_cbranch_scc1 .Lflush_P8
;     ...
;         for (int t = 0; t < nt - 2; t += 2) {
;             G_TILE(G_A0, G_B0, true, G_B1, G_A1, t + 1, true, t + 2, (void)0);
.LBB0_1038:
	s_mov_b32 m0, s64
	s_add_i32 s5, s4, 0xffffff80
	ds_read_b64_tr_b16 v[160:161], v178
	ds_read_b64_tr_b16 v[162:163], v179
	ds_read_b64_tr_b16 v[166:167], v179 offset:32
	ds_read_b128 v[168:171], v175
	ds_read_b64_tr_b16 v[164:165], v178 offset:32
	ds_read_b64_tr_b16 v[182:183], v178 offset:64
	ds_read_b64_tr_b16 v[186:187], v178 offset:96
	ds_read_b64_tr_b16 v[184:185], v179 offset:64
	ds_read_b64_tr_b16 v[188:189], v179 offset:96
	ds_read_b128 v[190:193], v175 offset:2048
	ds_read_b128 v[194:197], v175 offset:4096
	buffer_load_dwordx4 v176, s[16:19], s5 offen lds
	s_mov_b32 m0, s63
	v_mfma_f32_16x16x32_bf16 v[44:47], v[244:247], v[252:255], v[44:47]
	v_mfma_f32_16x16x32_bf16 v[40:43], v[248:251], v[252:255], v[40:43]
	v_mfma_f32_16x16x32_bf16 v[36:39], v[198:201], v[252:255], v[36:39]
	v_mfma_f32_16x16x32_bf16 v[32:35], v[202:205], v[252:255], v[32:35]
	s_waitcnt lgkmcnt(7)
	v_mfma_f32_16x16x32_bf16 v[156:159], v[160:163], v[168:171], v[156:159]
	buffer_load_dwordx4 v177, s[16:19], s5 offen lds
	s_waitcnt lgkmcnt(6)
	v_mfma_f32_16x16x32_bf16 v[152:155], v[164:167], v[168:171], v[152:155]
	s_waitcnt lgkmcnt(3)
	v_mfma_f32_16x16x32_bf16 v[148:151], v[182:185], v[168:171], v[148:151]
	s_waitcnt lgkmcnt(2)
	v_mfma_f32_16x16x32_bf16 v[144:147], v[186:189], v[168:171], v[144:147]
	s_waitcnt lgkmcnt(1)
	v_mfma_f32_16x16x32_bf16 v[140:143], v[160:163], v[190:193], v[140:143]
	s_mov_b32 m0, s62
	s_nop 0
	buffer_load_dwordx4 v180, s[16:19], s5 offen lds
	ds_read_b128 v[168:171], v175 offset:6144
	s_waitcnt vmcnt(10)
	v_cvt_pk_bf16_f32 v15, v14, v15
	v_cvt_pk_bf16_f32 v14, v12, v13
	v_mfma_f32_16x16x32_bf16 v[136:139], v[164:167], v[190:193], v[136:139]
	ds_write_b64 v174, v[14:15] offset:34816
	v_mfma_f32_16x16x32_bf16 v[132:135], v[182:185], v[190:193], v[132:135]
	s_mov_b32 m0, s61
	s_nop 0
	buffer_load_dwordx4 v181, s[16:19], s5 offen lds
	s_add_i32 s5, s1, 0xfff20000
	v_mfma_f32_16x16x32_bf16 v[128:131], v[186:189], v[190:193], v[128:131]
	s_waitcnt lgkmcnt(2)
	v_mfma_f32_16x16x32_bf16 v[124:127], v[160:163], v[194:197], v[124:127]
	ds_read_b128 v[190:193], v175 offset:8192
	v_mfma_f32_16x16x32_bf16 v[120:123], v[164:167], v[194:197], v[120:123]
	v_mfma_f32_16x16x32_bf16 v[116:119], v[182:185], v[194:197], v[116:119]
	v_mfma_f32_16x16x32_bf16 v[112:115], v[186:189], v[194:197], v[112:115]
	s_waitcnt lgkmcnt(2)
	v_mfma_f32_16x16x32_bf16 v[108:111], v[160:163], v[168:171], v[108:111]
	ds_read_b128 v[194:197], v175 offset:10240
	buffer_load_dwordx4 v[12:15], v173, s[8:11], s5 offen
	s_waitcnt vmcnt(10)
	v_cvt_pk_bf16_f32 v31, v30, v31
	v_cvt_pk_bf16_f32 v30, v28, v29
	v_mfma_f32_16x16x32_bf16 v[104:107], v[164:167], v[168:171], v[104:107]
	ds_write_b64 v174, v[30:31] offset:43520
	v_mfma_f32_16x16x32_bf16 v[100:103], v[182:185], v[168:171], v[100:103]
	v_mfma_f32_16x16x32_bf16 v[96:99], v[186:189], v[168:171], v[96:99]
	s_add_i32 s20, s1, 0xfff40000
	s_waitcnt lgkmcnt(2)
	v_mfma_f32_16x16x32_bf16 v[92:95], v[160:163], v[190:193], v[92:95]
	ds_read_b128 v[168:171], v175 offset:12288
	v_mfma_f32_16x16x32_bf16 v[88:91], v[164:167], v[190:193], v[88:91]
	v_mfma_f32_16x16x32_bf16 v[84:87], v[182:185], v[190:193], v[84:87]
	v_mfma_f32_16x16x32_bf16 v[80:83], v[186:189], v[190:193], v[80:83]
	s_waitcnt lgkmcnt(2)
	v_mfma_f32_16x16x32_bf16 v[76:79], v[160:163], v[194:197], v[76:79]
	ds_read_b128 v[190:193], v175 offset:14336
	v_cvt_pk_bf16_f32 v7, v6, v7
	v_cvt_pk_bf16_f32 v6, v4, v5
	v_mfma_f32_16x16x32_bf16 v[72:75], v[164:167], v[194:197], v[72:75]
	ds_write_b64 v174, v[6:7] offset:52224
	v_mfma_f32_16x16x32_bf16 v[68:71], v[182:185], v[194:197], v[68:71]
	v_mfma_f32_16x16x32_bf16 v[64:67], v[186:189], v[194:197], v[64:67]
	s_add_i32 s21, s1, 0xfff60000
	buffer_load_dwordx4 v[28:31], v173, s[8:11], s20 offen
	s_waitcnt lgkmcnt(2)
	v_mfma_f32_16x16x32_bf16 v[60:63], v[160:163], v[168:171], v[60:63]
	ds_read_b128 v[194:197], v175 offset:1024
	v_mfma_f32_16x16x32_bf16 v[56:59], v[164:167], v[168:171], v[56:59]
	v_mfma_f32_16x16x32_bf16 v[52:55], v[182:185], v[168:171], v[52:55]
	v_mfma_f32_16x16x32_bf16 v[48:51], v[186:189], v[168:171], v[48:51]
	s_waitcnt lgkmcnt(2)
	v_mfma_f32_16x16x32_bf16 v[44:47], v[160:163], v[190:193], v[44:47]
	ds_read_b128 v[160:163], v175 offset:3072
	buffer_load_dwordx4 v[4:7], v173, s[8:11], s21 offen
	s_waitcnt vmcnt(11)
	v_cvt_pk_bf16_f32 v27, v26, v27
	v_cvt_pk_bf16_f32 v26, v24, v25
	v_mfma_f32_16x16x32_bf16 v[40:43], v[164:167], v[190:193], v[40:43]
	ds_read_b64_tr_b16 v[244:245], v178 offset:17408
	ds_read_b64_tr_b16 v[248:249], v178 offset:17440
	ds_read_b64_tr_b16 v[198:199], v178 offset:17472
	ds_read_b64_tr_b16 v[202:203], v178 offset:17504
	ds_read_b64_tr_b16 v[246:247], v179 offset:17408
	ds_read_b64_tr_b16 v[250:251], v179 offset:17440
	ds_read_b64_tr_b16 v[200:201], v179 offset:17472
	ds_read_b64_tr_b16 v[204:205], v179 offset:17504
	ds_write_b64 v174, v[26:27] offset:60928
	v_mfma_f32_16x16x32_bf16 v[36:39], v[182:185], v[190:193], v[36:39]
	v_mfma_f32_16x16x32_bf16 v[32:35], v[186:189], v[190:193], v[32:35]
	s_add_i32 s22, s1, 0xfff80000
	s_waitcnt lgkmcnt(4)
	v_mfma_f32_16x16x32_bf16 v[156:159], v[244:247], v[194:197], v[156:159]
	ds_read_b128 v[182:185], v175 offset:5120
	s_waitcnt lgkmcnt(4)
	v_mfma_f32_16x16x32_bf16 v[152:155], v[248:251], v[194:197], v[152:155]
	s_waitcnt lgkmcnt(3)
	v_mfma_f32_16x16x32_bf16 v[148:151], v[198:201], v[194:197], v[148:151]
	s_waitcnt lgkmcnt(2)
	v_mfma_f32_16x16x32_bf16 v[144:147], v[202:205], v[194:197], v[144:147]
	v_mfma_f32_16x16x32_bf16 v[140:143], v[244:247], v[160:163], v[140:143]
	ds_read_b128 v[186:189], v175 offset:7168
	buffer_load_dwordx4 v[24:27], v173, s[8:11], s22 offen
	s_waitcnt vmcnt(11)
	v_cvt_pk_bf16_f32 v23, v22, v23
	v_cvt_pk_bf16_f32 v22, v20, v21
	v_mfma_f32_16x16x32_bf16 v[136:139], v[248:251], v[160:163], v[136:139]
	ds_write_b64 v174, v[22:23] offset:35072
	v_mfma_f32_16x16x32_bf16 v[132:135], v[198:201], v[160:163], v[132:135]
	v_mfma_f32_16x16x32_bf16 v[128:131], v[202:205], v[160:163], v[128:131]
	s_waitcnt lgkmcnt(2)
	v_mfma_f32_16x16x32_bf16 v[124:127], v[244:247], v[182:185], v[124:127]
	ds_read_b128 v[160:163], v175 offset:9216
	v_mfma_f32_16x16x32_bf16 v[120:123], v[248:251], v[182:185], v[120:123]
	v_mfma_f32_16x16x32_bf16 v[116:119], v[198:201], v[182:185], v[116:119]
	v_mfma_f32_16x16x32_bf16 v[112:115], v[202:205], v[182:185], v[112:115]
	s_waitcnt lgkmcnt(2)
	v_mfma_f32_16x16x32_bf16 v[108:111], v[244:247], v[186:189], v[108:111]
	ds_read_b128 v[182:185], v175 offset:11264
	buffer_load_dwordx4 v[20:23], v173, s[12:15], s5 offen
	s_waitcnt vmcnt(10)
	v_cvt_pk_bf16_f32 v11, v10, v11
	v_cvt_pk_bf16_f32 v10, v8, v9
	v_mfma_f32_16x16x32_bf16 v[104:107], v[248:251], v[186:189], v[104:107]
	ds_write_b64 v174, v[10:11] offset:43776
	v_mfma_f32_16x16x32_bf16 v[100:103], v[198:201], v[186:189], v[100:103]
	v_mfma_f32_16x16x32_bf16 v[96:99], v[202:205], v[186:189], v[96:99]
	s_waitcnt lgkmcnt(2)
	v_mfma_f32_16x16x32_bf16 v[92:95], v[244:247], v[160:163], v[92:95]
	ds_read_b128 v[186:189], v175 offset:13312
	v_mfma_f32_16x16x32_bf16 v[88:91], v[248:251], v[160:163], v[88:91]
	v_mfma_f32_16x16x32_bf16 v[84:87], v[198:201], v[160:163], v[84:87]
	v_mfma_f32_16x16x32_bf16 v[80:83], v[202:205], v[160:163], v[80:83]
	s_waitcnt lgkmcnt(2)
	v_mfma_f32_16x16x32_bf16 v[76:79], v[244:247], v[182:185], v[76:79]
	ds_read_b128 v[252:255], v175 offset:15360
	v_cvt_pk_bf16_f32 v3, v2, v3
	v_cvt_pk_bf16_f32 v2, v0, v1
	v_mfma_f32_16x16x32_bf16 v[72:75], v[248:251], v[182:185], v[72:75]
	ds_write_b64 v174, v[2:3] offset:52480
	v_mfma_f32_16x16x32_bf16 v[68:71], v[198:201], v[182:185], v[68:71]
	v_mfma_f32_16x16x32_bf16 v[64:67], v[202:205], v[182:185], v[64:67]
	buffer_load_dwordx4 v[8:11], v173, s[12:15], s20 offen
	s_waitcnt lgkmcnt(2)
	v_mfma_f32_16x16x32_bf16 v[60:63], v[244:247], v[186:189], v[60:63]
	buffer_load_dwordx4 v[0:3], v173, s[12:15], s21 offen
	s_waitcnt vmcnt(11)
	v_cvt_pk_bf16_f32 v19, v18, v19
	v_cvt_pk_bf16_f32 v18, v16, v17
	v_mfma_f32_16x16x32_bf16 v[56:59], v[248:251], v[186:189], v[56:59]
	ds_write_b64 v174, v[18:19] offset:61184
	v_mfma_f32_16x16x32_bf16 v[52:55], v[198:201], v[186:189], v[52:55]
	buffer_load_dwordx4 v[16:19], v173, s[12:15], s22 offen
	v_mfma_f32_16x16x32_bf16 v[48:51], v[202:205], v[186:189], v[48:51]
	s_waitcnt vmcnt(8)
	s_mov_b32 m0, s45
	s_waitcnt lgkmcnt(0)
	s_barrier
	ds_read_b64_tr_b16 v[160:161], v178 offset:34816
	ds_read_b64_tr_b16 v[162:163], v179 offset:34816
	ds_read_b64_tr_b16 v[166:167], v179 offset:34848
	ds_read_b128 v[168:171], v175 offset:32768
	ds_read_b64_tr_b16 v[164:165], v178 offset:34848
	ds_read_b64_tr_b16 v[182:183], v178 offset:34880
	ds_read_b64_tr_b16 v[186:187], v178 offset:34912
	ds_read_b64_tr_b16 v[184:185], v179 offset:34880
	ds_read_b64_tr_b16 v[188:189], v179 offset:34912
	ds_read_b128 v[190:193], v175 offset:34816
	ds_read_b128 v[194:197], v175 offset:36864
	buffer_load_dwordx4 v176, s[16:19], s4 offen lds
	s_mov_b32 m0, s53
	v_mfma_f32_16x16x32_bf16 v[44:47], v[244:247], v[252:255], v[44:47]
	v_mfma_f32_16x16x32_bf16 v[40:43], v[248:251], v[252:255], v[40:43]
	v_mfma_f32_16x16x32_bf16 v[36:39], v[198:201], v[252:255], v[36:39]
	v_mfma_f32_16x16x32_bf16 v[32:35], v[202:205], v[252:255], v[32:35]
	s_waitcnt lgkmcnt(7)
	v_mfma_f32_16x16x32_bf16 v[156:159], v[160:163], v[168:171], v[156:159]
	buffer_load_dwordx4 v177, s[16:19], s4 offen lds
	s_add_i32 s5, s1, 0xfffa0000
	s_waitcnt lgkmcnt(6)
	v_mfma_f32_16x16x32_bf16 v[152:155], v[164:167], v[168:171], v[152:155]
	s_waitcnt lgkmcnt(3)
	v_mfma_f32_16x16x32_bf16 v[148:151], v[182:185], v[168:171], v[148:151]
	s_waitcnt lgkmcnt(2)
	v_mfma_f32_16x16x32_bf16 v[144:147], v[186:189], v[168:171], v[144:147]
	s_waitcnt lgkmcnt(1)
	v_mfma_f32_16x16x32_bf16 v[140:143], v[160:163], v[190:193], v[140:143]
	s_mov_b32 m0, s54
	s_nop 0
	buffer_load_dwordx4 v180, s[16:19], s4 offen lds
	ds_read_b128 v[168:171], v175 offset:38912
	s_waitcnt vmcnt(10)
	v_cvt_pk_bf16_f32 v15, v14, v15
	v_cvt_pk_bf16_f32 v14, v12, v13
	v_mfma_f32_16x16x32_bf16 v[136:139], v[164:167], v[190:193], v[136:139]
	ds_write_b64 v174, v[14:15]
	v_mfma_f32_16x16x32_bf16 v[132:135], v[182:185], v[190:193], v[132:135]
	s_mov_b32 m0, s55
	s_nop 0
	buffer_load_dwordx4 v181, s[16:19], s4 offen lds
	v_mfma_f32_16x16x32_bf16 v[128:131], v[186:189], v[190:193], v[128:131]
	s_waitcnt lgkmcnt(2)
	v_mfma_f32_16x16x32_bf16 v[124:127], v[160:163], v[194:197], v[124:127]
	ds_read_b128 v[190:193], v175 offset:40960
	v_mfma_f32_16x16x32_bf16 v[120:123], v[164:167], v[194:197], v[120:123]
	v_mfma_f32_16x16x32_bf16 v[116:119], v[182:185], v[194:197], v[116:119]
	v_mfma_f32_16x16x32_bf16 v[112:115], v[186:189], v[194:197], v[112:115]
	s_waitcnt lgkmcnt(2)
	v_mfma_f32_16x16x32_bf16 v[108:111], v[160:163], v[168:171], v[108:111]
	ds_read_b128 v[194:197], v175 offset:43008
	buffer_load_dwordx4 v[12:15], v173, s[8:11], s5 offen
	s_waitcnt vmcnt(11)
	v_cvt_pk_bf16_f32 v31, v30, v31
	v_cvt_pk_bf16_f32 v30, v28, v29
	v_mfma_f32_16x16x32_bf16 v[104:107], v[164:167], v[168:171], v[104:107]
	ds_write_b64 v174, v[30:31] offset:8704
	v_mfma_f32_16x16x32_bf16 v[100:103], v[182:185], v[168:171], v[100:103]
	v_mfma_f32_16x16x32_bf16 v[96:99], v[186:189], v[168:171], v[96:99]
	s_add_i32 s20, s1, 0xfffc0000
	s_waitcnt lgkmcnt(2)
; #define G_ENDTILE(VM) do { asm volatile("s_waitcnt vmcnt(" #VM ")" ::: "memory"); \
;         asm volatile("s_waitcnt lgkmcnt(0)" ::: "memory"); __builtin_amdgcn_s_barrier(); asm volatile("" ::: "memory"); } while (0)
;     ...
;         for (int t = 0; t < nt - 2; t += 2) {
;             G_TILE(G_A0, G_B0, true, G_B1, G_A1, t + 1, true, t + 2, (void)0);
;             G_ENDTILE(8);
;             G_TILE(G_A1, G_B1, true, G_B0, G_A0, t + 2, true, t + 3, (void)0);
;             G_ENDTILE(8);
;         }
	v_mfma_f32_16x16x32_bf16 v[92:95], v[160:163], v[190:193], v[92:95]
	ds_read_b128 v[168:171], v175 offset:45056
	v_mfma_f32_16x16x32_bf16 v[88:91], v[164:167], v[190:193], v[88:91]
	v_mfma_f32_16x16x32_bf16 v[84:87], v[182:185], v[190:193], v[84:87]
	v_mfma_f32_16x16x32_bf16 v[80:83], v[186:189], v[190:193], v[80:83]
	s_waitcnt lgkmcnt(2)
	v_mfma_f32_16x16x32_bf16 v[76:79], v[160:163], v[194:197], v[76:79]
	ds_read_b128 v[190:193], v175 offset:47104
	buffer_load_dwordx4 v[28:31], v173, s[8:11], s20 offen
	s_waitcnt vmcnt(11)
	v_cvt_pk_bf16_f32 v7, v6, v7
	v_cvt_pk_bf16_f32 v6, v4, v5
	v_mfma_f32_16x16x32_bf16 v[72:75], v[164:167], v[194:197], v[72:75]
	ds_write_b64 v174, v[6:7] offset:17408
	v_mfma_f32_16x16x32_bf16 v[68:71], v[182:185], v[194:197], v[68:71]
	v_mfma_f32_16x16x32_bf16 v[64:67], v[186:189], v[194:197], v[64:67]
	s_add_i32 s21, s1, 0xfffe0000
	s_waitcnt lgkmcnt(2)
	v_mfma_f32_16x16x32_bf16 v[60:63], v[160:163], v[168:171], v[60:63]
	ds_read_b128 v[194:197], v175 offset:33792
	v_mfma_f32_16x16x32_bf16 v[56:59], v[164:167], v[168:171], v[56:59]
	v_mfma_f32_16x16x32_bf16 v[52:55], v[182:185], v[168:171], v[52:55]
	v_mfma_f32_16x16x32_bf16 v[48:51], v[186:189], v[168:171], v[48:51]
	s_waitcnt lgkmcnt(2)
	v_mfma_f32_16x16x32_bf16 v[44:47], v[160:163], v[190:193], v[44:47]
	ds_read_b128 v[160:163], v175 offset:35840
	buffer_load_dwordx4 v[4:7], v173, s[8:11], s21 offen
	s_waitcnt vmcnt(11)
	v_cvt_pk_bf16_f32 v27, v26, v27
	v_cvt_pk_bf16_f32 v26, v24, v25
	v_mfma_f32_16x16x32_bf16 v[40:43], v[164:167], v[190:193], v[40:43]
	ds_read_b64_tr_b16 v[244:245], v178 offset:52224
	ds_read_b64_tr_b16 v[248:249], v178 offset:52256
	ds_read_b64_tr_b16 v[198:199], v178 offset:52288
	ds_read_b64_tr_b16 v[202:203], v178 offset:52320
	ds_read_b64_tr_b16 v[246:247], v179 offset:52224
	ds_read_b64_tr_b16 v[250:251], v179 offset:52256
	ds_read_b64_tr_b16 v[200:201], v179 offset:52288
	ds_read_b64_tr_b16 v[204:205], v179 offset:52320
	ds_write_b64 v174, v[26:27] offset:26112
	v_mfma_f32_16x16x32_bf16 v[36:39], v[182:185], v[190:193], v[36:39]
	v_mfma_f32_16x16x32_bf16 v[32:35], v[186:189], v[190:193], v[32:35]
	s_waitcnt lgkmcnt(4)
	v_mfma_f32_16x16x32_bf16 v[156:159], v[244:247], v[194:197], v[156:159]
	ds_read_b128 v[182:185], v175 offset:37888
	s_waitcnt lgkmcnt(4)
	v_mfma_f32_16x16x32_bf16 v[152:155], v[248:251], v[194:197], v[152:155]
	s_waitcnt lgkmcnt(3)
	v_mfma_f32_16x16x32_bf16 v[148:151], v[198:201], v[194:197], v[148:151]
	s_waitcnt lgkmcnt(2)
	v_mfma_f32_16x16x32_bf16 v[144:147], v[202:205], v[194:197], v[144:147]
	v_mfma_f32_16x16x32_bf16 v[140:143], v[244:247], v[160:163], v[140:143]
	ds_read_b128 v[186:189], v175 offset:39936
	buffer_load_dwordx4 v[24:27], v173, s[8:11], s1 offen
	s_waitcnt vmcnt(11)
	v_cvt_pk_bf16_f32 v23, v22, v23
	v_cvt_pk_bf16_f32 v22, v20, v21
	v_mfma_f32_16x16x32_bf16 v[136:139], v[248:251], v[160:163], v[136:139]
	ds_write_b64 v174, v[22:23] offset:256
	v_mfma_f32_16x16x32_bf16 v[132:135], v[198:201], v[160:163], v[132:135]
	v_mfma_f32_16x16x32_bf16 v[128:131], v[202:205], v[160:163], v[128:131]
	s_waitcnt lgkmcnt(2)
	v_mfma_f32_16x16x32_bf16 v[124:127], v[244:247], v[182:185], v[124:127]
	ds_read_b128 v[160:163], v175 offset:41984
	v_mfma_f32_16x16x32_bf16 v[120:123], v[248:251], v[182:185], v[120:123]
	v_mfma_f32_16x16x32_bf16 v[116:119], v[198:201], v[182:185], v[116:119]
	v_mfma_f32_16x16x32_bf16 v[112:115], v[202:205], v[182:185], v[112:115]
	s_waitcnt lgkmcnt(2)
	v_mfma_f32_16x16x32_bf16 v[108:111], v[244:247], v[186:189], v[108:111]
	ds_read_b128 v[182:185], v175 offset:44032
	buffer_load_dwordx4 v[20:23], v173, s[12:15], s5 offen
	s_waitcnt vmcnt(11)
	v_cvt_pk_bf16_f32 v11, v10, v11
	v_cvt_pk_bf16_f32 v10, v8, v9
	v_mfma_f32_16x16x32_bf16 v[104:107], v[248:251], v[186:189], v[104:107]
	ds_write_b64 v174, v[10:11] offset:8960
	v_mfma_f32_16x16x32_bf16 v[100:103], v[198:201], v[186:189], v[100:103]
	v_mfma_f32_16x16x32_bf16 v[96:99], v[202:205], v[186:189], v[96:99]
	s_waitcnt lgkmcnt(2)
	v_mfma_f32_16x16x32_bf16 v[92:95], v[244:247], v[160:163], v[92:95]
	ds_read_b128 v[186:189], v175 offset:46080
	v_mfma_f32_16x16x32_bf16 v[88:91], v[248:251], v[160:163], v[88:91]
	v_mfma_f32_16x16x32_bf16 v[84:87], v[198:201], v[160:163], v[84:87]
	v_mfma_f32_16x16x32_bf16 v[80:83], v[202:205], v[160:163], v[80:83]
	s_waitcnt lgkmcnt(2)
	v_mfma_f32_16x16x32_bf16 v[76:79], v[244:247], v[182:185], v[76:79]
	ds_read_b128 v[252:255], v175 offset:48128
	buffer_load_dwordx4 v[8:11], v173, s[12:15], s20 offen
	s_waitcnt vmcnt(11)
	v_cvt_pk_bf16_f32 v3, v2, v3
	v_cvt_pk_bf16_f32 v2, v0, v1
	v_mfma_f32_16x16x32_bf16 v[72:75], v[248:251], v[182:185], v[72:75]
	ds_write_b64 v174, v[2:3] offset:17664
	v_mfma_f32_16x16x32_bf16 v[68:71], v[198:201], v[182:185], v[68:71]
	v_mfma_f32_16x16x32_bf16 v[64:67], v[202:205], v[182:185], v[64:67]
	s_waitcnt lgkmcnt(2)
	v_mfma_f32_16x16x32_bf16 v[60:63], v[244:247], v[186:189], v[60:63]
	buffer_load_dwordx4 v[0:3], v173, s[12:15], s21 offen
	s_waitcnt vmcnt(11)
	v_cvt_pk_bf16_f32 v19, v18, v19
	v_cvt_pk_bf16_f32 v18, v16, v17
	v_mfma_f32_16x16x32_bf16 v[56:59], v[248:251], v[186:189], v[56:59]
	ds_write_b64 v174, v[18:19] offset:26368
	v_mfma_f32_16x16x32_bf16 v[52:55], v[198:201], v[186:189], v[52:55]
	buffer_load_dwordx4 v[16:19], v173, s[12:15], s1 offen
	v_mfma_f32_16x16x32_bf16 v[48:51], v[202:205], v[186:189], v[48:51]
	s_add_i32 s0, s0, 2
	s_add_i32 s1, s1, 0x100000
	s_addk_i32 s4, 0x100
	s_cmp_ge_i32 s0, s60
	s_waitcnt vmcnt(8)
	s_waitcnt lgkmcnt(0)
	s_barrier
	s_cbranch_scc0 .LBB0_1038
